# stack on best: RoPE-table load pipelining in in-proj epilogue, counted lgkmcnt in pair follow loop, scalar fma instead of packed at step ends, g_final kept in registers in final phase, v_min clamp in
# speedup vs baseline: 1.0203x; 1.0014x over previous
;     template <int MODE>
;     __device__ __forceinline__ void store_tile(const f32x4 (&acc)[2][2][4][2], bf16_t* dst, int ld, int colbase, size_t rowbase, int nvalid, int pos0, size_t dupoff, int wr, int wc, int fr, int fq) const {
;     ...
;                         const int pos = pos0 + tr;
;                         const int i0 = MODE == 2 ? (wc & 1) * 32 + 8 * fq : 8 * fq;
;                         const int col = MODE == 2 ? (wc >> 1) * 128 + i0 : wc * 64 + i0;
;                         const int hw = MODE == 2 ? 64 : 32;
;     __device__ __forceinline__ void operator()(const f32x4 (&acc)[2][2][4][2], const Unit& u, int wr, int wc, int fr, int fq) const {
;     ...
;         const int sec = pn < 28 ? (pn >> 2) : (pn < 36 ? 7 : (pn < 44 ? 8 : 9));
;         const int mode = (sec == 2 || sec == 6) ? 0 : ((sec == 7 || sec == 8) ? 1 : ((sec == 3 || sec == 9) ? 3 : 2));
;         const int kt = (sec == 1 || sec == 2 || sec == 5 || sec == 6 || sec == 9) ? 1 : 0;
;         const int ld = (sec == 7 || sec == 8) ? 2048 : (sec == 9 ? 64 : 1024);
;         const int colbase = sec < 7 ? (pn & 3) * 256 : (sec == 7 ? (pn - 28) * 256 : (sec == 8 ? (pn - 36) * 256 : 0));
;         const size_t off = sec == 0 ? WS_QA : sec == 1 ? WS_KA : sec == 2 ? WS_VA : sec == 3 ? WS_QI : sec == 4 ? WS_QB : sec == 5 ? WS_KB : sec == 6 ? WS_VB : sec == 7 ? WS_GA : sec == 8 ? WS_GB : WS_KI;
;         if (sec == 9 && pm < 64 && wc == 2 && fq < 2) {
;             float* WI = (float*)(ws + WS_WI);
; #pragma unroll
;             for (int ai = 0; ai < 2; ++ai)
; #pragma unroll
;                 for (int m = 0; m < 4; ++m) { const int r = pm * 256 + ai * HALF + wr * 64 + m * 16 + fr;
;                     *(f32x4*)(WI + (size_t)r * 16 + 8 * fq) = acc[ai][0][m][0] * (1.0f / 32.0f); *(f32x4*)(WI + (size_t)r * 16 + 8 * fq + 4) = acc[ai][0][m][1] * (1.0f / 32.0f); }
;         }
;         const bool meta = pm >= 64;
;         const bool active = (sec != 9 || wc == 0) && (kt != 0 || !meta);
;         bf16_t* dst = (bf16_t*)(ws + off);
;         const int pos0 = meta ? 0 : NMETA + (pm & 31) * 256;
;         const int nvalid = active ? (meta ? NMETA : 256) : 0;
;         const size_t rowbase = meta ? (size_t)0 : (kt ? (size_t)(pm >> 5) * TP + pos0 : (size_t)pm * 256);
;         const size_t dupoff = meta ? (size_t)TP * ld : (size_t)0;
.LBB0_374:
	s_cmp_lg_u32 s64, 9
	s_cselect_b64 s[34:35], -1, 0
	s_or_b64 s[34:35], s[16:17], s[34:35]
	s_or_b64 s[40:41], s[40:41], s[4:5]
	s_and_b64 s[34:35], s[34:35], s[40:41]
	s_add_u32 s40, s70, s36
	s_addc_u32 s41, s71, s37
	s_and_b64 s[36:37], s[4:5], exec
	s_cselect_b32 s3, 0x100, 16
	s_and_b64 s[34:35], s[34:35], exec
	s_cselect_b32 s21, s3, 0
	s_add_i32 s3, s64, -7
	s_cmp_lt_u32 s3, 2
	s_cselect_b64 s[34:35], -1, 0
	s_and_b64 s[36:37], s[28:29], exec
	s_mov_b32 s3, 0x81000
	s_cselect_b32 s3, s3, 0x810000
	s_and_b64 s[36:37], s[34:35], exec
	s_cselect_b32 s42, 0x1020000, s3
	s_ashr_i32 s3, s2, 31
	s_lshl_b64 s[2:3], s[2:3], 1
	s_add_u32 s36, s40, s2
	s_addc_u32 s37, s41, s3
	v_cmp_gt_u32_e64 s[2:3], s21, v150
	s_cmp_lt_i32 s23, 2
	s_mov_b64 s[40:41], -1
	s_cbranch_scc1 .LBB0_428
	s_and_b64 s[40:41], s[4:5], exec
	s_cselect_b32 s43, s6, 0
	s_cmp_gt_i32 s23, 2
	s_mov_b64 s[40:41], -1
	s_cbranch_scc0 .LBB0_401
	v_add_u32_e32 v148, s43, v150
	v_lshlrev_b64 v[128:129], 8, v[148:149]
	v_lshl_add_u64 v[192:193], v[158:159], 0, v[128:129]
	global_load_dwordx4 v[128:131], v[192:193], off offset:48
	global_load_dwordx4 v[132:135], v[192:193], off offset:32
	global_load_dwordx4 v[188:191], v[192:193], off offset:16
	s_nop 0
	global_load_dwordx4 v[192:195], v[192:193], off
	v_add_u32_e32 v148, s43, v160
	v_lshlrev_b64 v[200:201], 8, v[148:149]
	v_lshl_add_u64 v[222:223], v[158:159], 0, v[200:201]
	global_load_dwordx4 v[200:203], v[222:223], off offset:48
	global_load_dwordx4 v[204:207], v[222:223], off offset:32
	global_load_dwordx4 v[218:221], v[222:223], off offset:16
	s_nop 0
	global_load_dwordx4 v[222:225], v[222:223], off
	s_nop 1
	v_add_u32_e32 v148, s43, v162
	v_lshlrev_b64 v[230:231], 8, v[148:149]
	v_lshl_add_u64 v[242:243], v[158:159], 0, v[230:231]
	global_load_dwordx4 v[230:233], v[242:243], off offset:48
	global_load_dwordx4 v[234:237], v[242:243], off offset:32
	global_load_dwordx4 v[238:241], v[242:243], off offset:16
	s_nop 0
	global_load_dwordx4 v[242:245], v[242:243], off
	s_and_saveexec_b64 s[40:41], s[2:3]
	s_and_b64 s[64:65], s[28:29], exec
	s_cselect_b32 s6, 6, 10
	s_and_b64 s[64:65], s[34:35], exec
	v_lshl_add_u64 v[196:197], s[30:31], 0, v[150:151]
	s_cselect_b32 s6, 11, s6
	v_lshlrev_b64 v[196:197], s6, v[196:197]
	v_lshl_add_u64 v[184:185], v[196:197], 1, s[36:37]
	s_andn2_b64 vcc, exec, s[38:39]
	s_waitcnt vmcnt(8)
	v_mov_b32_e32 v197, v194
	v_mov_b32_e32 v194, v193
	v_mov_b32_e32 v196, v192
	v_pk_mul_f32 v[192:193], v[116:117], v[194:195]
	s_nop 0
	v_pk_fma_f32 v[192:193], v[124:125], v[196:197], v[192:193] neg_lo:[0,0,1] neg_hi:[0,0,1]
	v_pk_mul_f32 v[196:197], v[116:117], v[196:197]
	s_nop 0
	v_pk_fma_f32 v[194:195], v[124:125], v[194:195], v[196:197]
	v_mov_b32_e32 v197, v190
	v_mov_b32_e32 v190, v189
	v_mov_b32_e32 v196, v188
	v_pk_mul_f32 v[188:189], v[118:119], v[190:191]
	s_nop 0
	v_pk_fma_f32 v[188:189], v[126:127], v[196:197], v[188:189] neg_lo:[0,0,1] neg_hi:[0,0,1]
	v_pk_mul_f32 v[196:197], v[118:119], v[196:197]
	s_nop 0
	v_pk_fma_f32 v[190:191], v[126:127], v[190:191], v[196:197]
	v_mov_b32_e32 v197, v134
	v_mov_b32_e32 v134, v133
	v_mov_b32_e32 v196, v132
	v_pk_mul_f32 v[132:133], v[112:113], v[134:135]
	s_nop 0
	v_pk_fma_f32 v[132:133], v[120:121], v[196:197], v[132:133] neg_lo:[0,0,1] neg_hi:[0,0,1]
	v_pk_mul_f32 v[196:197], v[112:113], v[196:197]
	s_nop 0
	v_pk_fma_f32 v[134:135], v[120:121], v[134:135], v[196:197]
	v_mov_b32_e32 v197, v130
	v_mov_b32_e32 v130, v129
	v_mov_b32_e32 v196, v128
	v_pk_mul_f32 v[128:129], v[114:115], v[130:131]
	v_cvt_pk_bf16_f32 v134, v134, v135
	v_pk_fma_f32 v[198:199], v[122:123], v[196:197], v[128:129] neg_lo:[0,0,1] neg_hi:[0,0,1]
	v_pk_mul_f32 v[128:129], v[114:115], v[196:197]
	s_nop 0
	v_pk_fma_f32 v[196:197], v[122:123], v[130:131], v[128:129]
	v_cvt_pk_bf16_f32 v128, v192, v193
	v_cvt_pk_bf16_f32 v129, v188, v189
	v_cvt_pk_bf16_f32 v130, v132, v133
	v_cvt_pk_bf16_f32 v131, v198, v199
	v_cvt_pk_bf16_f32 v132, v194, v195
	v_cvt_pk_bf16_f32 v133, v190, v191
	v_cvt_pk_bf16_f32 v135, v196, v197
	v_lshl_add_u64 v[188:189], v[156:157], 1, v[184:185]
	global_store_dwordx4 v[188:189], v[128:131], off
	global_store_dwordx4 v[188:189], v[132:135], off offset:64
	s_cbranch_vccnz .LBB0_379
	s_lshl_b32 s6, s42, 1
	v_lshl_add_u64 v[184:185], v[184:185], 0, s[6:7]
	v_lshl_add_u64 v[184:185], v[156:157], 1, v[184:185]
	global_store_dwordx4 v[184:185], v[128:131], off
	global_store_dwordx4 v[184:185], v[132:135], off offset:64
;     template <int MODE>
;     __device__ __forceinline__ void store_tile(const f32x4 (&acc)[2][2][4][2], bf16_t* dst, int ld, int colbase, size_t rowbase, int nvalid, int pos0, size_t dupoff, int wr, int wc, int fr, int fq) const {
;     ...
;         for (int ai = 0; ai < 2; ++ai)
; #pragma unroll
;             for (int m = 0; m < 4; ++m) {
;                 const int tr = ai * HALF + wr * 64 + m * 16 + fr;
;                 if (tr < nvalid) {
;                     bf16_t* rowp = dst + (rowbase + tr) * (size_t)ld + colbase;
;                     if (MODE == 0 || MODE == 1) {
; #pragma unroll
;                         for (int bj = 0; bj < 2; ++bj) { f32x4 v0 = acc[ai][bj][m][0] * sc, v1 = acc[ai][bj][m][1] * sc;
;                             if (MODE == 1) {
; #pragma unroll
;                                 for (int j = 0; j < 4; ++j) { v0[j] = __builtin_amdgcn_rcpf(1.f + __builtin_amdgcn_exp2f(-1.4426950408889634f * v0[j])); v1[j] = __builtin_amdgcn_rcpf(1.f + __builtin_amdgcn_exp2f(-1.4426950408889634f * v1[j])); } }
;                             u32x4 w; w.x = cvt_pk_bf16(v0[0], v0[1]); w.y = cvt_pk_bf16(v0[2], v0[3]); w.z = cvt_pk_bf16(v1[0], v1[1]); w.w = cvt_pk_bf16(v1[2], v1[3]);
;                             *(u32x4*)(rowp + bj * HALF + wc * 32 + 8 * fq) = w; if (dupoff) *(u32x4*)(rowp + dupoff + bj * HALF + wc * 32 + 8 * fq) = w; }
;                     } else {
;                         const int pos = pos0 + tr;
;                         const int i0 = MODE == 2 ? (wc & 1) * 32 + 8 * fq : 8 * fq;
;                         const int col = MODE == 2 ? (wc >> 1) * 128 + i0 : wc * 64 + i0;
;                         const int hw = MODE == 2 ? 64 : 32;
;                         const f32x4* tp = (const f32x4*)((MODE == 2 ? rope + (size_t)pos * 64 : ropei + (size_t)pos * 32) + i0);
;                         const f32x4 t0 = tp[0], t1 = tp[1], t2 = tp[2], t3 = tp[3];
;                         const f32x4 a0 = acc[ai][0][m][0], a1 = acc[ai][0][m][1], b0 = acc[ai][1][m][0], b1 = acc[ai][1][m][1];
;                         float y1[8], y2[8];
;                         y1[0] = a0[0] * t0[0] - b0[0] * t0[1]; y2[0] = b0[0] * t0[0] + a0[0] * t0[1];
;                         y1[1] = a0[1] * t0[2] - b0[1] * t0[3]; y2[1] = b0[1] * t0[2] + a0[1] * t0[3];
;                         y1[2] = a0[2] * t1[0] - b0[2] * t1[1]; y2[2] = b0[2] * t1[0] + a0[2] * t1[1];
.LBB0_379:
	s_or_b64 exec, exec, s[40:41]
	s_nop 1
	v_add_u32_e32 v148, s43, v164
	v_lshlrev_b64 v[128:129], 8, v[148:149]
	v_lshl_add_u64 v[192:193], v[158:159], 0, v[128:129]
	global_load_dwordx4 v[128:131], v[192:193], off offset:48
	global_load_dwordx4 v[132:135], v[192:193], off offset:32
	global_load_dwordx4 v[188:191], v[192:193], off offset:16
	s_nop 0
	global_load_dwordx4 v[192:195], v[192:193], off
	v_cmp_gt_u32_e32 vcc, s21, v160
	s_and_saveexec_b64 s[40:41], vcc
	s_and_b64 s[64:65], s[28:29], exec
	s_cselect_b32 s6, 6, 10
	s_and_b64 s[64:65], s[34:35], exec
	v_lshl_add_u64 v[226:227], s[30:31], 0, v[160:161]
	s_cselect_b32 s6, 11, s6
	v_lshlrev_b64 v[226:227], s6, v[226:227]
	v_lshl_add_u64 v[208:209], v[226:227], 1, s[36:37]
	s_andn2_b64 vcc, exec, s[38:39]
	s_waitcnt vmcnt(10)
	v_mov_b32_e32 v227, v224
	v_mov_b32_e32 v224, v223
	v_mov_b32_e32 v226, v222
	v_pk_mul_f32 v[222:223], v[100:101], v[224:225]
	s_nop 0
	v_pk_fma_f32 v[222:223], v[108:109], v[226:227], v[222:223] neg_lo:[0,0,1] neg_hi:[0,0,1]
	v_pk_mul_f32 v[226:227], v[100:101], v[226:227]
	s_nop 0
	v_pk_fma_f32 v[224:225], v[108:109], v[224:225], v[226:227]
	v_mov_b32_e32 v227, v220
	v_mov_b32_e32 v220, v219
	v_mov_b32_e32 v226, v218
	v_pk_mul_f32 v[218:219], v[102:103], v[220:221]
	s_nop 0
	v_pk_fma_f32 v[218:219], v[110:111], v[226:227], v[218:219] neg_lo:[0,0,1] neg_hi:[0,0,1]
	v_pk_mul_f32 v[226:227], v[102:103], v[226:227]
	s_nop 0
	v_pk_fma_f32 v[220:221], v[110:111], v[220:221], v[226:227]
	v_mov_b32_e32 v227, v206
	v_mov_b32_e32 v206, v205
	v_mov_b32_e32 v226, v204
	v_pk_mul_f32 v[204:205], v[96:97], v[206:207]
	s_nop 0
	v_pk_fma_f32 v[204:205], v[104:105], v[226:227], v[204:205] neg_lo:[0,0,1] neg_hi:[0,0,1]
	v_pk_mul_f32 v[226:227], v[96:97], v[226:227]
	s_nop 0
	v_pk_fma_f32 v[206:207], v[104:105], v[206:207], v[226:227]
	v_mov_b32_e32 v227, v202
	v_mov_b32_e32 v202, v201
	v_mov_b32_e32 v226, v200
	v_pk_mul_f32 v[200:201], v[98:99], v[202:203]
	v_cvt_pk_bf16_f32 v206, v206, v207
	v_pk_fma_f32 v[228:229], v[106:107], v[226:227], v[200:201] neg_lo:[0,0,1] neg_hi:[0,0,1]
	v_pk_mul_f32 v[200:201], v[98:99], v[226:227]
	s_nop 0
	v_pk_fma_f32 v[226:227], v[106:107], v[202:203], v[200:201]
	v_cvt_pk_bf16_f32 v200, v222, v223
	v_cvt_pk_bf16_f32 v201, v218, v219
	v_cvt_pk_bf16_f32 v202, v204, v205
	v_cvt_pk_bf16_f32 v203, v228, v229
	v_cvt_pk_bf16_f32 v204, v224, v225
	v_cvt_pk_bf16_f32 v205, v220, v221
	v_cvt_pk_bf16_f32 v207, v226, v227
	v_lshl_add_u64 v[218:219], v[156:157], 1, v[208:209]
	global_store_dwordx4 v[218:219], v[200:203], off
	global_store_dwordx4 v[218:219], v[204:207], off offset:64
	s_cbranch_vccnz .LBB0_382
	s_lshl_b32 s6, s42, 1
	v_lshl_add_u64 v[208:209], v[208:209], 0, s[6:7]
	v_lshl_add_u64 v[208:209], v[156:157], 1, v[208:209]
	global_store_dwordx4 v[208:209], v[200:203], off
	global_store_dwordx4 v[208:209], v[204:207], off offset:64
.LBB0_382:
	s_or_b64 exec, exec, s[40:41]
	s_nop 1
	v_add_u32_e32 v148, s43, v166
	v_lshlrev_b64 v[200:201], 8, v[148:149]
	v_lshl_add_u64 v[222:223], v[158:159], 0, v[200:201]
	global_load_dwordx4 v[200:203], v[222:223], off offset:48
	global_load_dwordx4 v[204:207], v[222:223], off offset:32
	global_load_dwordx4 v[218:221], v[222:223], off offset:16
	s_nop 0
	global_load_dwordx4 v[222:225], v[222:223], off
	v_cmp_gt_u32_e32 vcc, s21, v162
	s_and_saveexec_b64 s[40:41], vcc
	s_and_b64 s[64:65], s[28:29], exec
	s_cselect_b32 s6, 6, 10
	s_and_b64 s[64:65], s[34:35], exec
	v_lshl_add_u64 v[246:247], s[30:31], 0, v[162:163]
	s_cselect_b32 s6, 11, s6
	v_lshlrev_b64 v[246:247], s6, v[246:247]
	v_lshl_add_u64 v[210:211], v[246:247], 1, s[36:37]
	s_andn2_b64 vcc, exec, s[38:39]
	s_waitcnt vmcnt(12)
	v_mov_b32_e32 v247, v244
	v_mov_b32_e32 v244, v243
	v_mov_b32_e32 v246, v242
	v_pk_mul_f32 v[242:243], v[84:85], v[244:245]
	s_nop 0
	v_pk_fma_f32 v[242:243], v[92:93], v[246:247], v[242:243] neg_lo:[0,0,1] neg_hi:[0,0,1]
	v_pk_mul_f32 v[246:247], v[84:85], v[246:247]
	s_nop 0
	v_pk_fma_f32 v[244:245], v[92:93], v[244:245], v[246:247]
	v_mov_b32_e32 v247, v240
	v_mov_b32_e32 v240, v239
	v_mov_b32_e32 v246, v238
	v_pk_mul_f32 v[238:239], v[86:87], v[240:241]
	s_nop 0
	v_pk_fma_f32 v[238:239], v[94:95], v[246:247], v[238:239] neg_lo:[0,0,1] neg_hi:[0,0,1]
	v_pk_mul_f32 v[246:247], v[86:87], v[246:247]
	s_nop 0
	v_pk_fma_f32 v[240:241], v[94:95], v[240:241], v[246:247]
	v_mov_b32_e32 v247, v236
	v_mov_b32_e32 v236, v235
	v_mov_b32_e32 v246, v234
	v_pk_mul_f32 v[234:235], v[80:81], v[236:237]
	s_nop 0
	v_pk_fma_f32 v[234:235], v[88:89], v[246:247], v[234:235] neg_lo:[0,0,1] neg_hi:[0,0,1]
	v_pk_mul_f32 v[246:247], v[80:81], v[246:247]
	s_nop 0
	v_pk_fma_f32 v[236:237], v[88:89], v[236:237], v[246:247]
	v_mov_b32_e32 v247, v232
	v_mov_b32_e32 v232, v231
	v_mov_b32_e32 v246, v230
	v_pk_mul_f32 v[230:231], v[82:83], v[232:233]
	v_cvt_pk_bf16_f32 v236, v236, v237
	v_pk_fma_f32 v[248:249], v[90:91], v[246:247], v[230:231] neg_lo:[0,0,1] neg_hi:[0,0,1]
	v_pk_mul_f32 v[230:231], v[82:83], v[246:247]
	s_nop 0
	v_pk_fma_f32 v[246:247], v[90:91], v[232:233], v[230:231]
	v_cvt_pk_bf16_f32 v230, v242, v243
	v_cvt_pk_bf16_f32 v231, v238, v239
	v_cvt_pk_bf16_f32 v232, v234, v235
	v_cvt_pk_bf16_f32 v233, v248, v249
	v_cvt_pk_bf16_f32 v234, v244, v245
	v_cvt_pk_bf16_f32 v235, v240, v241
	v_cvt_pk_bf16_f32 v237, v246, v247
	v_lshl_add_u64 v[238:239], v[156:157], 1, v[210:211]
	global_store_dwordx4 v[238:239], v[230:233], off
	global_store_dwordx4 v[238:239], v[234:237], off offset:64
	s_cbranch_vccnz .LBB0_385
	s_lshl_b32 s6, s42, 1
	v_lshl_add_u64 v[210:211], v[210:211], 0, s[6:7]
	v_lshl_add_u64 v[210:211], v[156:157], 1, v[210:211]
	global_store_dwordx4 v[210:211], v[230:233], off
	global_store_dwordx4 v[210:211], v[234:237], off offset:64
;     template <int MODE>
;     __device__ __forceinline__ void store_tile(const f32x4 (&acc)[2][2][4][2], bf16_t* dst, int ld, int colbase, size_t rowbase, int nvalid, int pos0, size_t dupoff, int wr, int wc, int fr, int fq) const {
;     ...
;         for (int ai = 0; ai < 2; ++ai)
; #pragma unroll
;             for (int m = 0; m < 4; ++m) {
;                 const int tr = ai * HALF + wr * 64 + m * 16 + fr;
;                 if (tr < nvalid) {
;                     bf16_t* rowp = dst + (rowbase + tr) * (size_t)ld + colbase;
;                     if (MODE == 0 || MODE == 1) {
; #pragma unroll
;                         for (int bj = 0; bj < 2; ++bj) { f32x4 v0 = acc[ai][bj][m][0] * sc, v1 = acc[ai][bj][m][1] * sc;
;                             if (MODE == 1) {
; #pragma unroll
;                                 for (int j = 0; j < 4; ++j) { v0[j] = __builtin_amdgcn_rcpf(1.f + __builtin_amdgcn_exp2f(-1.4426950408889634f * v0[j])); v1[j] = __builtin_amdgcn_rcpf(1.f + __builtin_amdgcn_exp2f(-1.4426950408889634f * v1[j])); } }
;                             u32x4 w; w.x = cvt_pk_bf16(v0[0], v0[1]); w.y = cvt_pk_bf16(v0[2], v0[3]); w.z = cvt_pk_bf16(v1[0], v1[1]); w.w = cvt_pk_bf16(v1[2], v1[3]);
;                             *(u32x4*)(rowp + bj * HALF + wc * 32 + 8 * fq) = w; if (dupoff) *(u32x4*)(rowp + dupoff + bj * HALF + wc * 32 + 8 * fq) = w; }
;                     } else {
;                         const int pos = pos0 + tr;
;                         const int i0 = MODE == 2 ? (wc & 1) * 32 + 8 * fq : 8 * fq;
;                         const int col = MODE == 2 ? (wc >> 1) * 128 + i0 : wc * 64 + i0;
;                         const int hw = MODE == 2 ? 64 : 32;
;                         const f32x4* tp = (const f32x4*)((MODE == 2 ? rope + (size_t)pos * 64 : ropei + (size_t)pos * 32) + i0);
;                         const f32x4 t0 = tp[0], t1 = tp[1], t2 = tp[2], t3 = tp[3];
;                         const f32x4 a0 = acc[ai][0][m][0], a1 = acc[ai][0][m][1], b0 = acc[ai][1][m][0], b1 = acc[ai][1][m][1];
;                         float y1[8], y2[8];
;                         y1[0] = a0[0] * t0[0] - b0[0] * t0[1]; y2[0] = b0[0] * t0[0] + a0[0] * t0[1];
;                         y1[1] = a0[1] * t0[2] - b0[1] * t0[3]; y2[1] = b0[1] * t0[2] + a0[1] * t0[3];
;                         y1[2] = a0[2] * t1[0] - b0[2] * t1[1]; y2[2] = b0[2] * t1[0] + a0[2] * t1[1];
.LBB0_385:
	s_or_b64 exec, exec, s[40:41]
	s_nop 1
	v_add_u32_e32 v148, s43, v168
	v_lshlrev_b64 v[230:231], 8, v[148:149]
	v_lshl_add_u64 v[242:243], v[158:159], 0, v[230:231]
	global_load_dwordx4 v[230:233], v[242:243], off offset:48
	global_load_dwordx4 v[234:237], v[242:243], off offset:32
	global_load_dwordx4 v[238:241], v[242:243], off offset:16
	s_nop 0
	global_load_dwordx4 v[242:245], v[242:243], off
	v_cmp_gt_u32_e32 vcc, s21, v164
	s_and_saveexec_b64 s[40:41], vcc
	s_and_b64 s[64:65], s[28:29], exec
	s_cselect_b32 s6, 6, 10
	s_and_b64 s[64:65], s[34:35], exec
	v_lshl_add_u64 v[196:197], s[30:31], 0, v[164:165]
	s_cselect_b32 s6, 11, s6
	v_lshlrev_b64 v[196:197], s6, v[196:197]
	v_lshl_add_u64 v[184:185], v[196:197], 1, s[36:37]
	s_andn2_b64 vcc, exec, s[38:39]
	s_waitcnt vmcnt(12)
	v_mov_b32_e32 v197, v194
	v_mov_b32_e32 v194, v193
	v_mov_b32_e32 v196, v192
	v_pk_mul_f32 v[192:193], v[68:69], v[194:195]
	s_nop 0
	v_pk_fma_f32 v[192:193], v[76:77], v[196:197], v[192:193] neg_lo:[0,0,1] neg_hi:[0,0,1]
	v_pk_mul_f32 v[196:197], v[68:69], v[196:197]
	s_nop 0
	v_pk_fma_f32 v[194:195], v[76:77], v[194:195], v[196:197]
	v_mov_b32_e32 v197, v190
	v_mov_b32_e32 v190, v189
	v_mov_b32_e32 v196, v188
	v_pk_mul_f32 v[188:189], v[70:71], v[190:191]
	s_nop 0
	v_pk_fma_f32 v[188:189], v[78:79], v[196:197], v[188:189] neg_lo:[0,0,1] neg_hi:[0,0,1]
	v_pk_mul_f32 v[196:197], v[70:71], v[196:197]
	s_nop 0
	v_pk_fma_f32 v[190:191], v[78:79], v[190:191], v[196:197]
	v_mov_b32_e32 v197, v134
	v_mov_b32_e32 v134, v133
	v_mov_b32_e32 v196, v132
	v_pk_mul_f32 v[132:133], v[64:65], v[134:135]
	s_nop 0
	v_pk_fma_f32 v[132:133], v[72:73], v[196:197], v[132:133] neg_lo:[0,0,1] neg_hi:[0,0,1]
	v_pk_mul_f32 v[196:197], v[64:65], v[196:197]
	s_nop 0
	v_pk_fma_f32 v[134:135], v[72:73], v[134:135], v[196:197]
	v_mov_b32_e32 v197, v130
	v_mov_b32_e32 v130, v129
	v_mov_b32_e32 v196, v128
	v_pk_mul_f32 v[128:129], v[66:67], v[130:131]
	v_cvt_pk_bf16_f32 v134, v134, v135
	v_pk_fma_f32 v[198:199], v[74:75], v[196:197], v[128:129] neg_lo:[0,0,1] neg_hi:[0,0,1]
	v_pk_mul_f32 v[128:129], v[66:67], v[196:197]
	s_nop 0
	v_pk_fma_f32 v[196:197], v[74:75], v[130:131], v[128:129]
	v_cvt_pk_bf16_f32 v128, v192, v193
	v_cvt_pk_bf16_f32 v129, v188, v189
	v_cvt_pk_bf16_f32 v130, v132, v133
	v_cvt_pk_bf16_f32 v131, v198, v199
	v_cvt_pk_bf16_f32 v132, v194, v195
	v_cvt_pk_bf16_f32 v133, v190, v191
	v_cvt_pk_bf16_f32 v135, v196, v197
	v_lshl_add_u64 v[188:189], v[156:157], 1, v[184:185]
	global_store_dwordx4 v[188:189], v[128:131], off
	global_store_dwordx4 v[188:189], v[132:135], off offset:64
	s_cbranch_vccnz .LBB0_388
	s_lshl_b32 s6, s42, 1
	v_lshl_add_u64 v[184:185], v[184:185], 0, s[6:7]
	v_lshl_add_u64 v[184:185], v[156:157], 1, v[184:185]
	global_store_dwordx4 v[184:185], v[128:131], off
	global_store_dwordx4 v[184:185], v[132:135], off offset:64
.LBB0_388:
	s_or_b64 exec, exec, s[40:41]
	s_nop 1
	v_add_u32_e32 v148, s43, v170
	v_lshlrev_b64 v[128:129], 8, v[148:149]
	v_lshl_add_u64 v[192:193], v[158:159], 0, v[128:129]
	global_load_dwordx4 v[128:131], v[192:193], off offset:48
	global_load_dwordx4 v[132:135], v[192:193], off offset:32
	global_load_dwordx4 v[188:191], v[192:193], off offset:16
	s_nop 0
	global_load_dwordx4 v[192:195], v[192:193], off
	v_cmp_gt_u32_e32 vcc, s21, v166
	s_and_saveexec_b64 s[40:41], vcc
	s_and_b64 s[64:65], s[28:29], exec
	s_cselect_b32 s6, 6, 10
	s_and_b64 s[64:65], s[34:35], exec
	v_lshl_add_u64 v[226:227], s[30:31], 0, v[166:167]
	s_cselect_b32 s6, 11, s6
	v_lshlrev_b64 v[226:227], s6, v[226:227]
	v_lshl_add_u64 v[208:209], v[226:227], 1, s[36:37]
	s_andn2_b64 vcc, exec, s[38:39]
	s_waitcnt vmcnt(12)
	v_mov_b32_e32 v227, v224
	v_mov_b32_e32 v224, v223
	v_mov_b32_e32 v226, v222
	v_pk_mul_f32 v[222:223], v[52:53], v[224:225]
	s_nop 0
	v_pk_fma_f32 v[222:223], v[60:61], v[226:227], v[222:223] neg_lo:[0,0,1] neg_hi:[0,0,1]
	v_pk_mul_f32 v[226:227], v[52:53], v[226:227]
	s_nop 0
	v_pk_fma_f32 v[224:225], v[60:61], v[224:225], v[226:227]
	v_mov_b32_e32 v227, v220
	v_mov_b32_e32 v220, v219
	v_mov_b32_e32 v226, v218
	v_pk_mul_f32 v[218:219], v[54:55], v[220:221]
	s_nop 0
	v_pk_fma_f32 v[218:219], v[62:63], v[226:227], v[218:219] neg_lo:[0,0,1] neg_hi:[0,0,1]
	v_pk_mul_f32 v[226:227], v[54:55], v[226:227]
	s_nop 0
	v_pk_fma_f32 v[220:221], v[62:63], v[220:221], v[226:227]
	v_mov_b32_e32 v227, v206
	v_mov_b32_e32 v206, v205
	v_mov_b32_e32 v226, v204
	v_pk_mul_f32 v[204:205], v[48:49], v[206:207]
	s_nop 0
	v_pk_fma_f32 v[204:205], v[56:57], v[226:227], v[204:205] neg_lo:[0,0,1] neg_hi:[0,0,1]
	v_pk_mul_f32 v[226:227], v[48:49], v[226:227]
	s_nop 0
	v_pk_fma_f32 v[206:207], v[56:57], v[206:207], v[226:227]
	v_mov_b32_e32 v227, v202
	v_mov_b32_e32 v202, v201
	v_mov_b32_e32 v226, v200
	v_pk_mul_f32 v[200:201], v[50:51], v[202:203]
	v_cvt_pk_bf16_f32 v206, v206, v207
	v_pk_fma_f32 v[228:229], v[58:59], v[226:227], v[200:201] neg_lo:[0,0,1] neg_hi:[0,0,1]
	v_pk_mul_f32 v[200:201], v[50:51], v[226:227]
	s_nop 0
	v_pk_fma_f32 v[226:227], v[58:59], v[202:203], v[200:201]
	v_cvt_pk_bf16_f32 v200, v222, v223
	v_cvt_pk_bf16_f32 v201, v218, v219
	v_cvt_pk_bf16_f32 v202, v204, v205
	v_cvt_pk_bf16_f32 v203, v228, v229
	v_cvt_pk_bf16_f32 v204, v224, v225
	v_cvt_pk_bf16_f32 v205, v220, v221
	v_cvt_pk_bf16_f32 v207, v226, v227
	v_lshl_add_u64 v[218:219], v[156:157], 1, v[208:209]
	global_store_dwordx4 v[218:219], v[200:203], off
	global_store_dwordx4 v[218:219], v[204:207], off offset:64
	s_cbranch_vccnz .LBB0_391
	s_lshl_b32 s6, s42, 1
	v_lshl_add_u64 v[208:209], v[208:209], 0, s[6:7]
	v_lshl_add_u64 v[208:209], v[156:157], 1, v[208:209]
	global_store_dwordx4 v[208:209], v[200:203], off
	global_store_dwordx4 v[208:209], v[204:207], off offset:64
;     template <int MODE>
;     __device__ __forceinline__ void store_tile(const f32x4 (&acc)[2][2][4][2], bf16_t* dst, int ld, int colbase, size_t rowbase, int nvalid, int pos0, size_t dupoff, int wr, int wc, int fr, int fq) const {
;     ...
;         for (int ai = 0; ai < 2; ++ai)
; #pragma unroll
;             for (int m = 0; m < 4; ++m) {
;                 const int tr = ai * HALF + wr * 64 + m * 16 + fr;
;                 if (tr < nvalid) {
;                     bf16_t* rowp = dst + (rowbase + tr) * (size_t)ld + colbase;
;                     if (MODE == 0 || MODE == 1) {
; #pragma unroll
;                         for (int bj = 0; bj < 2; ++bj) { f32x4 v0 = acc[ai][bj][m][0] * sc, v1 = acc[ai][bj][m][1] * sc;
;                             if (MODE == 1) {
; #pragma unroll
;                                 for (int j = 0; j < 4; ++j) { v0[j] = __builtin_amdgcn_rcpf(1.f + __builtin_amdgcn_exp2f(-1.4426950408889634f * v0[j])); v1[j] = __builtin_amdgcn_rcpf(1.f + __builtin_amdgcn_exp2f(-1.4426950408889634f * v1[j])); } }
;                             u32x4 w; w.x = cvt_pk_bf16(v0[0], v0[1]); w.y = cvt_pk_bf16(v0[2], v0[3]); w.z = cvt_pk_bf16(v1[0], v1[1]); w.w = cvt_pk_bf16(v1[2], v1[3]);
;                             *(u32x4*)(rowp + bj * HALF + wc * 32 + 8 * fq) = w; if (dupoff) *(u32x4*)(rowp + dupoff + bj * HALF + wc * 32 + 8 * fq) = w; }
;                     } else {
;                         const int pos = pos0 + tr;
;                         const int i0 = MODE == 2 ? (wc & 1) * 32 + 8 * fq : 8 * fq;
;                         const int col = MODE == 2 ? (wc >> 1) * 128 + i0 : wc * 64 + i0;
;                         const int hw = MODE == 2 ? 64 : 32;
;                         const f32x4* tp = (const f32x4*)((MODE == 2 ? rope + (size_t)pos * 64 : ropei + (size_t)pos * 32) + i0);
;                         const f32x4 t0 = tp[0], t1 = tp[1], t2 = tp[2], t3 = tp[3];
;                         const f32x4 a0 = acc[ai][0][m][0], a1 = acc[ai][0][m][1], b0 = acc[ai][1][m][0], b1 = acc[ai][1][m][1];
;                         float y1[8], y2[8];
;                         y1[0] = a0[0] * t0[0] - b0[0] * t0[1]; y2[0] = b0[0] * t0[0] + a0[0] * t0[1];
;                         y1[1] = a0[1] * t0[2] - b0[1] * t0[3]; y2[1] = b0[1] * t0[2] + a0[1] * t0[3];
;                         y1[2] = a0[2] * t1[0] - b0[2] * t1[1]; y2[2] = b0[2] * t1[0] + a0[2] * t1[1];
.LBB0_391:
	s_or_b64 exec, exec, s[40:41]
	s_nop 1
	v_add_u32_e32 v148, s43, v172
	v_lshlrev_b64 v[200:201], 8, v[148:149]
	v_lshl_add_u64 v[222:223], v[158:159], 0, v[200:201]
	global_load_dwordx4 v[200:203], v[222:223], off offset:48
	global_load_dwordx4 v[204:207], v[222:223], off offset:32
	global_load_dwordx4 v[218:221], v[222:223], off offset:16
	s_nop 0
	global_load_dwordx4 v[222:225], v[222:223], off
	v_cmp_gt_u32_e32 vcc, s21, v168
	s_and_saveexec_b64 s[40:41], vcc
	s_and_b64 s[64:65], s[28:29], exec
	s_cselect_b32 s6, 6, 10
	s_and_b64 s[64:65], s[34:35], exec
	v_lshl_add_u64 v[246:247], s[30:31], 0, v[168:169]
	s_cselect_b32 s6, 11, s6
	v_lshlrev_b64 v[246:247], s6, v[246:247]
	v_lshl_add_u64 v[210:211], v[246:247], 1, s[36:37]
	s_andn2_b64 vcc, exec, s[38:39]
	s_waitcnt vmcnt(12)
	v_mov_b32_e32 v247, v244
	v_mov_b32_e32 v244, v243
	v_mov_b32_e32 v246, v242
	v_pk_mul_f32 v[242:243], v[36:37], v[244:245]
	s_nop 0
	v_pk_fma_f32 v[242:243], v[44:45], v[246:247], v[242:243] neg_lo:[0,0,1] neg_hi:[0,0,1]
	v_pk_mul_f32 v[246:247], v[36:37], v[246:247]
	s_nop 0
	v_pk_fma_f32 v[244:245], v[44:45], v[244:245], v[246:247]
	v_mov_b32_e32 v247, v240
	v_mov_b32_e32 v240, v239
	v_mov_b32_e32 v246, v238
	v_pk_mul_f32 v[238:239], v[38:39], v[240:241]
	s_nop 0
	v_pk_fma_f32 v[238:239], v[46:47], v[246:247], v[238:239] neg_lo:[0,0,1] neg_hi:[0,0,1]
	v_pk_mul_f32 v[246:247], v[38:39], v[246:247]
	s_nop 0
	v_pk_fma_f32 v[240:241], v[46:47], v[240:241], v[246:247]
	v_mov_b32_e32 v247, v236
	v_mov_b32_e32 v236, v235
	v_mov_b32_e32 v246, v234
	v_pk_mul_f32 v[234:235], v[32:33], v[236:237]
	s_nop 0
	v_pk_fma_f32 v[234:235], v[40:41], v[246:247], v[234:235] neg_lo:[0,0,1] neg_hi:[0,0,1]
	v_pk_mul_f32 v[246:247], v[32:33], v[246:247]
	s_nop 0
	v_pk_fma_f32 v[236:237], v[40:41], v[236:237], v[246:247]
	v_mov_b32_e32 v247, v232
	v_mov_b32_e32 v232, v231
	v_mov_b32_e32 v246, v230
	v_pk_mul_f32 v[230:231], v[34:35], v[232:233]
	v_cvt_pk_bf16_f32 v236, v236, v237
	v_pk_fma_f32 v[248:249], v[42:43], v[246:247], v[230:231] neg_lo:[0,0,1] neg_hi:[0,0,1]
	v_pk_mul_f32 v[230:231], v[34:35], v[246:247]
	s_nop 0
	v_pk_fma_f32 v[246:247], v[42:43], v[232:233], v[230:231]
	v_cvt_pk_bf16_f32 v230, v242, v243
	v_cvt_pk_bf16_f32 v231, v238, v239
	v_cvt_pk_bf16_f32 v232, v234, v235
	v_cvt_pk_bf16_f32 v233, v248, v249
	v_cvt_pk_bf16_f32 v234, v244, v245
	v_cvt_pk_bf16_f32 v235, v240, v241
	v_cvt_pk_bf16_f32 v237, v246, v247
	v_lshl_add_u64 v[238:239], v[156:157], 1, v[210:211]
	global_store_dwordx4 v[238:239], v[230:233], off
	global_store_dwordx4 v[238:239], v[234:237], off offset:64
	s_cbranch_vccnz .LBB0_394
	s_lshl_b32 s6, s42, 1
	v_lshl_add_u64 v[210:211], v[210:211], 0, s[6:7]
	v_lshl_add_u64 v[210:211], v[156:157], 1, v[210:211]
	global_store_dwordx4 v[210:211], v[230:233], off
	global_store_dwordx4 v[210:211], v[234:237], off offset:64
;     template <int MODE>
;     __device__ __forceinline__ void store_tile(const f32x4 (&acc)[2][2][4][2], bf16_t* dst, int ld, int colbase, size_t rowbase, int nvalid, int pos0, size_t dupoff, int wr, int wc, int fr, int fq) const {
;     ...
;         for (int ai = 0; ai < 2; ++ai)
; #pragma unroll
;             for (int m = 0; m < 4; ++m) {
;                 const int tr = ai * HALF + wr * 64 + m * 16 + fr;
;                 if (tr < nvalid) {
;                     bf16_t* rowp = dst + (rowbase + tr) * (size_t)ld + colbase;
;                     if (MODE == 0 || MODE == 1) {
; #pragma unroll
;                         for (int bj = 0; bj < 2; ++bj) { f32x4 v0 = acc[ai][bj][m][0] * sc, v1 = acc[ai][bj][m][1] * sc;
;                             if (MODE == 1) {
; #pragma unroll
;                                 for (int j = 0; j < 4; ++j) { v0[j] = __builtin_amdgcn_rcpf(1.f + __builtin_amdgcn_exp2f(-1.4426950408889634f * v0[j])); v1[j] = __builtin_amdgcn_rcpf(1.f + __builtin_amdgcn_exp2f(-1.4426950408889634f * v1[j])); } }
;                             u32x4 w; w.x = cvt_pk_bf16(v0[0], v0[1]); w.y = cvt_pk_bf16(v0[2], v0[3]); w.z = cvt_pk_bf16(v1[0], v1[1]); w.w = cvt_pk_bf16(v1[2], v1[3]);
;                             *(u32x4*)(rowp + bj * HALF + wc * 32 + 8 * fq) = w; if (dupoff) *(u32x4*)(rowp + dupoff + bj * HALF + wc * 32 + 8 * fq) = w; }
;                     } else {
;                         const int pos = pos0 + tr;
;                         const int i0 = MODE == 2 ? (wc & 1) * 32 + 8 * fq : 8 * fq;
;                         const int col = MODE == 2 ? (wc >> 1) * 128 + i0 : wc * 64 + i0;
;                         const int hw = MODE == 2 ? 64 : 32;
;                         const f32x4* tp = (const f32x4*)((MODE == 2 ? rope + (size_t)pos * 64 : ropei + (size_t)pos * 32) + i0);
;                         const f32x4 t0 = tp[0], t1 = tp[1], t2 = tp[2], t3 = tp[3];
;                         const f32x4 a0 = acc[ai][0][m][0], a1 = acc[ai][0][m][1], b0 = acc[ai][1][m][0], b1 = acc[ai][1][m][1];
;                         float y1[8], y2[8];
;                         y1[0] = a0[0] * t0[0] - b0[0] * t0[1]; y2[0] = b0[0] * t0[0] + a0[0] * t0[1];
;                         y1[1] = a0[1] * t0[2] - b0[1] * t0[3]; y2[1] = b0[1] * t0[2] + a0[1] * t0[3];
;                         y1[2] = a0[2] * t1[0] - b0[2] * t1[1]; y2[2] = b0[2] * t1[0] + a0[2] * t1[1];
.LBB0_394:
	s_or_b64 exec, exec, s[40:41]
	v_cmp_gt_u32_e32 vcc, s21, v170
	s_and_saveexec_b64 s[40:41], vcc
	s_and_b64 s[64:65], s[28:29], exec
	s_cselect_b32 s6, 6, 10
	s_and_b64 s[64:65], s[34:35], exec
	v_lshl_add_u64 v[196:197], s[30:31], 0, v[170:171]
	s_cselect_b32 s6, 11, s6
	v_lshlrev_b64 v[196:197], s6, v[196:197]
	v_lshl_add_u64 v[184:185], v[196:197], 1, s[36:37]
	s_andn2_b64 vcc, exec, s[38:39]
	s_waitcnt vmcnt(8)
	v_mov_b32_e32 v197, v194
	v_mov_b32_e32 v194, v193
	v_mov_b32_e32 v196, v192
	v_pk_mul_f32 v[192:193], v[20:21], v[194:195]
	s_nop 0
	v_pk_fma_f32 v[192:193], v[28:29], v[196:197], v[192:193] neg_lo:[0,0,1] neg_hi:[0,0,1]
	v_pk_mul_f32 v[196:197], v[20:21], v[196:197]
	s_nop 0
	v_pk_fma_f32 v[194:195], v[28:29], v[194:195], v[196:197]
	v_mov_b32_e32 v197, v190
	v_mov_b32_e32 v190, v189
	v_mov_b32_e32 v196, v188
	v_pk_mul_f32 v[188:189], v[22:23], v[190:191]
	s_nop 0
	v_pk_fma_f32 v[188:189], v[30:31], v[196:197], v[188:189] neg_lo:[0,0,1] neg_hi:[0,0,1]
	v_pk_mul_f32 v[196:197], v[22:23], v[196:197]
	s_nop 0
	v_pk_fma_f32 v[190:191], v[30:31], v[190:191], v[196:197]
	v_mov_b32_e32 v197, v134
	v_mov_b32_e32 v134, v133
	v_mov_b32_e32 v196, v132
	v_pk_mul_f32 v[132:133], v[16:17], v[134:135]
	s_nop 0
	v_pk_fma_f32 v[132:133], v[24:25], v[196:197], v[132:133] neg_lo:[0,0,1] neg_hi:[0,0,1]
	v_pk_mul_f32 v[196:197], v[16:17], v[196:197]
	s_nop 0
	v_pk_fma_f32 v[134:135], v[24:25], v[134:135], v[196:197]
	v_mov_b32_e32 v197, v130
	v_mov_b32_e32 v130, v129
	v_mov_b32_e32 v196, v128
	v_pk_mul_f32 v[128:129], v[18:19], v[130:131]
	v_cvt_pk_bf16_f32 v134, v134, v135
	v_pk_fma_f32 v[198:199], v[26:27], v[196:197], v[128:129] neg_lo:[0,0,1] neg_hi:[0,0,1]
	v_pk_mul_f32 v[128:129], v[18:19], v[196:197]
	s_nop 0
	v_pk_fma_f32 v[196:197], v[26:27], v[130:131], v[128:129]
	v_cvt_pk_bf16_f32 v128, v192, v193
	v_cvt_pk_bf16_f32 v129, v188, v189
	v_cvt_pk_bf16_f32 v130, v132, v133
	v_cvt_pk_bf16_f32 v131, v198, v199
	v_cvt_pk_bf16_f32 v132, v194, v195
	v_cvt_pk_bf16_f32 v133, v190, v191
	v_cvt_pk_bf16_f32 v135, v196, v197
	v_lshl_add_u64 v[188:189], v[156:157], 1, v[184:185]
	global_store_dwordx4 v[188:189], v[128:131], off
	global_store_dwordx4 v[188:189], v[132:135], off offset:64
	s_cbranch_vccnz .LBB0_397
	s_lshl_b32 s6, s42, 1
	v_lshl_add_u64 v[184:185], v[184:185], 0, s[6:7]
	v_lshl_add_u64 v[184:185], v[156:157], 1, v[184:185]
	global_store_dwordx4 v[184:185], v[128:131], off
	global_store_dwordx4 v[184:185], v[132:135], off offset:64
.LBB0_397:
	s_or_b64 exec, exec, s[40:41]
	v_cmp_gt_u32_e32 vcc, s21, v172
	s_and_saveexec_b64 s[40:41], vcc
	s_and_b64 s[64:65], s[28:29], exec
	s_cselect_b32 s6, 6, 10
	s_and_b64 s[64:65], s[34:35], exec
	v_lshl_add_u64 v[226:227], s[30:31], 0, v[172:173]
	s_cselect_b32 s6, 11, s6
	v_lshlrev_b64 v[226:227], s6, v[226:227]
	v_lshl_add_u64 v[208:209], v[226:227], 1, s[36:37]
	s_andn2_b64 vcc, exec, s[38:39]
	s_waitcnt vmcnt(4)
	v_mov_b32_e32 v227, v224
	v_mov_b32_e32 v224, v223
	v_mov_b32_e32 v226, v222
	v_pk_mul_f32 v[222:223], v[4:5], v[224:225]
	s_nop 0
	v_pk_fma_f32 v[222:223], v[12:13], v[226:227], v[222:223] neg_lo:[0,0,1] neg_hi:[0,0,1]
	v_pk_mul_f32 v[226:227], v[4:5], v[226:227]
	s_nop 0
	v_pk_fma_f32 v[224:225], v[12:13], v[224:225], v[226:227]
	v_mov_b32_e32 v227, v220
	v_mov_b32_e32 v220, v219
	v_mov_b32_e32 v226, v218
	v_pk_mul_f32 v[218:219], v[6:7], v[220:221]
	s_nop 0
	v_pk_fma_f32 v[218:219], v[14:15], v[226:227], v[218:219] neg_lo:[0,0,1] neg_hi:[0,0,1]
	v_pk_mul_f32 v[226:227], v[6:7], v[226:227]
	s_nop 0
	v_pk_fma_f32 v[220:221], v[14:15], v[220:221], v[226:227]
	v_mov_b32_e32 v227, v206
	v_mov_b32_e32 v206, v205
	v_mov_b32_e32 v226, v204
	v_pk_mul_f32 v[204:205], v[0:1], v[206:207]
	s_nop 0
	v_pk_fma_f32 v[204:205], v[8:9], v[226:227], v[204:205] neg_lo:[0,0,1] neg_hi:[0,0,1]
	v_pk_mul_f32 v[226:227], v[0:1], v[226:227]
	s_nop 0
	v_pk_fma_f32 v[206:207], v[8:9], v[206:207], v[226:227]
	v_mov_b32_e32 v227, v202
	v_mov_b32_e32 v202, v201
	v_mov_b32_e32 v226, v200
	v_pk_mul_f32 v[200:201], v[2:3], v[202:203]
	v_cvt_pk_bf16_f32 v206, v206, v207
	v_pk_fma_f32 v[228:229], v[10:11], v[226:227], v[200:201] neg_lo:[0,0,1] neg_hi:[0,0,1]
	v_pk_mul_f32 v[200:201], v[2:3], v[226:227]
	s_nop 0
	v_pk_fma_f32 v[226:227], v[10:11], v[202:203], v[200:201]
	v_cvt_pk_bf16_f32 v200, v222, v223
	v_cvt_pk_bf16_f32 v201, v218, v219
	v_cvt_pk_bf16_f32 v202, v204, v205
	v_cvt_pk_bf16_f32 v203, v228, v229
	v_cvt_pk_bf16_f32 v204, v224, v225
	v_cvt_pk_bf16_f32 v205, v220, v221
	v_cvt_pk_bf16_f32 v207, v226, v227
	v_lshl_add_u64 v[218:219], v[156:157], 1, v[208:209]
	global_store_dwordx4 v[218:219], v[200:203], off
	global_store_dwordx4 v[218:219], v[204:207], off offset:64
	s_cbranch_vccnz .LBB0_400
	s_lshl_b32 s6, s42, 1
	v_lshl_add_u64 v[208:209], v[208:209], 0, s[6:7]
	v_lshl_add_u64 v[208:209], v[156:157], 1, v[208:209]
	global_store_dwordx4 v[208:209], v[200:203], off
	global_store_dwordx4 v[208:209], v[204:207], off offset:64
.LBB0_400:
	s_or_b64 exec, exec, s[40:41]
	s_cmpk_eq_u32 s21, 0x100
	s_cbranch_scc1 .Lrope_nd_a
	s_waitcnt vmcnt(0)

;     template <int MODE>
;     __device__ __forceinline__ void store_tile(const f32x4 (&acc)[2][2][4][2], bf16_t* dst, int ld, int colbase, size_t rowbase, int nvalid, int pos0, size_t dupoff, int wr, int wc, int fr, int fq) const {
;     ...
;         for (int ai = 0; ai < 2; ++ai)
; #pragma unroll
;             for (int m = 0; m < 4; ++m) {
;                 const int tr = ai * HALF + wr * 64 + m * 16 + fr;
;                 if (tr < nvalid) {
;                     bf16_t* rowp = dst + (rowbase + tr) * (size_t)ld + colbase;
;                     if (MODE == 0 || MODE == 1) {
; #pragma unroll
;                         for (int bj = 0; bj < 2; ++bj) { f32x4 v0 = acc[ai][bj][m][0] * sc, v1 = acc[ai][bj][m][1] * sc;
;                             if (MODE == 1) {
; #pragma unroll
;                                 for (int j = 0; j < 4; ++j) { v0[j] = __builtin_amdgcn_rcpf(1.f + __builtin_amdgcn_exp2f(-1.4426950408889634f * v0[j])); v1[j] = __builtin_amdgcn_rcpf(1.f + __builtin_amdgcn_exp2f(-1.4426950408889634f * v1[j])); } }
;                             u32x4 w; w.x = cvt_pk_bf16(v0[0], v0[1]); w.y = cvt_pk_bf16(v0[2], v0[3]); w.z = cvt_pk_bf16(v1[0], v1[1]); w.w = cvt_pk_bf16(v1[2], v1[3]);
;                             *(u32x4*)(rowp + bj * HALF + wc * 32 + 8 * fq) = w; if (dupoff) *(u32x4*)(rowp + dupoff + bj * HALF + wc * 32 + 8 * fq) = w; }
;                     } else {
;                         const int pos = pos0 + tr;
;                         const int i0 = MODE == 2 ? (wc & 1) * 32 + 8 * fq : 8 * fq;
;                         const int col = MODE == 2 ? (wc >> 1) * 128 + i0 : wc * 64 + i0;
;                         const int hw = MODE == 2 ? 64 : 32;
;                         const f32x4* tp = (const f32x4*)((MODE == 2 ? rope + (size_t)pos * 64 : ropei + (size_t)pos * 32) + i0);
;                         const f32x4 t0 = tp[0], t1 = tp[1], t2 = tp[2], t3 = tp[3];
;                         const f32x4 a0 = acc[ai][0][m][0], a1 = acc[ai][0][m][1], b0 = acc[ai][1][m][0], b1 = acc[ai][1][m][1];
;                         float y1[8], y2[8];
;                         y1[0] = a0[0] * t0[0] - b0[0] * t0[1]; y2[0] = b0[0] * t0[0] + a0[0] * t0[1];
;                         y1[1] = a0[1] * t0[2] - b0[1] * t0[3]; y2[1] = b0[1] * t0[2] + a0[1] * t0[3];
;                         y1[2] = a0[2] * t1[0] - b0[2] * t1[1]; y2[2] = b0[2] * t1[0] + a0[2] * t1[1];
.LBB0_401:
	s_and_b64 vcc, exec, s[40:41]
	s_cbranch_vccz .LBB0_427
	v_add_u32_e32 v148, s43, v150
	v_lshlrev_b64 v[128:129], 9, v[148:149]
	v_lshl_add_u64 v[192:193], v[176:177], 0, v[128:129]
	global_load_dwordx4 v[128:131], v[192:193], off offset:48
	global_load_dwordx4 v[132:135], v[192:193], off offset:32
	global_load_dwordx4 v[188:191], v[192:193], off offset:16
	s_nop 0
	global_load_dwordx4 v[192:195], v[192:193], off
	v_add_u32_e32 v148, s43, v160
	v_lshlrev_b64 v[200:201], 9, v[148:149]
	v_lshl_add_u64 v[222:223], v[176:177], 0, v[200:201]
	global_load_dwordx4 v[200:203], v[222:223], off offset:48
	global_load_dwordx4 v[204:207], v[222:223], off offset:32
	global_load_dwordx4 v[218:221], v[222:223], off offset:16
	s_nop 0
	global_load_dwordx4 v[222:225], v[222:223], off
	s_nop 1
	v_add_u32_e32 v148, s43, v162
	v_lshlrev_b64 v[230:231], 9, v[148:149]
	v_lshl_add_u64 v[242:243], v[176:177], 0, v[230:231]
	global_load_dwordx4 v[230:233], v[242:243], off offset:48
	global_load_dwordx4 v[234:237], v[242:243], off offset:32
	global_load_dwordx4 v[238:241], v[242:243], off offset:16
	s_nop 0
	global_load_dwordx4 v[242:245], v[242:243], off
	s_and_saveexec_b64 s[40:41], s[2:3]
	s_and_b64 s[64:65], s[28:29], exec
	s_cselect_b32 s6, 6, 10
	s_and_b64 s[64:65], s[34:35], exec
	v_lshl_add_u64 v[196:197], s[30:31], 0, v[150:151]
	s_cselect_b32 s6, 11, s6
	v_lshlrev_b64 v[196:197], s6, v[196:197]
	v_lshl_add_u64 v[184:185], v[196:197], 1, s[36:37]
	s_andn2_b64 vcc, exec, s[38:39]
	s_waitcnt vmcnt(8)
	v_mov_b32_e32 v197, v194
	v_mov_b32_e32 v194, v193
	v_mov_b32_e32 v196, v192
	v_pk_mul_f32 v[192:193], v[116:117], v[194:195]
	s_nop 0
	v_pk_fma_f32 v[192:193], v[124:125], v[196:197], v[192:193] neg_lo:[0,0,1] neg_hi:[0,0,1]
	v_pk_mul_f32 v[196:197], v[116:117], v[196:197]
	s_nop 0
	v_pk_fma_f32 v[194:195], v[124:125], v[194:195], v[196:197]
	v_mov_b32_e32 v197, v190
	v_mov_b32_e32 v190, v189
	v_mov_b32_e32 v196, v188
	v_pk_mul_f32 v[188:189], v[118:119], v[190:191]
	s_nop 0
	v_pk_fma_f32 v[188:189], v[126:127], v[196:197], v[188:189] neg_lo:[0,0,1] neg_hi:[0,0,1]
	v_pk_mul_f32 v[196:197], v[118:119], v[196:197]
	s_nop 0
	v_pk_fma_f32 v[190:191], v[126:127], v[190:191], v[196:197]
	v_mov_b32_e32 v197, v134
	v_mov_b32_e32 v134, v133
	v_mov_b32_e32 v196, v132
	v_pk_mul_f32 v[132:133], v[112:113], v[134:135]
	s_nop 0
	v_pk_fma_f32 v[132:133], v[120:121], v[196:197], v[132:133] neg_lo:[0,0,1] neg_hi:[0,0,1]
	v_pk_mul_f32 v[196:197], v[112:113], v[196:197]
	s_nop 0
	v_pk_fma_f32 v[134:135], v[120:121], v[134:135], v[196:197]
	v_mov_b32_e32 v197, v130
	v_mov_b32_e32 v130, v129
	v_mov_b32_e32 v196, v128
	v_pk_mul_f32 v[128:129], v[114:115], v[130:131]
	v_cvt_pk_bf16_f32 v134, v134, v135
	v_pk_fma_f32 v[198:199], v[122:123], v[196:197], v[128:129] neg_lo:[0,0,1] neg_hi:[0,0,1]
	v_pk_mul_f32 v[128:129], v[114:115], v[196:197]
	s_nop 0
	v_pk_fma_f32 v[196:197], v[122:123], v[130:131], v[128:129]
	v_cvt_pk_bf16_f32 v128, v192, v193
	v_cvt_pk_bf16_f32 v129, v188, v189
	v_cvt_pk_bf16_f32 v130, v132, v133
	v_cvt_pk_bf16_f32 v131, v198, v199
	v_cvt_pk_bf16_f32 v132, v194, v195
	v_cvt_pk_bf16_f32 v133, v190, v191
	v_cvt_pk_bf16_f32 v135, v196, v197
	v_lshl_add_u64 v[188:189], v[174:175], 1, v[184:185]
	global_store_dwordx4 v[188:189], v[128:131], off
	global_store_dwordx4 v[188:189], v[132:135], off offset:128
	s_cbranch_vccnz .LBB0_405
	s_lshl_b32 s6, s42, 1
	v_lshl_add_u64 v[184:185], v[184:185], 0, s[6:7]
	v_lshl_add_u64 v[184:185], v[174:175], 1, v[184:185]
	global_store_dwordx4 v[184:185], v[128:131], off
	global_store_dwordx4 v[184:185], v[132:135], off offset:128
.LBB0_405:
	s_or_b64 exec, exec, s[40:41]
	s_nop 1
	v_add_u32_e32 v148, s43, v164
	v_lshlrev_b64 v[128:129], 9, v[148:149]
	v_lshl_add_u64 v[192:193], v[176:177], 0, v[128:129]
	global_load_dwordx4 v[128:131], v[192:193], off offset:48
	global_load_dwordx4 v[132:135], v[192:193], off offset:32
	global_load_dwordx4 v[188:191], v[192:193], off offset:16
	s_nop 0
	global_load_dwordx4 v[192:195], v[192:193], off
	v_cmp_gt_u32_e32 vcc, s21, v160
	s_and_saveexec_b64 s[40:41], vcc
	s_and_b64 s[64:65], s[28:29], exec
	s_cselect_b32 s6, 6, 10
	s_and_b64 s[64:65], s[34:35], exec
	v_lshl_add_u64 v[226:227], s[30:31], 0, v[160:161]
	s_cselect_b32 s6, 11, s6
	v_lshlrev_b64 v[226:227], s6, v[226:227]
	v_lshl_add_u64 v[208:209], v[226:227], 1, s[36:37]
	s_andn2_b64 vcc, exec, s[38:39]
	s_waitcnt vmcnt(10)
	v_mov_b32_e32 v227, v224
	v_mov_b32_e32 v224, v223
	v_mov_b32_e32 v226, v222
	v_pk_mul_f32 v[222:223], v[100:101], v[224:225]
	s_nop 0
	v_pk_fma_f32 v[222:223], v[108:109], v[226:227], v[222:223] neg_lo:[0,0,1] neg_hi:[0,0,1]
	v_pk_mul_f32 v[226:227], v[100:101], v[226:227]
	s_nop 0
	v_pk_fma_f32 v[224:225], v[108:109], v[224:225], v[226:227]
	v_mov_b32_e32 v227, v220
	v_mov_b32_e32 v220, v219
	v_mov_b32_e32 v226, v218
	v_pk_mul_f32 v[218:219], v[102:103], v[220:221]
	s_nop 0
	v_pk_fma_f32 v[218:219], v[110:111], v[226:227], v[218:219] neg_lo:[0,0,1] neg_hi:[0,0,1]
	v_pk_mul_f32 v[226:227], v[102:103], v[226:227]
	s_nop 0
	v_pk_fma_f32 v[220:221], v[110:111], v[220:221], v[226:227]
	v_mov_b32_e32 v227, v206
	v_mov_b32_e32 v206, v205
	v_mov_b32_e32 v226, v204
	v_pk_mul_f32 v[204:205], v[96:97], v[206:207]
	s_nop 0
	v_pk_fma_f32 v[204:205], v[104:105], v[226:227], v[204:205] neg_lo:[0,0,1] neg_hi:[0,0,1]
	v_pk_mul_f32 v[226:227], v[96:97], v[226:227]
	s_nop 0
	v_pk_fma_f32 v[206:207], v[104:105], v[206:207], v[226:227]
	v_mov_b32_e32 v227, v202
	v_mov_b32_e32 v202, v201
	v_mov_b32_e32 v226, v200
	v_pk_mul_f32 v[200:201], v[98:99], v[202:203]
	v_cvt_pk_bf16_f32 v206, v206, v207
	v_pk_fma_f32 v[228:229], v[106:107], v[226:227], v[200:201] neg_lo:[0,0,1] neg_hi:[0,0,1]
	v_pk_mul_f32 v[200:201], v[98:99], v[226:227]
	s_nop 0
	v_pk_fma_f32 v[226:227], v[106:107], v[202:203], v[200:201]
	v_cvt_pk_bf16_f32 v200, v222, v223
	v_cvt_pk_bf16_f32 v201, v218, v219
	v_cvt_pk_bf16_f32 v202, v204, v205
	v_cvt_pk_bf16_f32 v203, v228, v229
	v_cvt_pk_bf16_f32 v204, v224, v225
	v_cvt_pk_bf16_f32 v205, v220, v221
	v_cvt_pk_bf16_f32 v207, v226, v227
	v_lshl_add_u64 v[218:219], v[174:175], 1, v[208:209]
	global_store_dwordx4 v[218:219], v[200:203], off
	global_store_dwordx4 v[218:219], v[204:207], off offset:128
	s_cbranch_vccnz .LBB0_408
	s_lshl_b32 s6, s42, 1
	v_lshl_add_u64 v[208:209], v[208:209], 0, s[6:7]
	v_lshl_add_u64 v[208:209], v[174:175], 1, v[208:209]
	global_store_dwordx4 v[208:209], v[200:203], off
	global_store_dwordx4 v[208:209], v[204:207], off offset:128
;     template <int MODE>
;     __device__ __forceinline__ void store_tile(const f32x4 (&acc)[2][2][4][2], bf16_t* dst, int ld, int colbase, size_t rowbase, int nvalid, int pos0, size_t dupoff, int wr, int wc, int fr, int fq) const {
;     ...
;         for (int ai = 0; ai < 2; ++ai)
; #pragma unroll
;             for (int m = 0; m < 4; ++m) {
;                 const int tr = ai * HALF + wr * 64 + m * 16 + fr;
;                 if (tr < nvalid) {
;                     bf16_t* rowp = dst + (rowbase + tr) * (size_t)ld + colbase;
;                     if (MODE == 0 || MODE == 1) {
; #pragma unroll
;                         for (int bj = 0; bj < 2; ++bj) { f32x4 v0 = acc[ai][bj][m][0] * sc, v1 = acc[ai][bj][m][1] * sc;
;                             if (MODE == 1) {
; #pragma unroll
;                                 for (int j = 0; j < 4; ++j) { v0[j] = __builtin_amdgcn_rcpf(1.f + __builtin_amdgcn_exp2f(-1.4426950408889634f * v0[j])); v1[j] = __builtin_amdgcn_rcpf(1.f + __builtin_amdgcn_exp2f(-1.4426950408889634f * v1[j])); } }
;                             u32x4 w; w.x = cvt_pk_bf16(v0[0], v0[1]); w.y = cvt_pk_bf16(v0[2], v0[3]); w.z = cvt_pk_bf16(v1[0], v1[1]); w.w = cvt_pk_bf16(v1[2], v1[3]);
;                             *(u32x4*)(rowp + bj * HALF + wc * 32 + 8 * fq) = w; if (dupoff) *(u32x4*)(rowp + dupoff + bj * HALF + wc * 32 + 8 * fq) = w; }
;                     } else {
;                         const int pos = pos0 + tr;
;                         const int i0 = MODE == 2 ? (wc & 1) * 32 + 8 * fq : 8 * fq;
;                         const int col = MODE == 2 ? (wc >> 1) * 128 + i0 : wc * 64 + i0;
;                         const int hw = MODE == 2 ? 64 : 32;
;                         const f32x4* tp = (const f32x4*)((MODE == 2 ? rope + (size_t)pos * 64 : ropei + (size_t)pos * 32) + i0);
;                         const f32x4 t0 = tp[0], t1 = tp[1], t2 = tp[2], t3 = tp[3];
;                         const f32x4 a0 = acc[ai][0][m][0], a1 = acc[ai][0][m][1], b0 = acc[ai][1][m][0], b1 = acc[ai][1][m][1];
;                         float y1[8], y2[8];
;                         y1[0] = a0[0] * t0[0] - b0[0] * t0[1]; y2[0] = b0[0] * t0[0] + a0[0] * t0[1];
;                         y1[1] = a0[1] * t0[2] - b0[1] * t0[3]; y2[1] = b0[1] * t0[2] + a0[1] * t0[3];
;                         y1[2] = a0[2] * t1[0] - b0[2] * t1[1]; y2[2] = b0[2] * t1[0] + a0[2] * t1[1];
.LBB0_408:
	s_or_b64 exec, exec, s[40:41]
	s_nop 1
	v_add_u32_e32 v148, s43, v166
	v_lshlrev_b64 v[200:201], 9, v[148:149]
	v_lshl_add_u64 v[222:223], v[176:177], 0, v[200:201]
	global_load_dwordx4 v[200:203], v[222:223], off offset:48
	global_load_dwordx4 v[204:207], v[222:223], off offset:32
	global_load_dwordx4 v[218:221], v[222:223], off offset:16
	s_nop 0
	global_load_dwordx4 v[222:225], v[222:223], off
	v_cmp_gt_u32_e32 vcc, s21, v162
	s_and_saveexec_b64 s[40:41], vcc
	s_and_b64 s[64:65], s[28:29], exec
	s_cselect_b32 s6, 6, 10
	s_and_b64 s[64:65], s[34:35], exec
	v_lshl_add_u64 v[246:247], s[30:31], 0, v[162:163]
	s_cselect_b32 s6, 11, s6
	v_lshlrev_b64 v[246:247], s6, v[246:247]
	v_lshl_add_u64 v[210:211], v[246:247], 1, s[36:37]
	s_andn2_b64 vcc, exec, s[38:39]
	s_waitcnt vmcnt(12)
	v_mov_b32_e32 v247, v244
	v_mov_b32_e32 v244, v243
	v_mov_b32_e32 v246, v242
	v_pk_mul_f32 v[242:243], v[84:85], v[244:245]
	s_nop 0
	v_pk_fma_f32 v[242:243], v[92:93], v[246:247], v[242:243] neg_lo:[0,0,1] neg_hi:[0,0,1]
	v_pk_mul_f32 v[246:247], v[84:85], v[246:247]
	s_nop 0
	v_pk_fma_f32 v[244:245], v[92:93], v[244:245], v[246:247]
	v_mov_b32_e32 v247, v240
	v_mov_b32_e32 v240, v239
	v_mov_b32_e32 v246, v238
	v_pk_mul_f32 v[238:239], v[86:87], v[240:241]
	s_nop 0
	v_pk_fma_f32 v[238:239], v[94:95], v[246:247], v[238:239] neg_lo:[0,0,1] neg_hi:[0,0,1]
	v_pk_mul_f32 v[246:247], v[86:87], v[246:247]
	s_nop 0
	v_pk_fma_f32 v[240:241], v[94:95], v[240:241], v[246:247]
	v_mov_b32_e32 v247, v236
	v_mov_b32_e32 v236, v235
	v_mov_b32_e32 v246, v234
	v_pk_mul_f32 v[234:235], v[80:81], v[236:237]
	s_nop 0
	v_pk_fma_f32 v[234:235], v[88:89], v[246:247], v[234:235] neg_lo:[0,0,1] neg_hi:[0,0,1]
	v_pk_mul_f32 v[246:247], v[80:81], v[246:247]
	s_nop 0
	v_pk_fma_f32 v[236:237], v[88:89], v[236:237], v[246:247]
	v_mov_b32_e32 v247, v232
	v_mov_b32_e32 v232, v231
	v_mov_b32_e32 v246, v230
	v_pk_mul_f32 v[230:231], v[82:83], v[232:233]
	v_cvt_pk_bf16_f32 v236, v236, v237
	v_pk_fma_f32 v[248:249], v[90:91], v[246:247], v[230:231] neg_lo:[0,0,1] neg_hi:[0,0,1]
	v_pk_mul_f32 v[230:231], v[82:83], v[246:247]
	s_nop 0
	v_pk_fma_f32 v[246:247], v[90:91], v[232:233], v[230:231]
	v_cvt_pk_bf16_f32 v230, v242, v243
	v_cvt_pk_bf16_f32 v231, v238, v239
	v_cvt_pk_bf16_f32 v232, v234, v235
	v_cvt_pk_bf16_f32 v233, v248, v249
	v_cvt_pk_bf16_f32 v234, v244, v245
	v_cvt_pk_bf16_f32 v235, v240, v241
	v_cvt_pk_bf16_f32 v237, v246, v247
	v_lshl_add_u64 v[238:239], v[174:175], 1, v[210:211]
	global_store_dwordx4 v[238:239], v[230:233], off
	global_store_dwordx4 v[238:239], v[234:237], off offset:128
	s_cbranch_vccnz .LBB0_411
	s_lshl_b32 s6, s42, 1
	v_lshl_add_u64 v[210:211], v[210:211], 0, s[6:7]
	v_lshl_add_u64 v[210:211], v[174:175], 1, v[210:211]
	global_store_dwordx4 v[210:211], v[230:233], off
	global_store_dwordx4 v[210:211], v[234:237], off offset:128
.LBB0_411:
	s_or_b64 exec, exec, s[40:41]
	s_nop 1
	v_add_u32_e32 v148, s43, v168
	v_lshlrev_b64 v[230:231], 9, v[148:149]
	v_lshl_add_u64 v[242:243], v[176:177], 0, v[230:231]
	global_load_dwordx4 v[230:233], v[242:243], off offset:48
	global_load_dwordx4 v[234:237], v[242:243], off offset:32
	global_load_dwordx4 v[238:241], v[242:243], off offset:16
	s_nop 0
	global_load_dwordx4 v[242:245], v[242:243], off
	v_cmp_gt_u32_e32 vcc, s21, v164
	s_and_saveexec_b64 s[40:41], vcc
	s_and_b64 s[64:65], s[28:29], exec
	s_cselect_b32 s6, 6, 10
	s_and_b64 s[64:65], s[34:35], exec
	v_lshl_add_u64 v[196:197], s[30:31], 0, v[164:165]
	s_cselect_b32 s6, 11, s6
	v_lshlrev_b64 v[196:197], s6, v[196:197]
	v_lshl_add_u64 v[184:185], v[196:197], 1, s[36:37]
	s_andn2_b64 vcc, exec, s[38:39]
	s_waitcnt vmcnt(12)
	v_mov_b32_e32 v197, v194
	v_mov_b32_e32 v194, v193
	v_mov_b32_e32 v196, v192
	v_pk_mul_f32 v[192:193], v[68:69], v[194:195]
	s_nop 0
	v_pk_fma_f32 v[192:193], v[76:77], v[196:197], v[192:193] neg_lo:[0,0,1] neg_hi:[0,0,1]
	v_pk_mul_f32 v[196:197], v[68:69], v[196:197]
	s_nop 0
	v_pk_fma_f32 v[194:195], v[76:77], v[194:195], v[196:197]
	v_mov_b32_e32 v197, v190
	v_mov_b32_e32 v190, v189
	v_mov_b32_e32 v196, v188
	v_pk_mul_f32 v[188:189], v[70:71], v[190:191]
	s_nop 0
	v_pk_fma_f32 v[188:189], v[78:79], v[196:197], v[188:189] neg_lo:[0,0,1] neg_hi:[0,0,1]
	v_pk_mul_f32 v[196:197], v[70:71], v[196:197]
	s_nop 0
	v_pk_fma_f32 v[190:191], v[78:79], v[190:191], v[196:197]
	v_mov_b32_e32 v197, v134
	v_mov_b32_e32 v134, v133
	v_mov_b32_e32 v196, v132
	v_pk_mul_f32 v[132:133], v[64:65], v[134:135]
	s_nop 0
	v_pk_fma_f32 v[132:133], v[72:73], v[196:197], v[132:133] neg_lo:[0,0,1] neg_hi:[0,0,1]
	v_pk_mul_f32 v[196:197], v[64:65], v[196:197]
	s_nop 0
	v_pk_fma_f32 v[134:135], v[72:73], v[134:135], v[196:197]
	v_mov_b32_e32 v197, v130
	v_mov_b32_e32 v130, v129
	v_mov_b32_e32 v196, v128
	v_pk_mul_f32 v[128:129], v[66:67], v[130:131]
	v_cvt_pk_bf16_f32 v134, v134, v135
	v_pk_fma_f32 v[198:199], v[74:75], v[196:197], v[128:129] neg_lo:[0,0,1] neg_hi:[0,0,1]
	v_pk_mul_f32 v[128:129], v[66:67], v[196:197]
	s_nop 0
	v_pk_fma_f32 v[196:197], v[74:75], v[130:131], v[128:129]
	v_cvt_pk_bf16_f32 v128, v192, v193
	v_cvt_pk_bf16_f32 v129, v188, v189
	v_cvt_pk_bf16_f32 v130, v132, v133
	v_cvt_pk_bf16_f32 v131, v198, v199
	v_cvt_pk_bf16_f32 v132, v194, v195
	v_cvt_pk_bf16_f32 v133, v190, v191
	v_cvt_pk_bf16_f32 v135, v196, v197
	v_lshl_add_u64 v[188:189], v[174:175], 1, v[184:185]
	global_store_dwordx4 v[188:189], v[128:131], off
	global_store_dwordx4 v[188:189], v[132:135], off offset:128
	s_cbranch_vccnz .LBB0_414
	s_lshl_b32 s6, s42, 1
	v_lshl_add_u64 v[184:185], v[184:185], 0, s[6:7]
	v_lshl_add_u64 v[184:185], v[174:175], 1, v[184:185]
	global_store_dwordx4 v[184:185], v[128:131], off
	global_store_dwordx4 v[184:185], v[132:135], off offset:128
;     template <int MODE>
;     __device__ __forceinline__ void store_tile(const f32x4 (&acc)[2][2][4][2], bf16_t* dst, int ld, int colbase, size_t rowbase, int nvalid, int pos0, size_t dupoff, int wr, int wc, int fr, int fq) const {
;     ...
;         for (int ai = 0; ai < 2; ++ai)
; #pragma unroll
;             for (int m = 0; m < 4; ++m) {
;                 const int tr = ai * HALF + wr * 64 + m * 16 + fr;
;                 if (tr < nvalid) {
;                     bf16_t* rowp = dst + (rowbase + tr) * (size_t)ld + colbase;
;                     if (MODE == 0 || MODE == 1) {
; #pragma unroll
;                         for (int bj = 0; bj < 2; ++bj) { f32x4 v0 = acc[ai][bj][m][0] * sc, v1 = acc[ai][bj][m][1] * sc;
;                             if (MODE == 1) {
; #pragma unroll
;                                 for (int j = 0; j < 4; ++j) { v0[j] = __builtin_amdgcn_rcpf(1.f + __builtin_amdgcn_exp2f(-1.4426950408889634f * v0[j])); v1[j] = __builtin_amdgcn_rcpf(1.f + __builtin_amdgcn_exp2f(-1.4426950408889634f * v1[j])); } }
;                             u32x4 w; w.x = cvt_pk_bf16(v0[0], v0[1]); w.y = cvt_pk_bf16(v0[2], v0[3]); w.z = cvt_pk_bf16(v1[0], v1[1]); w.w = cvt_pk_bf16(v1[2], v1[3]);
;                             *(u32x4*)(rowp + bj * HALF + wc * 32 + 8 * fq) = w; if (dupoff) *(u32x4*)(rowp + dupoff + bj * HALF + wc * 32 + 8 * fq) = w; }
;                     } else {
;                         const int pos = pos0 + tr;
;                         const int i0 = MODE == 2 ? (wc & 1) * 32 + 8 * fq : 8 * fq;
;                         const int col = MODE == 2 ? (wc >> 1) * 128 + i0 : wc * 64 + i0;
;                         const int hw = MODE == 2 ? 64 : 32;
;                         const f32x4* tp = (const f32x4*)((MODE == 2 ? rope + (size_t)pos * 64 : ropei + (size_t)pos * 32) + i0);
;                         const f32x4 t0 = tp[0], t1 = tp[1], t2 = tp[2], t3 = tp[3];
;                         const f32x4 a0 = acc[ai][0][m][0], a1 = acc[ai][0][m][1], b0 = acc[ai][1][m][0], b1 = acc[ai][1][m][1];
;                         float y1[8], y2[8];
;                         y1[0] = a0[0] * t0[0] - b0[0] * t0[1]; y2[0] = b0[0] * t0[0] + a0[0] * t0[1];
;                         y1[1] = a0[1] * t0[2] - b0[1] * t0[3]; y2[1] = b0[1] * t0[2] + a0[1] * t0[3];
;                         y1[2] = a0[2] * t1[0] - b0[2] * t1[1]; y2[2] = b0[2] * t1[0] + a0[2] * t1[1];
.LBB0_414:
	s_or_b64 exec, exec, s[40:41]
	s_nop 1
	v_add_u32_e32 v148, s43, v170
	v_lshlrev_b64 v[128:129], 9, v[148:149]
	v_lshl_add_u64 v[192:193], v[176:177], 0, v[128:129]
	global_load_dwordx4 v[128:131], v[192:193], off offset:48
	global_load_dwordx4 v[132:135], v[192:193], off offset:32
	global_load_dwordx4 v[188:191], v[192:193], off offset:16
	s_nop 0
	global_load_dwordx4 v[192:195], v[192:193], off
	v_cmp_gt_u32_e32 vcc, s21, v166
	s_and_saveexec_b64 s[40:41], vcc
	s_and_b64 s[64:65], s[28:29], exec
	s_cselect_b32 s6, 6, 10
	s_and_b64 s[64:65], s[34:35], exec
	v_lshl_add_u64 v[226:227], s[30:31], 0, v[166:167]
	s_cselect_b32 s6, 11, s6
	v_lshlrev_b64 v[226:227], s6, v[226:227]
	v_lshl_add_u64 v[208:209], v[226:227], 1, s[36:37]
	s_andn2_b64 vcc, exec, s[38:39]
	s_waitcnt vmcnt(12)
	v_mov_b32_e32 v227, v224
	v_mov_b32_e32 v224, v223
	v_mov_b32_e32 v226, v222
	v_pk_mul_f32 v[222:223], v[52:53], v[224:225]
	s_nop 0
	v_pk_fma_f32 v[222:223], v[60:61], v[226:227], v[222:223] neg_lo:[0,0,1] neg_hi:[0,0,1]
	v_pk_mul_f32 v[226:227], v[52:53], v[226:227]
	s_nop 0
	v_pk_fma_f32 v[224:225], v[60:61], v[224:225], v[226:227]
	v_mov_b32_e32 v227, v220
	v_mov_b32_e32 v220, v219
	v_mov_b32_e32 v226, v218
	v_pk_mul_f32 v[218:219], v[54:55], v[220:221]
	s_nop 0
	v_pk_fma_f32 v[218:219], v[62:63], v[226:227], v[218:219] neg_lo:[0,0,1] neg_hi:[0,0,1]
	v_pk_mul_f32 v[226:227], v[54:55], v[226:227]
	s_nop 0
	v_pk_fma_f32 v[220:221], v[62:63], v[220:221], v[226:227]
	v_mov_b32_e32 v227, v206
	v_mov_b32_e32 v206, v205
	v_mov_b32_e32 v226, v204
	v_pk_mul_f32 v[204:205], v[48:49], v[206:207]
	s_nop 0
	v_pk_fma_f32 v[204:205], v[56:57], v[226:227], v[204:205] neg_lo:[0,0,1] neg_hi:[0,0,1]
	v_pk_mul_f32 v[226:227], v[48:49], v[226:227]
	s_nop 0
	v_pk_fma_f32 v[206:207], v[56:57], v[206:207], v[226:227]
	v_mov_b32_e32 v227, v202
	v_mov_b32_e32 v202, v201
	v_mov_b32_e32 v226, v200
	v_pk_mul_f32 v[200:201], v[50:51], v[202:203]
	v_cvt_pk_bf16_f32 v206, v206, v207
	v_pk_fma_f32 v[228:229], v[58:59], v[226:227], v[200:201] neg_lo:[0,0,1] neg_hi:[0,0,1]
	v_pk_mul_f32 v[200:201], v[50:51], v[226:227]
	s_nop 0
	v_pk_fma_f32 v[226:227], v[58:59], v[202:203], v[200:201]
	v_cvt_pk_bf16_f32 v200, v222, v223
	v_cvt_pk_bf16_f32 v201, v218, v219
	v_cvt_pk_bf16_f32 v202, v204, v205
	v_cvt_pk_bf16_f32 v203, v228, v229
	v_cvt_pk_bf16_f32 v204, v224, v225
	v_cvt_pk_bf16_f32 v205, v220, v221
	v_cvt_pk_bf16_f32 v207, v226, v227
	v_lshl_add_u64 v[218:219], v[174:175], 1, v[208:209]
	global_store_dwordx4 v[218:219], v[200:203], off
	global_store_dwordx4 v[218:219], v[204:207], off offset:128
	s_cbranch_vccnz .LBB0_417
	s_lshl_b32 s6, s42, 1
	v_lshl_add_u64 v[208:209], v[208:209], 0, s[6:7]
	v_lshl_add_u64 v[208:209], v[174:175], 1, v[208:209]
	global_store_dwordx4 v[208:209], v[200:203], off
	global_store_dwordx4 v[208:209], v[204:207], off offset:128
.LBB0_417:
	s_or_b64 exec, exec, s[40:41]
	s_nop 1
	v_add_u32_e32 v148, s43, v172
	v_lshlrev_b64 v[200:201], 9, v[148:149]
	v_lshl_add_u64 v[222:223], v[176:177], 0, v[200:201]
	global_load_dwordx4 v[200:203], v[222:223], off offset:48
	global_load_dwordx4 v[204:207], v[222:223], off offset:32
	global_load_dwordx4 v[218:221], v[222:223], off offset:16
	s_nop 0
	global_load_dwordx4 v[222:225], v[222:223], off
	v_cmp_gt_u32_e32 vcc, s21, v168
	s_and_saveexec_b64 s[40:41], vcc
	s_and_b64 s[64:65], s[28:29], exec
	s_cselect_b32 s6, 6, 10
	s_and_b64 s[64:65], s[34:35], exec
	v_lshl_add_u64 v[246:247], s[30:31], 0, v[168:169]
	s_cselect_b32 s6, 11, s6
	v_lshlrev_b64 v[246:247], s6, v[246:247]
	v_lshl_add_u64 v[210:211], v[246:247], 1, s[36:37]
	s_andn2_b64 vcc, exec, s[38:39]
	s_waitcnt vmcnt(12)
	v_mov_b32_e32 v247, v244
	v_mov_b32_e32 v244, v243
	v_mov_b32_e32 v246, v242
	v_pk_mul_f32 v[242:243], v[36:37], v[244:245]
	s_nop 0
	v_pk_fma_f32 v[242:243], v[44:45], v[246:247], v[242:243] neg_lo:[0,0,1] neg_hi:[0,0,1]
	v_pk_mul_f32 v[246:247], v[36:37], v[246:247]
	s_nop 0
	v_pk_fma_f32 v[244:245], v[44:45], v[244:245], v[246:247]
	v_mov_b32_e32 v247, v240
	v_mov_b32_e32 v240, v239
	v_mov_b32_e32 v246, v238
	v_pk_mul_f32 v[238:239], v[38:39], v[240:241]
	s_nop 0
	v_pk_fma_f32 v[238:239], v[46:47], v[246:247], v[238:239] neg_lo:[0,0,1] neg_hi:[0,0,1]
	v_pk_mul_f32 v[246:247], v[38:39], v[246:247]
	s_nop 0
	v_pk_fma_f32 v[240:241], v[46:47], v[240:241], v[246:247]
	v_mov_b32_e32 v247, v236
	v_mov_b32_e32 v236, v235
	v_mov_b32_e32 v246, v234
	v_pk_mul_f32 v[234:235], v[32:33], v[236:237]
	s_nop 0
	v_pk_fma_f32 v[234:235], v[40:41], v[246:247], v[234:235] neg_lo:[0,0,1] neg_hi:[0,0,1]
	v_pk_mul_f32 v[246:247], v[32:33], v[246:247]
	s_nop 0
	v_pk_fma_f32 v[236:237], v[40:41], v[236:237], v[246:247]
	v_mov_b32_e32 v247, v232
	v_mov_b32_e32 v232, v231
	v_mov_b32_e32 v246, v230
	v_pk_mul_f32 v[230:231], v[34:35], v[232:233]
	v_cvt_pk_bf16_f32 v236, v236, v237
	v_pk_fma_f32 v[248:249], v[42:43], v[246:247], v[230:231] neg_lo:[0,0,1] neg_hi:[0,0,1]
	v_pk_mul_f32 v[230:231], v[34:35], v[246:247]
	s_nop 0
	v_pk_fma_f32 v[246:247], v[42:43], v[232:233], v[230:231]
	v_cvt_pk_bf16_f32 v230, v242, v243
	v_cvt_pk_bf16_f32 v231, v238, v239
	v_cvt_pk_bf16_f32 v232, v234, v235
	v_cvt_pk_bf16_f32 v233, v248, v249
	v_cvt_pk_bf16_f32 v234, v244, v245
	v_cvt_pk_bf16_f32 v235, v240, v241
	v_cvt_pk_bf16_f32 v237, v246, v247
	v_lshl_add_u64 v[238:239], v[174:175], 1, v[210:211]
	global_store_dwordx4 v[238:239], v[230:233], off
	global_store_dwordx4 v[238:239], v[234:237], off offset:128
	s_cbranch_vccnz .LBB0_420
	s_lshl_b32 s6, s42, 1
	v_lshl_add_u64 v[210:211], v[210:211], 0, s[6:7]
	v_lshl_add_u64 v[210:211], v[174:175], 1, v[210:211]
	global_store_dwordx4 v[210:211], v[230:233], off
	global_store_dwordx4 v[210:211], v[234:237], off offset:128
;     template <int MODE>
;     __device__ __forceinline__ void store_tile(const f32x4 (&acc)[2][2][4][2], bf16_t* dst, int ld, int colbase, size_t rowbase, int nvalid, int pos0, size_t dupoff, int wr, int wc, int fr, int fq) const {
;     ...
;         for (int ai = 0; ai < 2; ++ai)
; #pragma unroll
;             for (int m = 0; m < 4; ++m) {
;                 const int tr = ai * HALF + wr * 64 + m * 16 + fr;
;                 if (tr < nvalid) {
;                     bf16_t* rowp = dst + (rowbase + tr) * (size_t)ld + colbase;
;                     if (MODE == 0 || MODE == 1) {
; #pragma unroll
;                         for (int bj = 0; bj < 2; ++bj) { f32x4 v0 = acc[ai][bj][m][0] * sc, v1 = acc[ai][bj][m][1] * sc;
;                             if (MODE == 1) {
; #pragma unroll
;                                 for (int j = 0; j < 4; ++j) { v0[j] = __builtin_amdgcn_rcpf(1.f + __builtin_amdgcn_exp2f(-1.4426950408889634f * v0[j])); v1[j] = __builtin_amdgcn_rcpf(1.f + __builtin_amdgcn_exp2f(-1.4426950408889634f * v1[j])); } }
;                             u32x4 w; w.x = cvt_pk_bf16(v0[0], v0[1]); w.y = cvt_pk_bf16(v0[2], v0[3]); w.z = cvt_pk_bf16(v1[0], v1[1]); w.w = cvt_pk_bf16(v1[2], v1[3]);
;                             *(u32x4*)(rowp + bj * HALF + wc * 32 + 8 * fq) = w; if (dupoff) *(u32x4*)(rowp + dupoff + bj * HALF + wc * 32 + 8 * fq) = w; }
;                     } else {
;                         const int pos = pos0 + tr;
;                         const int i0 = MODE == 2 ? (wc & 1) * 32 + 8 * fq : 8 * fq;
;                         const int col = MODE == 2 ? (wc >> 1) * 128 + i0 : wc * 64 + i0;
;                         const int hw = MODE == 2 ? 64 : 32;
;                         const f32x4* tp = (const f32x4*)((MODE == 2 ? rope + (size_t)pos * 64 : ropei + (size_t)pos * 32) + i0);
;                         const f32x4 t0 = tp[0], t1 = tp[1], t2 = tp[2], t3 = tp[3];
;                         const f32x4 a0 = acc[ai][0][m][0], a1 = acc[ai][0][m][1], b0 = acc[ai][1][m][0], b1 = acc[ai][1][m][1];
;                         float y1[8], y2[8];
;                         y1[0] = a0[0] * t0[0] - b0[0] * t0[1]; y2[0] = b0[0] * t0[0] + a0[0] * t0[1];
;                         y1[1] = a0[1] * t0[2] - b0[1] * t0[3]; y2[1] = b0[1] * t0[2] + a0[1] * t0[3];
;                         y1[2] = a0[2] * t1[0] - b0[2] * t1[1]; y2[2] = b0[2] * t1[0] + a0[2] * t1[1];
.LBB0_420:
	s_or_b64 exec, exec, s[40:41]
	v_cmp_gt_u32_e32 vcc, s21, v170
	s_and_saveexec_b64 s[40:41], vcc
	s_and_b64 s[64:65], s[28:29], exec
	s_cselect_b32 s6, 6, 10
	s_and_b64 s[64:65], s[34:35], exec
	v_lshl_add_u64 v[196:197], s[30:31], 0, v[170:171]
	s_cselect_b32 s6, 11, s6
	v_lshlrev_b64 v[196:197], s6, v[196:197]
	v_lshl_add_u64 v[184:185], v[196:197], 1, s[36:37]
	s_andn2_b64 vcc, exec, s[38:39]
	s_waitcnt vmcnt(8)
	v_mov_b32_e32 v197, v194
	v_mov_b32_e32 v194, v193
	v_mov_b32_e32 v196, v192
	v_pk_mul_f32 v[192:193], v[20:21], v[194:195]
	s_nop 0
	v_pk_fma_f32 v[192:193], v[28:29], v[196:197], v[192:193] neg_lo:[0,0,1] neg_hi:[0,0,1]
	v_pk_mul_f32 v[196:197], v[20:21], v[196:197]
	s_nop 0
	v_pk_fma_f32 v[194:195], v[28:29], v[194:195], v[196:197]
	v_mov_b32_e32 v197, v190
	v_mov_b32_e32 v190, v189
	v_mov_b32_e32 v196, v188
	v_pk_mul_f32 v[188:189], v[22:23], v[190:191]
	s_nop 0
	v_pk_fma_f32 v[188:189], v[30:31], v[196:197], v[188:189] neg_lo:[0,0,1] neg_hi:[0,0,1]
	v_pk_mul_f32 v[196:197], v[22:23], v[196:197]
	s_nop 0
	v_pk_fma_f32 v[190:191], v[30:31], v[190:191], v[196:197]
	v_mov_b32_e32 v197, v134
	v_mov_b32_e32 v134, v133
	v_mov_b32_e32 v196, v132
	v_pk_mul_f32 v[132:133], v[16:17], v[134:135]
	s_nop 0
	v_pk_fma_f32 v[132:133], v[24:25], v[196:197], v[132:133] neg_lo:[0,0,1] neg_hi:[0,0,1]
	v_pk_mul_f32 v[196:197], v[16:17], v[196:197]
	s_nop 0
	v_pk_fma_f32 v[134:135], v[24:25], v[134:135], v[196:197]
	v_mov_b32_e32 v197, v130
	v_mov_b32_e32 v130, v129
	v_mov_b32_e32 v196, v128
	v_pk_mul_f32 v[128:129], v[18:19], v[130:131]
	v_cvt_pk_bf16_f32 v134, v134, v135
	v_pk_fma_f32 v[198:199], v[26:27], v[196:197], v[128:129] neg_lo:[0,0,1] neg_hi:[0,0,1]
	v_pk_mul_f32 v[128:129], v[18:19], v[196:197]
	s_nop 0
	v_pk_fma_f32 v[196:197], v[26:27], v[130:131], v[128:129]
	v_cvt_pk_bf16_f32 v128, v192, v193
	v_cvt_pk_bf16_f32 v129, v188, v189
	v_cvt_pk_bf16_f32 v130, v132, v133
	v_cvt_pk_bf16_f32 v131, v198, v199
	v_cvt_pk_bf16_f32 v132, v194, v195
	v_cvt_pk_bf16_f32 v133, v190, v191
	v_cvt_pk_bf16_f32 v135, v196, v197
	v_lshl_add_u64 v[188:189], v[174:175], 1, v[184:185]
	global_store_dwordx4 v[188:189], v[128:131], off
	global_store_dwordx4 v[188:189], v[132:135], off offset:128
	s_cbranch_vccnz .LBB0_423
	s_lshl_b32 s6, s42, 1
	v_lshl_add_u64 v[184:185], v[184:185], 0, s[6:7]
	v_lshl_add_u64 v[184:185], v[174:175], 1, v[184:185]
	global_store_dwordx4 v[184:185], v[128:131], off
	global_store_dwordx4 v[184:185], v[132:135], off offset:128
.LBB0_423:
	s_or_b64 exec, exec, s[40:41]
	v_cmp_gt_u32_e32 vcc, s21, v172
	s_and_saveexec_b64 s[40:41], vcc
	s_and_b64 s[64:65], s[28:29], exec
	s_cselect_b32 s6, 6, 10
	s_and_b64 s[64:65], s[34:35], exec
	v_lshl_add_u64 v[226:227], s[30:31], 0, v[172:173]
	s_cselect_b32 s6, 11, s6
	v_lshlrev_b64 v[226:227], s6, v[226:227]
	v_lshl_add_u64 v[208:209], v[226:227], 1, s[36:37]
	s_andn2_b64 vcc, exec, s[38:39]
	s_waitcnt vmcnt(4)
	v_mov_b32_e32 v227, v224
	v_mov_b32_e32 v224, v223
	v_mov_b32_e32 v226, v222
	v_pk_mul_f32 v[222:223], v[4:5], v[224:225]
	s_nop 0
	v_pk_fma_f32 v[222:223], v[12:13], v[226:227], v[222:223] neg_lo:[0,0,1] neg_hi:[0,0,1]
	v_pk_mul_f32 v[226:227], v[4:5], v[226:227]
	s_nop 0
	v_pk_fma_f32 v[224:225], v[12:13], v[224:225], v[226:227]
	v_mov_b32_e32 v227, v220
	v_mov_b32_e32 v220, v219
	v_mov_b32_e32 v226, v218
	v_pk_mul_f32 v[218:219], v[6:7], v[220:221]
	s_nop 0
	v_pk_fma_f32 v[218:219], v[14:15], v[226:227], v[218:219] neg_lo:[0,0,1] neg_hi:[0,0,1]
	v_pk_mul_f32 v[226:227], v[6:7], v[226:227]
	s_nop 0
	v_pk_fma_f32 v[220:221], v[14:15], v[220:221], v[226:227]
	v_mov_b32_e32 v227, v206
	v_mov_b32_e32 v206, v205
	v_mov_b32_e32 v226, v204
	v_pk_mul_f32 v[204:205], v[0:1], v[206:207]
	s_nop 0
	v_pk_fma_f32 v[204:205], v[8:9], v[226:227], v[204:205] neg_lo:[0,0,1] neg_hi:[0,0,1]
	v_pk_mul_f32 v[226:227], v[0:1], v[226:227]
	s_nop 0
	v_pk_fma_f32 v[206:207], v[8:9], v[206:207], v[226:227]
	v_mov_b32_e32 v227, v202
	v_mov_b32_e32 v202, v201
	v_mov_b32_e32 v226, v200
	v_pk_mul_f32 v[200:201], v[2:3], v[202:203]
	v_cvt_pk_bf16_f32 v206, v206, v207
	v_pk_fma_f32 v[228:229], v[10:11], v[226:227], v[200:201] neg_lo:[0,0,1] neg_hi:[0,0,1]
	v_pk_mul_f32 v[200:201], v[2:3], v[226:227]
	s_nop 0
	v_pk_fma_f32 v[226:227], v[10:11], v[202:203], v[200:201]
	v_cvt_pk_bf16_f32 v200, v222, v223
	v_cvt_pk_bf16_f32 v201, v218, v219
	v_cvt_pk_bf16_f32 v202, v204, v205
	v_cvt_pk_bf16_f32 v203, v228, v229
	v_cvt_pk_bf16_f32 v204, v224, v225
	v_cvt_pk_bf16_f32 v205, v220, v221
	v_cvt_pk_bf16_f32 v207, v226, v227
	v_lshl_add_u64 v[218:219], v[174:175], 1, v[208:209]
	global_store_dwordx4 v[218:219], v[200:203], off
	global_store_dwordx4 v[218:219], v[204:207], off offset:128
	s_cbranch_vccnz .LBB0_426
	s_lshl_b32 s6, s42, 1
	v_lshl_add_u64 v[208:209], v[208:209], 0, s[6:7]
	v_lshl_add_u64 v[208:209], v[174:175], 1, v[208:209]
	global_store_dwordx4 v[208:209], v[200:203], off
	global_store_dwordx4 v[208:209], v[204:207], off offset:128

;     __device__ __forceinline__ void operator()(const f32x4 (&acc)[2][2][4][2], const Unit& u, int wr, int wc, int fr, int fq) const {
;     ...
;         if (mode == 0) store_tile<0>(acc, dst, ld, colbase, rowbase, nvalid, pos0, dupoff, wr, wc, fr, fq);
;         else if (mode == 1) store_tile<1>(acc, dst, ld, colbase, rowbase, nvalid, pos0, dupoff, wr, wc, fr, fq);
;         else if (mode == 2) store_tile<2>(acc, dst, ld, colbase, rowbase, nvalid, pos0, dupoff, wr, wc, fr, fq);
;         else store_tile<3>(acc, dst, ld, colbase, rowbase, nvalid, pos0, dupoff, wr, wc, fr, fq);
.Lrope_nd_b:
.LBB0_427:
	s_mov_b64 s[40:41], 0

; #define LAS __attribute__((address_space(3)))
; __device__ __forceinline__ void topk_phase(Frame& F) {
;     ...
;             LAS unsigned* dump = cbuf + 24 * 64 + lane; int ctot = 0;
; #pragma unroll
;             for (int j = 0; j < 129; ++j) { const unsigned kv = j < 128 ? key[j] : key128; const bool p = kv >= ts;
;                 const unsigned long long m = __ballot(p);
;                 const int pos = ctot + (int)__builtin_amdgcn_mbcnt_hi((unsigned)(m >> 32), __builtin_amdgcn_mbcnt_lo((unsigned)m, 0u));
;                 LAS unsigned* a = (p && pos < 24 * 64) ? cbuf + pos : dump; *a = kv; ctot += __popcll(m);
;                 if ((j & 7) == 7) __builtin_amdgcn_sched_barrier(0); }
.LBB0_955:
	s_mov_b32 s1, s93
	s_add_i32 s14, s93, 0x1800
	v_cmp_le_u32_e32 vcc, s0, v24
	s_nop 1
	s_bcnt1_i32_b64 s2, vcc
	v_mbcnt_lo_u32_b32 v0, vcc_lo, 0
	v_mbcnt_hi_u32_b32 v0, vcc_hi, v0
	v_lshl_add_u32 v0, v0, 2, s1
	v_min_u32_e32 v0, s14, v0
	v_cndmask_b32_e32 v0, v140, v0, vcc
	s_lshl2_add_u32 s1, s2, s1
	v_cmp_le_u32_e32 vcc, s0, v25
	ds_write_b32 v0, v24
	s_bcnt1_i32_b64 s2, vcc
	v_mbcnt_lo_u32_b32 v0, vcc_lo, 0
	v_mbcnt_hi_u32_b32 v0, vcc_hi, v0
	v_lshl_add_u32 v0, v0, 2, s1
	v_min_u32_e32 v0, s14, v0
	v_cndmask_b32_e32 v0, v140, v0, vcc
	s_lshl2_add_u32 s1, s2, s1
	v_cmp_le_u32_e32 vcc, s0, v26
	ds_write_b32 v0, v25
	s_bcnt1_i32_b64 s2, vcc
	v_mbcnt_lo_u32_b32 v0, vcc_lo, 0
	v_mbcnt_hi_u32_b32 v0, vcc_hi, v0
	v_lshl_add_u32 v0, v0, 2, s1
	v_min_u32_e32 v0, s14, v0
	v_cndmask_b32_e32 v0, v140, v0, vcc
	s_lshl2_add_u32 s1, s2, s1
	v_cmp_le_u32_e32 vcc, s0, v29
	ds_write_b32 v0, v26
	s_bcnt1_i32_b64 s2, vcc
	v_mbcnt_lo_u32_b32 v0, vcc_lo, 0
	v_mbcnt_hi_u32_b32 v0, vcc_hi, v0
	v_lshl_add_u32 v0, v0, 2, s1
	v_min_u32_e32 v0, s14, v0
	v_cndmask_b32_e32 v0, v140, v0, vcc
	s_lshl2_add_u32 s1, s2, s1
	v_cmp_le_u32_e32 vcc, s0, v28
	ds_write_b32 v0, v29
	s_bcnt1_i32_b64 s2, vcc
	v_mbcnt_lo_u32_b32 v0, vcc_lo, 0
	v_mbcnt_hi_u32_b32 v0, vcc_hi, v0
	v_lshl_add_u32 v0, v0, 2, s1
	v_min_u32_e32 v0, s14, v0
	v_cndmask_b32_e32 v0, v140, v0, vcc
	s_lshl2_add_u32 s1, s2, s1
	v_cmp_le_u32_e32 vcc, s0, v30
	ds_write_b32 v0, v28
	s_bcnt1_i32_b64 s2, vcc
	v_mbcnt_lo_u32_b32 v0, vcc_lo, 0
	v_mbcnt_hi_u32_b32 v0, vcc_hi, v0
	v_lshl_add_u32 v0, v0, 2, s1
	v_min_u32_e32 v0, s14, v0
	v_cndmask_b32_e32 v0, v140, v0, vcc
	s_lshl2_add_u32 s1, s2, s1
	v_cmp_le_u32_e32 vcc, s0, v31
	ds_write_b32 v0, v30
	s_bcnt1_i32_b64 s2, vcc
	v_mbcnt_lo_u32_b32 v0, vcc_lo, 0
	v_mbcnt_hi_u32_b32 v0, vcc_hi, v0
	v_lshl_add_u32 v0, v0, 2, s1
	v_min_u32_e32 v0, s14, v0
	v_cndmask_b32_e32 v0, v140, v0, vcc
	s_lshl2_add_u32 s1, s2, s1
	v_cmp_le_u32_e32 vcc, s0, v59
	ds_write_b32 v0, v31
	s_bcnt1_i32_b64 s2, vcc
	v_mbcnt_lo_u32_b32 v0, vcc_lo, 0
	v_mbcnt_hi_u32_b32 v0, vcc_hi, v0
	v_lshl_add_u32 v0, v0, 2, s1
	v_min_u32_e32 v0, s14, v0
	v_cndmask_b32_e32 v0, v140, v0, vcc
	s_lshl2_add_u32 s1, s2, s1
	v_cmp_le_u32_e32 vcc, s0, v58
	ds_write_b32 v0, v59
	s_bcnt1_i32_b64 s2, vcc
	v_mbcnt_lo_u32_b32 v0, vcc_lo, 0
	v_mbcnt_hi_u32_b32 v0, vcc_hi, v0
	v_lshl_add_u32 v0, v0, 2, s1
	v_min_u32_e32 v0, s14, v0
	v_cndmask_b32_e32 v0, v140, v0, vcc
	s_lshl2_add_u32 s1, s2, s1
	v_cmp_le_u32_e32 vcc, s0, v60
	ds_write_b32 v0, v58
	s_bcnt1_i32_b64 s2, vcc
	v_mbcnt_lo_u32_b32 v0, vcc_lo, 0
	v_mbcnt_hi_u32_b32 v0, vcc_hi, v0
	v_lshl_add_u32 v0, v0, 2, s1
	v_min_u32_e32 v0, s14, v0
	v_cndmask_b32_e32 v0, v140, v0, vcc
	s_lshl2_add_u32 s1, s2, s1
	v_cmp_le_u32_e32 vcc, s0, v63
	ds_write_b32 v0, v60
	s_bcnt1_i32_b64 s2, vcc
	v_mbcnt_lo_u32_b32 v0, vcc_lo, 0
	v_mbcnt_hi_u32_b32 v0, vcc_hi, v0
	v_lshl_add_u32 v0, v0, 2, s1
	v_min_u32_e32 v0, s14, v0
	v_cndmask_b32_e32 v0, v140, v0, vcc
	s_lshl2_add_u32 s1, s2, s1
	v_cmp_le_u32_e32 vcc, s0, v188
	ds_write_b32 v0, v63
	s_bcnt1_i32_b64 s2, vcc
	v_mbcnt_lo_u32_b32 v0, vcc_lo, 0
	v_mbcnt_hi_u32_b32 v0, vcc_hi, v0
	v_lshl_add_u32 v0, v0, 2, s1
	v_min_u32_e32 v0, s14, v0
	v_cndmask_b32_e32 v0, v140, v0, vcc
	s_lshl2_add_u32 s1, s2, s1
	v_cmp_le_u32_e32 vcc, s0, v187
	ds_write_b32 v0, v188
	s_bcnt1_i32_b64 s2, vcc
	v_mbcnt_lo_u32_b32 v0, vcc_lo, 0
	v_mbcnt_hi_u32_b32 v0, vcc_hi, v0
	v_lshl_add_u32 v0, v0, 2, s1
	v_min_u32_e32 v0, s14, v0
	v_cndmask_b32_e32 v0, v140, v0, vcc
	s_lshl2_add_u32 s1, s2, s1
	v_cmp_le_u32_e32 vcc, s0, v189
	ds_write_b32 v0, v187
	s_bcnt1_i32_b64 s2, vcc
	v_mbcnt_lo_u32_b32 v0, vcc_lo, 0
	v_mbcnt_hi_u32_b32 v0, vcc_hi, v0
	v_lshl_add_u32 v0, v0, 2, s1
	v_min_u32_e32 v0, s14, v0
	v_cndmask_b32_e32 v0, v140, v0, vcc
	s_lshl2_add_u32 s1, s2, s1
	v_cmp_le_u32_e32 vcc, s0, v192
	ds_write_b32 v0, v189
	s_bcnt1_i32_b64 s2, vcc
	v_mbcnt_lo_u32_b32 v0, vcc_lo, 0
	v_mbcnt_hi_u32_b32 v0, vcc_hi, v0
	v_lshl_add_u32 v0, v0, 2, s1
	v_min_u32_e32 v0, s14, v0
	v_cndmask_b32_e32 v0, v140, v0, vcc
	s_lshl2_add_u32 s1, s2, s1
	v_cmp_le_u32_e32 vcc, s0, v194
	ds_write_b32 v0, v192
	s_bcnt1_i32_b64 s2, vcc
	v_mbcnt_lo_u32_b32 v0, vcc_lo, 0
	v_mbcnt_hi_u32_b32 v0, vcc_hi, v0
	v_lshl_add_u32 v0, v0, 2, s1
	v_min_u32_e32 v0, s14, v0
	v_cndmask_b32_e32 v0, v140, v0, vcc
	s_lshl2_add_u32 s1, s2, s1
	v_cmp_le_u32_e32 vcc, s0, v193
	ds_write_b32 v0, v194
	s_bcnt1_i32_b64 s2, vcc
	v_mbcnt_lo_u32_b32 v0, vcc_lo, 0
	v_mbcnt_hi_u32_b32 v0, vcc_hi, v0
	v_lshl_add_u32 v0, v0, 2, s1
	v_min_u32_e32 v0, s14, v0
	v_cndmask_b32_e32 v0, v140, v0, vcc
	s_lshl2_add_u32 s1, s2, s1
	v_cmp_le_u32_e32 vcc, s0, v195
	ds_write_b32 v0, v193
	s_bcnt1_i32_b64 s2, vcc
	v_mbcnt_lo_u32_b32 v0, vcc_lo, 0
	v_mbcnt_hi_u32_b32 v0, vcc_hi, v0
	v_lshl_add_u32 v0, v0, 2, s1
	v_min_u32_e32 v0, s14, v0
	v_cndmask_b32_e32 v0, v140, v0, vcc
	s_lshl2_add_u32 s1, s2, s1
	v_cmp_le_u32_e32 vcc, s0, v197
	ds_write_b32 v0, v195
	s_bcnt1_i32_b64 s2, vcc
	v_mbcnt_lo_u32_b32 v0, vcc_lo, 0
	v_mbcnt_hi_u32_b32 v0, vcc_hi, v0
	v_lshl_add_u32 v0, v0, 2, s1
	v_min_u32_e32 v0, s14, v0
	v_cndmask_b32_e32 v0, v140, v0, vcc
	s_lshl2_add_u32 s1, s2, s1
	v_cmp_le_u32_e32 vcc, s0, v199
	ds_write_b32 v0, v197
	s_bcnt1_i32_b64 s2, vcc
	v_mbcnt_lo_u32_b32 v0, vcc_lo, 0
	v_mbcnt_hi_u32_b32 v0, vcc_hi, v0
	v_lshl_add_u32 v0, v0, 2, s1
	v_min_u32_e32 v0, s14, v0
	v_cndmask_b32_e32 v0, v140, v0, vcc
	s_lshl2_add_u32 s1, s2, s1
	v_cmp_le_u32_e32 vcc, s0, v196
	ds_write_b32 v0, v199
	s_bcnt1_i32_b64 s2, vcc
	v_mbcnt_lo_u32_b32 v0, vcc_lo, 0
	v_mbcnt_hi_u32_b32 v0, vcc_hi, v0
	v_lshl_add_u32 v0, v0, 2, s1
	v_min_u32_e32 v0, s14, v0
; #define LAS __attribute__((address_space(3)))
; __device__ __forceinline__ void topk_phase(Frame& F) {
;     ...
;             LAS unsigned* dump = cbuf + 24 * 64 + lane; int ctot = 0;
; #pragma unroll
;             for (int j = 0; j < 129; ++j) { const unsigned kv = j < 128 ? key[j] : key128; const bool p = kv >= ts;
;                 const unsigned long long m = __ballot(p);
;                 const int pos = ctot + (int)__builtin_amdgcn_mbcnt_hi((unsigned)(m >> 32), __builtin_amdgcn_mbcnt_lo((unsigned)m, 0u));
;                 LAS unsigned* a = (p && pos < 24 * 64) ? cbuf + pos : dump; *a = kv; ctot += __popcll(m);
;                 if ((j & 7) == 7) __builtin_amdgcn_sched_barrier(0); }
	v_cndmask_b32_e32 v0, v140, v0, vcc
	s_lshl2_add_u32 s1, s2, s1
	v_cmp_le_u32_e32 vcc, s0, v198
	ds_write_b32 v0, v196
	s_bcnt1_i32_b64 s2, vcc
	v_mbcnt_lo_u32_b32 v0, vcc_lo, 0
	v_mbcnt_hi_u32_b32 v0, vcc_hi, v0
	v_lshl_add_u32 v0, v0, 2, s1
	v_min_u32_e32 v0, s14, v0
	v_cndmask_b32_e32 v0, v140, v0, vcc
	s_lshl2_add_u32 s1, s2, s1
	v_cmp_le_u32_e32 vcc, s0, v201
	ds_write_b32 v0, v198
	s_bcnt1_i32_b64 s2, vcc
	v_mbcnt_lo_u32_b32 v0, vcc_lo, 0
	v_mbcnt_hi_u32_b32 v0, vcc_hi, v0
	v_lshl_add_u32 v0, v0, 2, s1
	v_min_u32_e32 v0, s14, v0
	v_cndmask_b32_e32 v0, v140, v0, vcc
	s_lshl2_add_u32 s1, s2, s1
	v_cmp_le_u32_e32 vcc, s0, v203
	ds_write_b32 v0, v201
	s_bcnt1_i32_b64 s2, vcc
	v_mbcnt_lo_u32_b32 v0, vcc_lo, 0
	v_mbcnt_hi_u32_b32 v0, vcc_hi, v0
	v_lshl_add_u32 v0, v0, 2, s1
	v_min_u32_e32 v0, s14, v0
	v_cndmask_b32_e32 v0, v140, v0, vcc
	s_lshl2_add_u32 s1, s2, s1
	v_cmp_le_u32_e32 vcc, s0, v200
	ds_write_b32 v0, v203
	s_bcnt1_i32_b64 s2, vcc
	v_mbcnt_lo_u32_b32 v0, vcc_lo, 0
	v_mbcnt_hi_u32_b32 v0, vcc_hi, v0
	v_lshl_add_u32 v0, v0, 2, s1
	v_min_u32_e32 v0, s14, v0
	v_cndmask_b32_e32 v0, v140, v0, vcc
	s_lshl2_add_u32 s1, s2, s1
	v_cmp_le_u32_e32 vcc, s0, v202
	ds_write_b32 v0, v200
	s_bcnt1_i32_b64 s2, vcc
	v_mbcnt_lo_u32_b32 v0, vcc_lo, 0
	v_mbcnt_hi_u32_b32 v0, vcc_hi, v0
	v_lshl_add_u32 v0, v0, 2, s1
	v_min_u32_e32 v0, s14, v0
	v_cndmask_b32_e32 v0, v140, v0, vcc
	s_lshl2_add_u32 s1, s2, s1
	v_cmp_le_u32_e32 vcc, s0, v205
	ds_write_b32 v0, v202
	s_bcnt1_i32_b64 s2, vcc
	v_mbcnt_lo_u32_b32 v0, vcc_lo, 0
	v_mbcnt_hi_u32_b32 v0, vcc_hi, v0
	v_lshl_add_u32 v0, v0, 2, s1
	v_min_u32_e32 v0, s14, v0
	v_cndmask_b32_e32 v0, v140, v0, vcc
	s_lshl2_add_u32 s1, s2, s1
	v_cmp_le_u32_e32 vcc, s0, v207
	ds_write_b32 v0, v205
	s_bcnt1_i32_b64 s2, vcc
	v_mbcnt_lo_u32_b32 v0, vcc_lo, 0
	v_mbcnt_hi_u32_b32 v0, vcc_hi, v0
	v_lshl_add_u32 v0, v0, 2, s1
	v_min_u32_e32 v0, s14, v0
	v_cndmask_b32_e32 v0, v140, v0, vcc
	s_lshl2_add_u32 s1, s2, s1
	v_cmp_le_u32_e32 vcc, s0, v204
	ds_write_b32 v0, v207
	s_bcnt1_i32_b64 s2, vcc
	v_mbcnt_lo_u32_b32 v0, vcc_lo, 0
	v_mbcnt_hi_u32_b32 v0, vcc_hi, v0
	v_lshl_add_u32 v0, v0, 2, s1
	v_min_u32_e32 v0, s14, v0
	v_cndmask_b32_e32 v0, v140, v0, vcc
	s_lshl2_add_u32 s1, s2, s1
	v_cmp_le_u32_e32 vcc, s0, v206
	ds_write_b32 v0, v204
	s_bcnt1_i32_b64 s2, vcc
	v_mbcnt_lo_u32_b32 v0, vcc_lo, 0
	v_mbcnt_hi_u32_b32 v0, vcc_hi, v0
	v_lshl_add_u32 v0, v0, 2, s1
	v_min_u32_e32 v0, s14, v0
	v_cndmask_b32_e32 v0, v140, v0, vcc
	s_lshl2_add_u32 s1, s2, s1
	v_cmp_le_u32_e32 vcc, s0, v208
	ds_write_b32 v0, v206
	s_bcnt1_i32_b64 s2, vcc
	v_mbcnt_lo_u32_b32 v0, vcc_lo, 0
	v_mbcnt_hi_u32_b32 v0, vcc_hi, v0
	v_lshl_add_u32 v0, v0, 2, s1
	v_min_u32_e32 v0, s14, v0
	v_cndmask_b32_e32 v0, v140, v0, vcc
	s_lshl2_add_u32 s1, s2, s1
	v_cmp_le_u32_e32 vcc, s0, v209
	ds_write_b32 v0, v208
	s_bcnt1_i32_b64 s2, vcc
	v_mbcnt_lo_u32_b32 v0, vcc_lo, 0
	v_mbcnt_hi_u32_b32 v0, vcc_hi, v0
	v_lshl_add_u32 v0, v0, 2, s1
	v_min_u32_e32 v0, s14, v0
	v_cndmask_b32_e32 v0, v140, v0, vcc
	s_lshl2_add_u32 s1, s2, s1
	v_cmp_le_u32_e32 vcc, s0, v32
	ds_write_b32 v0, v209
	s_bcnt1_i32_b64 s2, vcc
	v_mbcnt_lo_u32_b32 v0, vcc_lo, 0
	v_mbcnt_hi_u32_b32 v0, vcc_hi, v0
	v_lshl_add_u32 v0, v0, 2, s1
	v_min_u32_e32 v0, s14, v0
	v_cndmask_b32_e32 v0, v140, v0, vcc
	s_lshl2_add_u32 s1, s2, s1
	v_cmp_le_u32_e32 vcc, s0, v33
	ds_write_b32 v0, v32
	s_bcnt1_i32_b64 s2, vcc
	v_mbcnt_lo_u32_b32 v0, vcc_lo, 0
	v_mbcnt_hi_u32_b32 v0, vcc_hi, v0
	v_lshl_add_u32 v0, v0, 2, s1
	v_min_u32_e32 v0, s14, v0
	v_cndmask_b32_e32 v0, v140, v0, vcc
	s_lshl2_add_u32 s1, s2, s1
	v_cmp_le_u32_e32 vcc, s0, v34
	ds_write_b32 v0, v33
	s_bcnt1_i32_b64 s2, vcc
	v_mbcnt_lo_u32_b32 v0, vcc_lo, 0
	v_mbcnt_hi_u32_b32 v0, vcc_hi, v0
	v_lshl_add_u32 v0, v0, 2, s1
	v_min_u32_e32 v0, s14, v0
	v_cndmask_b32_e32 v0, v140, v0, vcc
	s_lshl2_add_u32 s1, s2, s1
	v_cmp_le_u32_e32 vcc, s0, v35
	ds_write_b32 v0, v34
	s_bcnt1_i32_b64 s2, vcc
	v_mbcnt_lo_u32_b32 v0, vcc_lo, 0
	v_mbcnt_hi_u32_b32 v0, vcc_hi, v0
	v_lshl_add_u32 v0, v0, 2, s1
	v_min_u32_e32 v0, s14, v0
	v_cndmask_b32_e32 v0, v140, v0, vcc
	s_lshl2_add_u32 s1, s2, s1
	v_cmp_le_u32_e32 vcc, s0, v36
	ds_write_b32 v0, v35
	s_bcnt1_i32_b64 s2, vcc
	v_mbcnt_lo_u32_b32 v0, vcc_lo, 0
	v_mbcnt_hi_u32_b32 v0, vcc_hi, v0
	v_lshl_add_u32 v0, v0, 2, s1
	v_min_u32_e32 v0, s14, v0
	v_cndmask_b32_e32 v0, v140, v0, vcc
	s_lshl2_add_u32 s1, s2, s1
	v_cmp_le_u32_e32 vcc, s0, v37
	ds_write_b32 v0, v36
	s_bcnt1_i32_b64 s2, vcc
	v_mbcnt_lo_u32_b32 v0, vcc_lo, 0
	v_mbcnt_hi_u32_b32 v0, vcc_hi, v0
	v_lshl_add_u32 v0, v0, 2, s1
	v_min_u32_e32 v0, s14, v0
	v_cndmask_b32_e32 v0, v140, v0, vcc
	s_lshl2_add_u32 s1, s2, s1
	v_cmp_le_u32_e32 vcc, s0, v38
	ds_write_b32 v0, v37
	s_bcnt1_i32_b64 s2, vcc
	v_mbcnt_lo_u32_b32 v0, vcc_lo, 0
	v_mbcnt_hi_u32_b32 v0, vcc_hi, v0
	v_lshl_add_u32 v0, v0, 2, s1
	v_min_u32_e32 v0, s14, v0
	v_cndmask_b32_e32 v0, v140, v0, vcc
	s_lshl2_add_u32 s1, s2, s1
	v_cmp_le_u32_e32 vcc, s0, v39
	ds_write_b32 v0, v38
	s_bcnt1_i32_b64 s2, vcc
	v_mbcnt_lo_u32_b32 v0, vcc_lo, 0
	v_mbcnt_hi_u32_b32 v0, vcc_hi, v0
	v_lshl_add_u32 v0, v0, 2, s1
	v_min_u32_e32 v0, s14, v0
	v_cndmask_b32_e32 v0, v140, v0, vcc
	s_lshl2_add_u32 s1, s2, s1
	v_cmp_le_u32_e32 vcc, s0, v40
	ds_write_b32 v0, v39
	s_bcnt1_i32_b64 s2, vcc
	v_mbcnt_lo_u32_b32 v0, vcc_lo, 0
	v_mbcnt_hi_u32_b32 v0, vcc_hi, v0
	v_lshl_add_u32 v0, v0, 2, s1
	v_min_u32_e32 v0, s14, v0
	v_cndmask_b32_e32 v0, v140, v0, vcc
	s_lshl2_add_u32 s1, s2, s1
	v_cmp_le_u32_e32 vcc, s0, v41
	ds_write_b32 v0, v40
	s_bcnt1_i32_b64 s2, vcc
	v_mbcnt_lo_u32_b32 v0, vcc_lo, 0
	v_mbcnt_hi_u32_b32 v0, vcc_hi, v0
	v_lshl_add_u32 v0, v0, 2, s1
; #define LAS __attribute__((address_space(3)))
; __device__ __forceinline__ void topk_phase(Frame& F) {
;     ...
;             LAS unsigned* dump = cbuf + 24 * 64 + lane; int ctot = 0;
; #pragma unroll
;             for (int j = 0; j < 129; ++j) { const unsigned kv = j < 128 ? key[j] : key128; const bool p = kv >= ts;
;                 const unsigned long long m = __ballot(p);
;                 const int pos = ctot + (int)__builtin_amdgcn_mbcnt_hi((unsigned)(m >> 32), __builtin_amdgcn_mbcnt_lo((unsigned)m, 0u));
;                 LAS unsigned* a = (p && pos < 24 * 64) ? cbuf + pos : dump; *a = kv; ctot += __popcll(m);
;                 if ((j & 7) == 7) __builtin_amdgcn_sched_barrier(0); }
	v_min_u32_e32 v0, s14, v0
	v_cndmask_b32_e32 v0, v140, v0, vcc
	s_lshl2_add_u32 s1, s2, s1
	v_cmp_le_u32_e32 vcc, s0, v42
	ds_write_b32 v0, v41
	s_bcnt1_i32_b64 s2, vcc
	v_mbcnt_lo_u32_b32 v0, vcc_lo, 0
	v_mbcnt_hi_u32_b32 v0, vcc_hi, v0
	v_lshl_add_u32 v0, v0, 2, s1
	v_min_u32_e32 v0, s14, v0
	v_cndmask_b32_e32 v0, v140, v0, vcc
	s_lshl2_add_u32 s1, s2, s1
	v_cmp_le_u32_e32 vcc, s0, v43
	ds_write_b32 v0, v42
	s_bcnt1_i32_b64 s2, vcc
	v_mbcnt_lo_u32_b32 v0, vcc_lo, 0
	v_mbcnt_hi_u32_b32 v0, vcc_hi, v0
	v_lshl_add_u32 v0, v0, 2, s1
	v_min_u32_e32 v0, s14, v0
	v_cndmask_b32_e32 v0, v140, v0, vcc
	s_lshl2_add_u32 s1, s2, s1
	v_cmp_le_u32_e32 vcc, s0, v44
	ds_write_b32 v0, v43
	s_bcnt1_i32_b64 s2, vcc
	v_mbcnt_lo_u32_b32 v0, vcc_lo, 0
	v_mbcnt_hi_u32_b32 v0, vcc_hi, v0
	v_lshl_add_u32 v0, v0, 2, s1
	v_min_u32_e32 v0, s14, v0
	v_cndmask_b32_e32 v0, v140, v0, vcc
	s_lshl2_add_u32 s1, s2, s1
	v_cmp_le_u32_e32 vcc, s0, v45
	ds_write_b32 v0, v44
	s_bcnt1_i32_b64 s2, vcc
	v_mbcnt_lo_u32_b32 v0, vcc_lo, 0
	v_mbcnt_hi_u32_b32 v0, vcc_hi, v0
	v_lshl_add_u32 v0, v0, 2, s1
	v_min_u32_e32 v0, s14, v0
	v_cndmask_b32_e32 v0, v140, v0, vcc
	s_lshl2_add_u32 s1, s2, s1
	v_cmp_le_u32_e32 vcc, s0, v46
	ds_write_b32 v0, v45
	s_bcnt1_i32_b64 s2, vcc
	v_mbcnt_lo_u32_b32 v0, vcc_lo, 0
	v_mbcnt_hi_u32_b32 v0, vcc_hi, v0
	v_lshl_add_u32 v0, v0, 2, s1
	v_min_u32_e32 v0, s14, v0
	v_cndmask_b32_e32 v0, v140, v0, vcc
	s_lshl2_add_u32 s1, s2, s1
	v_cmp_le_u32_e32 vcc, s0, v47
	ds_write_b32 v0, v46
	s_bcnt1_i32_b64 s2, vcc
	v_mbcnt_lo_u32_b32 v0, vcc_lo, 0
	v_mbcnt_hi_u32_b32 v0, vcc_hi, v0
	v_lshl_add_u32 v0, v0, 2, s1
	v_min_u32_e32 v0, s14, v0
	v_cndmask_b32_e32 v0, v140, v0, vcc
	s_lshl2_add_u32 s1, s2, s1
	v_cmp_le_u32_e32 vcc, s0, v48
	ds_write_b32 v0, v47
	s_bcnt1_i32_b64 s2, vcc
	v_mbcnt_lo_u32_b32 v0, vcc_lo, 0
	v_mbcnt_hi_u32_b32 v0, vcc_hi, v0
	v_lshl_add_u32 v0, v0, 2, s1
	v_min_u32_e32 v0, s14, v0
	v_cndmask_b32_e32 v0, v140, v0, vcc
	s_lshl2_add_u32 s1, s2, s1
	v_cmp_le_u32_e32 vcc, s0, v49
	ds_write_b32 v0, v48
	s_bcnt1_i32_b64 s2, vcc
	v_mbcnt_lo_u32_b32 v0, vcc_lo, 0
	v_mbcnt_hi_u32_b32 v0, vcc_hi, v0
	v_lshl_add_u32 v0, v0, 2, s1
	v_min_u32_e32 v0, s14, v0
	v_cndmask_b32_e32 v0, v140, v0, vcc
	s_lshl2_add_u32 s1, s2, s1
	v_cmp_le_u32_e32 vcc, s0, v50
	ds_write_b32 v0, v49
	s_bcnt1_i32_b64 s2, vcc
	v_mbcnt_lo_u32_b32 v0, vcc_lo, 0
	v_mbcnt_hi_u32_b32 v0, vcc_hi, v0
	v_lshl_add_u32 v0, v0, 2, s1
	v_min_u32_e32 v0, s14, v0
	v_cndmask_b32_e32 v0, v140, v0, vcc
	s_lshl2_add_u32 s1, s2, s1
	v_cmp_le_u32_e32 vcc, s0, v51
	ds_write_b32 v0, v50
	s_bcnt1_i32_b64 s2, vcc
	v_mbcnt_lo_u32_b32 v0, vcc_lo, 0
	v_mbcnt_hi_u32_b32 v0, vcc_hi, v0
	v_lshl_add_u32 v0, v0, 2, s1
	v_min_u32_e32 v0, s14, v0
	v_cndmask_b32_e32 v0, v140, v0, vcc
	s_lshl2_add_u32 s1, s2, s1
	v_cmp_le_u32_e32 vcc, s0, v52
	ds_write_b32 v0, v51
	s_bcnt1_i32_b64 s2, vcc
	v_mbcnt_lo_u32_b32 v0, vcc_lo, 0
	v_mbcnt_hi_u32_b32 v0, vcc_hi, v0
	v_lshl_add_u32 v0, v0, 2, s1
	v_min_u32_e32 v0, s14, v0
	v_cndmask_b32_e32 v0, v140, v0, vcc
	s_lshl2_add_u32 s1, s2, s1
	v_cmp_le_u32_e32 vcc, s0, v53
	ds_write_b32 v0, v52
	s_bcnt1_i32_b64 s2, vcc
	v_mbcnt_lo_u32_b32 v0, vcc_lo, 0
	v_mbcnt_hi_u32_b32 v0, vcc_hi, v0
	v_lshl_add_u32 v0, v0, 2, s1
	v_min_u32_e32 v0, s14, v0
	v_cndmask_b32_e32 v0, v140, v0, vcc
	s_lshl2_add_u32 s1, s2, s1
	v_cmp_le_u32_e32 vcc, s0, v54
	ds_write_b32 v0, v53
	s_bcnt1_i32_b64 s2, vcc
	v_mbcnt_lo_u32_b32 v0, vcc_lo, 0
	v_mbcnt_hi_u32_b32 v0, vcc_hi, v0
	v_lshl_add_u32 v0, v0, 2, s1
	v_min_u32_e32 v0, s14, v0
	v_cndmask_b32_e32 v0, v140, v0, vcc
	s_lshl2_add_u32 s1, s2, s1
	v_cmp_le_u32_e32 vcc, s0, v55
	ds_write_b32 v0, v54
	s_bcnt1_i32_b64 s2, vcc
	v_mbcnt_lo_u32_b32 v0, vcc_lo, 0
	v_mbcnt_hi_u32_b32 v0, vcc_hi, v0
	v_lshl_add_u32 v0, v0, 2, s1
	v_min_u32_e32 v0, s14, v0
	v_cndmask_b32_e32 v0, v140, v0, vcc
	s_lshl2_add_u32 s1, s2, s1
	v_cmp_le_u32_e32 vcc, s0, v56
	ds_write_b32 v0, v55
	s_bcnt1_i32_b64 s2, vcc
	v_mbcnt_lo_u32_b32 v0, vcc_lo, 0
	v_mbcnt_hi_u32_b32 v0, vcc_hi, v0
	v_lshl_add_u32 v0, v0, 2, s1
	v_min_u32_e32 v0, s14, v0
	v_cndmask_b32_e32 v0, v140, v0, vcc
	s_lshl2_add_u32 s1, s2, s1
	v_cmp_le_u32_e32 vcc, s0, v57
	ds_write_b32 v0, v56
	s_bcnt1_i32_b64 s2, vcc
	v_mbcnt_lo_u32_b32 v0, vcc_lo, 0
	v_mbcnt_hi_u32_b32 v0, vcc_hi, v0
	v_lshl_add_u32 v0, v0, 2, s1
	v_min_u32_e32 v0, s14, v0
	v_cndmask_b32_e32 v0, v140, v0, vcc
	s_lshl2_add_u32 s1, s2, s1
	v_cmp_le_u32_e32 vcc, s0, v61
	ds_write_b32 v0, v57
	s_bcnt1_i32_b64 s2, vcc
	v_mbcnt_lo_u32_b32 v0, vcc_lo, 0
	v_mbcnt_hi_u32_b32 v0, vcc_hi, v0
	v_lshl_add_u32 v0, v0, 2, s1
	v_min_u32_e32 v0, s14, v0
	v_cndmask_b32_e32 v0, v140, v0, vcc
	s_lshl2_add_u32 s1, s2, s1
	v_cmp_le_u32_e32 vcc, s0, v62
	ds_write_b32 v0, v61
	s_bcnt1_i32_b64 s2, vcc
	v_mbcnt_lo_u32_b32 v0, vcc_lo, 0
	v_mbcnt_hi_u32_b32 v0, vcc_hi, v0
	v_lshl_add_u32 v0, v0, 2, s1
	v_min_u32_e32 v0, s14, v0
	v_cndmask_b32_e32 v0, v140, v0, vcc
	s_lshl2_add_u32 s1, s2, s1
	v_cmp_le_u32_e32 vcc, s0, v134
	ds_write_b32 v0, v62
	s_bcnt1_i32_b64 s2, vcc
	v_mbcnt_lo_u32_b32 v0, vcc_lo, 0
	v_mbcnt_hi_u32_b32 v0, vcc_hi, v0
	v_lshl_add_u32 v0, v0, 2, s1
	v_min_u32_e32 v0, s14, v0
	v_cndmask_b32_e32 v0, v140, v0, vcc
	s_lshl2_add_u32 s1, s2, s1
	v_cmp_le_u32_e32 vcc, s0, v135
	ds_write_b32 v0, v134
	s_bcnt1_i32_b64 s2, vcc
	v_mbcnt_lo_u32_b32 v0, vcc_lo, 0
	v_mbcnt_hi_u32_b32 v0, vcc_hi, v0
	v_lshl_add_u32 v0, v0, 2, s1
	v_min_u32_e32 v0, s14, v0
	v_cndmask_b32_e32 v0, v140, v0, vcc
	s_lshl2_add_u32 s1, s2, s1
	v_cmp_le_u32_e32 vcc, s0, v190
	ds_write_b32 v0, v135
	s_bcnt1_i32_b64 s2, vcc
	v_mbcnt_lo_u32_b32 v0, vcc_lo, 0
	v_mbcnt_hi_u32_b32 v0, vcc_hi, v0
	v_lshl_add_u32 v0, v0, 2, s1
; #define LAS __attribute__((address_space(3)))
; __device__ __forceinline__ void topk_phase(Frame& F) {
;     ...
;             for (int j = 0; j < 129; ++j) { const unsigned kv = j < 128 ? key[j] : key128; const bool p = kv >= ts;
;                 const unsigned long long m = __ballot(p);
;                 const int pos = ctot + (int)__builtin_amdgcn_mbcnt_hi((unsigned)(m >> 32), __builtin_amdgcn_mbcnt_lo((unsigned)m, 0u));
;                 LAS unsigned* a = (p && pos < 24 * 64) ? cbuf + pos : dump; *a = kv; ctot += __popcll(m);
;                 if ((j & 7) == 7) __builtin_amdgcn_sched_barrier(0); }
	v_min_u32_e32 v0, s14, v0
	v_cndmask_b32_e32 v0, v140, v0, vcc
	s_lshl2_add_u32 s1, s2, s1
	v_cmp_le_u32_e32 vcc, s0, v191
	ds_write_b32 v0, v190
	s_bcnt1_i32_b64 s2, vcc
	v_mbcnt_lo_u32_b32 v0, vcc_lo, 0
	v_mbcnt_hi_u32_b32 v0, vcc_hi, v0
	v_lshl_add_u32 v0, v0, 2, s1
	v_min_u32_e32 v0, s14, v0
	v_cndmask_b32_e32 v0, v140, v0, vcc
	s_lshl2_add_u32 s1, s2, s1
	v_cmp_le_u32_e32 vcc, s0, v64
	ds_write_b32 v0, v191
	s_bcnt1_i32_b64 s2, vcc
	v_mbcnt_lo_u32_b32 v0, vcc_lo, 0
	v_mbcnt_hi_u32_b32 v0, vcc_hi, v0
	v_lshl_add_u32 v0, v0, 2, s1
	v_min_u32_e32 v0, s14, v0
	v_cndmask_b32_e32 v0, v140, v0, vcc
	s_lshl2_add_u32 s1, s2, s1
	v_cmp_le_u32_e32 vcc, s0, v65
	ds_write_b32 v0, v64
	s_bcnt1_i32_b64 s2, vcc
	v_mbcnt_lo_u32_b32 v0, vcc_lo, 0
	v_mbcnt_hi_u32_b32 v0, vcc_hi, v0
	v_lshl_add_u32 v0, v0, 2, s1
	v_min_u32_e32 v0, s14, v0
	v_cndmask_b32_e32 v0, v140, v0, vcc
	s_lshl2_add_u32 s1, s2, s1
	v_cmp_le_u32_e32 vcc, s0, v66
	ds_write_b32 v0, v65
	s_bcnt1_i32_b64 s2, vcc
	v_mbcnt_lo_u32_b32 v0, vcc_lo, 0
	v_mbcnt_hi_u32_b32 v0, vcc_hi, v0
	v_lshl_add_u32 v0, v0, 2, s1
	v_min_u32_e32 v0, s14, v0
	v_cndmask_b32_e32 v0, v140, v0, vcc
	s_lshl2_add_u32 s1, s2, s1
	v_cmp_le_u32_e32 vcc, s0, v67
	ds_write_b32 v0, v66
	s_bcnt1_i32_b64 s2, vcc
	v_mbcnt_lo_u32_b32 v0, vcc_lo, 0
	v_mbcnt_hi_u32_b32 v0, vcc_hi, v0
	v_lshl_add_u32 v0, v0, 2, s1
	v_min_u32_e32 v0, s14, v0
	v_cndmask_b32_e32 v0, v140, v0, vcc
	s_lshl2_add_u32 s1, s2, s1
	v_cmp_le_u32_e32 vcc, s0, v68
	ds_write_b32 v0, v67
	s_bcnt1_i32_b64 s2, vcc
	v_mbcnt_lo_u32_b32 v0, vcc_lo, 0
	v_mbcnt_hi_u32_b32 v0, vcc_hi, v0
	v_lshl_add_u32 v0, v0, 2, s1
	v_min_u32_e32 v0, s14, v0
	v_cndmask_b32_e32 v0, v140, v0, vcc
	s_lshl2_add_u32 s1, s2, s1
	v_cmp_le_u32_e32 vcc, s0, v69
	ds_write_b32 v0, v68
	s_bcnt1_i32_b64 s2, vcc
	v_mbcnt_lo_u32_b32 v0, vcc_lo, 0
	v_mbcnt_hi_u32_b32 v0, vcc_hi, v0
	v_lshl_add_u32 v0, v0, 2, s1
	v_min_u32_e32 v0, s14, v0
	v_cndmask_b32_e32 v0, v140, v0, vcc
	s_lshl2_add_u32 s1, s2, s1
	v_cmp_le_u32_e32 vcc, s0, v70
	ds_write_b32 v0, v69
	s_bcnt1_i32_b64 s2, vcc
	v_mbcnt_lo_u32_b32 v0, vcc_lo, 0
	v_mbcnt_hi_u32_b32 v0, vcc_hi, v0
	v_lshl_add_u32 v0, v0, 2, s1
	v_min_u32_e32 v0, s14, v0
	v_cndmask_b32_e32 v0, v140, v0, vcc
	s_lshl2_add_u32 s1, s2, s1
	v_cmp_le_u32_e32 vcc, s0, v71
	ds_write_b32 v0, v70
	s_bcnt1_i32_b64 s2, vcc
	v_mbcnt_lo_u32_b32 v0, vcc_lo, 0
	v_mbcnt_hi_u32_b32 v0, vcc_hi, v0
	v_lshl_add_u32 v0, v0, 2, s1
	v_min_u32_e32 v0, s14, v0
	v_cndmask_b32_e32 v0, v140, v0, vcc
	s_lshl2_add_u32 s1, s2, s1
	v_cmp_le_u32_e32 vcc, s0, v76
	ds_write_b32 v0, v71
	s_bcnt1_i32_b64 s2, vcc
	v_mbcnt_lo_u32_b32 v0, vcc_lo, 0
	v_mbcnt_hi_u32_b32 v0, vcc_hi, v0
	v_lshl_add_u32 v0, v0, 2, s1
	v_min_u32_e32 v0, s14, v0
	v_cndmask_b32_e32 v0, v140, v0, vcc
	s_lshl2_add_u32 s1, s2, s1
	v_cmp_le_u32_e32 vcc, s0, v77
	ds_write_b32 v0, v76
	s_bcnt1_i32_b64 s2, vcc
	v_mbcnt_lo_u32_b32 v0, vcc_lo, 0
	v_mbcnt_hi_u32_b32 v0, vcc_hi, v0
	v_lshl_add_u32 v0, v0, 2, s1
	v_min_u32_e32 v0, s14, v0
	v_cndmask_b32_e32 v0, v140, v0, vcc
	s_lshl2_add_u32 s1, s2, s1
	v_cmp_le_u32_e32 vcc, s0, v78
	ds_write_b32 v0, v77
	s_bcnt1_i32_b64 s2, vcc
	v_mbcnt_lo_u32_b32 v0, vcc_lo, 0
	v_mbcnt_hi_u32_b32 v0, vcc_hi, v0
	v_lshl_add_u32 v0, v0, 2, s1
	v_min_u32_e32 v0, s14, v0
	v_cndmask_b32_e32 v0, v140, v0, vcc
	s_lshl2_add_u32 s1, s2, s1
	v_cmp_le_u32_e32 vcc, s0, v79
	ds_write_b32 v0, v78
	s_bcnt1_i32_b64 s2, vcc
	v_mbcnt_lo_u32_b32 v0, vcc_lo, 0
	v_mbcnt_hi_u32_b32 v0, vcc_hi, v0
	v_lshl_add_u32 v0, v0, 2, s1
	v_min_u32_e32 v0, s14, v0
	v_cndmask_b32_e32 v0, v140, v0, vcc
	s_lshl2_add_u32 s1, s2, s1
	v_cmp_le_u32_e32 vcc, s0, v80
	ds_write_b32 v0, v79
	s_bcnt1_i32_b64 s2, vcc
	v_mbcnt_lo_u32_b32 v0, vcc_lo, 0
	v_mbcnt_hi_u32_b32 v0, vcc_hi, v0
	v_lshl_add_u32 v0, v0, 2, s1
	v_min_u32_e32 v0, s14, v0
	v_cndmask_b32_e32 v0, v140, v0, vcc
	s_lshl2_add_u32 s1, s2, s1
	v_cmp_le_u32_e32 vcc, s0, v81
	ds_write_b32 v0, v80
	s_bcnt1_i32_b64 s2, vcc
	v_mbcnt_lo_u32_b32 v0, vcc_lo, 0
	v_mbcnt_hi_u32_b32 v0, vcc_hi, v0
	v_lshl_add_u32 v0, v0, 2, s1
	v_min_u32_e32 v0, s14, v0
	v_cndmask_b32_e32 v0, v140, v0, vcc
	s_lshl2_add_u32 s1, s2, s1
	v_cmp_le_u32_e32 vcc, s0, v82
	ds_write_b32 v0, v81
	s_bcnt1_i32_b64 s2, vcc
	v_mbcnt_lo_u32_b32 v0, vcc_lo, 0
	v_mbcnt_hi_u32_b32 v0, vcc_hi, v0
	v_lshl_add_u32 v0, v0, 2, s1
	v_min_u32_e32 v0, s14, v0
	v_cndmask_b32_e32 v0, v140, v0, vcc
	s_lshl2_add_u32 s1, s2, s1
	v_cmp_le_u32_e32 vcc, s0, v83
	ds_write_b32 v0, v82
	s_bcnt1_i32_b64 s2, vcc
	v_mbcnt_lo_u32_b32 v0, vcc_lo, 0
	v_mbcnt_hi_u32_b32 v0, vcc_hi, v0
	v_lshl_add_u32 v0, v0, 2, s1
	v_min_u32_e32 v0, s14, v0
	v_cndmask_b32_e32 v0, v140, v0, vcc
	s_lshl2_add_u32 s1, s2, s1
	v_cmp_le_u32_e32 vcc, s0, v84
	ds_write_b32 v0, v83
	s_bcnt1_i32_b64 s2, vcc
	v_mbcnt_lo_u32_b32 v0, vcc_lo, 0
	v_mbcnt_hi_u32_b32 v0, vcc_hi, v0
	v_lshl_add_u32 v0, v0, 2, s1
	v_min_u32_e32 v0, s14, v0
	v_cndmask_b32_e32 v0, v140, v0, vcc
	s_lshl2_add_u32 s1, s2, s1
	v_cmp_le_u32_e32 vcc, s0, v85
	ds_write_b32 v0, v84
	s_bcnt1_i32_b64 s2, vcc
	v_mbcnt_lo_u32_b32 v0, vcc_lo, 0
	v_mbcnt_hi_u32_b32 v0, vcc_hi, v0
	v_lshl_add_u32 v0, v0, 2, s1
	v_min_u32_e32 v0, s14, v0
	v_cndmask_b32_e32 v0, v140, v0, vcc
	s_lshl2_add_u32 s1, s2, s1
	v_cmp_le_u32_e32 vcc, s0, v86
	ds_write_b32 v0, v85
	s_bcnt1_i32_b64 s2, vcc
	v_mbcnt_lo_u32_b32 v0, vcc_lo, 0
	v_mbcnt_hi_u32_b32 v0, vcc_hi, v0
	v_lshl_add_u32 v0, v0, 2, s1
	v_min_u32_e32 v0, s14, v0
	v_cndmask_b32_e32 v0, v140, v0, vcc
	s_lshl2_add_u32 s1, s2, s1
	v_cmp_le_u32_e32 vcc, s0, v87
	ds_write_b32 v0, v86
	s_bcnt1_i32_b64 s2, vcc
	v_mbcnt_lo_u32_b32 v0, vcc_lo, 0
	v_mbcnt_hi_u32_b32 v0, vcc_hi, v0
	v_lshl_add_u32 v0, v0, 2, s1
; #define LAS __attribute__((address_space(3)))
; __device__ __forceinline__ void topk_phase(Frame& F) {
;     ...
;             for (int j = 0; j < 129; ++j) { const unsigned kv = j < 128 ? key[j] : key128; const bool p = kv >= ts;
;                 const unsigned long long m = __ballot(p);
;                 const int pos = ctot + (int)__builtin_amdgcn_mbcnt_hi((unsigned)(m >> 32), __builtin_amdgcn_mbcnt_lo((unsigned)m, 0u));
;                 LAS unsigned* a = (p && pos < 24 * 64) ? cbuf + pos : dump; *a = kv; ctot += __popcll(m);
;                 if ((j & 7) == 7) __builtin_amdgcn_sched_barrier(0); }
	v_min_u32_e32 v0, s14, v0
	v_cndmask_b32_e32 v0, v140, v0, vcc
	s_lshl2_add_u32 s1, s2, s1
	v_cmp_le_u32_e32 vcc, s0, v88
	ds_write_b32 v0, v87
	s_bcnt1_i32_b64 s2, vcc
	v_mbcnt_lo_u32_b32 v0, vcc_lo, 0
	v_mbcnt_hi_u32_b32 v0, vcc_hi, v0
	v_lshl_add_u32 v0, v0, 2, s1
	v_min_u32_e32 v0, s14, v0
	v_cndmask_b32_e32 v0, v140, v0, vcc
	s_lshl2_add_u32 s1, s2, s1
	v_cmp_le_u32_e32 vcc, s0, v89
	ds_write_b32 v0, v88
	s_bcnt1_i32_b64 s2, vcc
	v_mbcnt_lo_u32_b32 v0, vcc_lo, 0
	v_mbcnt_hi_u32_b32 v0, vcc_hi, v0
	v_lshl_add_u32 v0, v0, 2, s1
	v_min_u32_e32 v0, s14, v0
	v_cndmask_b32_e32 v0, v140, v0, vcc
	s_lshl2_add_u32 s1, s2, s1
	v_cmp_le_u32_e32 vcc, s0, v90
	ds_write_b32 v0, v89
	s_bcnt1_i32_b64 s2, vcc
	v_mbcnt_lo_u32_b32 v0, vcc_lo, 0
	v_mbcnt_hi_u32_b32 v0, vcc_hi, v0
	v_lshl_add_u32 v0, v0, 2, s1
	v_min_u32_e32 v0, s14, v0
	v_cndmask_b32_e32 v0, v140, v0, vcc
	s_lshl2_add_u32 s1, s2, s1
	v_cmp_le_u32_e32 vcc, s0, v91
	ds_write_b32 v0, v90
	s_bcnt1_i32_b64 s2, vcc
	v_mbcnt_lo_u32_b32 v0, vcc_lo, 0
	v_mbcnt_hi_u32_b32 v0, vcc_hi, v0
	v_lshl_add_u32 v0, v0, 2, s1
	v_min_u32_e32 v0, s14, v0
	v_cndmask_b32_e32 v0, v140, v0, vcc
	s_lshl2_add_u32 s1, s2, s1
	v_cmp_le_u32_e32 vcc, s0, v92
	ds_write_b32 v0, v91
	s_bcnt1_i32_b64 s2, vcc
	v_mbcnt_lo_u32_b32 v0, vcc_lo, 0
	v_mbcnt_hi_u32_b32 v0, vcc_hi, v0
	v_lshl_add_u32 v0, v0, 2, s1
	v_min_u32_e32 v0, s14, v0
	v_cndmask_b32_e32 v0, v140, v0, vcc
	s_lshl2_add_u32 s1, s2, s1
	v_cmp_le_u32_e32 vcc, s0, v93
	ds_write_b32 v0, v92
	s_bcnt1_i32_b64 s2, vcc
	v_mbcnt_lo_u32_b32 v0, vcc_lo, 0
	v_mbcnt_hi_u32_b32 v0, vcc_hi, v0
	v_lshl_add_u32 v0, v0, 2, s1
	v_min_u32_e32 v0, s14, v0
	v_cndmask_b32_e32 v0, v140, v0, vcc
	s_lshl2_add_u32 s1, s2, s1
	v_cmp_le_u32_e32 vcc, s0, v94
	ds_write_b32 v0, v93
	s_bcnt1_i32_b64 s2, vcc
	v_mbcnt_lo_u32_b32 v0, vcc_lo, 0
	v_mbcnt_hi_u32_b32 v0, vcc_hi, v0
	v_lshl_add_u32 v0, v0, 2, s1
	v_min_u32_e32 v0, s14, v0
	v_cndmask_b32_e32 v0, v140, v0, vcc
	s_lshl2_add_u32 s1, s2, s1
	v_cmp_le_u32_e32 vcc, s0, v95
	ds_write_b32 v0, v94
	s_bcnt1_i32_b64 s2, vcc
	v_mbcnt_lo_u32_b32 v0, vcc_lo, 0
	v_mbcnt_hi_u32_b32 v0, vcc_hi, v0
	v_lshl_add_u32 v0, v0, 2, s1
	v_min_u32_e32 v0, s14, v0
	v_cndmask_b32_e32 v0, v140, v0, vcc
	s_lshl2_add_u32 s1, s2, s1
	v_cmp_le_u32_e32 vcc, s0, v96
	ds_write_b32 v0, v95
	s_bcnt1_i32_b64 s2, vcc
	v_mbcnt_lo_u32_b32 v0, vcc_lo, 0
	v_mbcnt_hi_u32_b32 v0, vcc_hi, v0
	v_lshl_add_u32 v0, v0, 2, s1
	v_min_u32_e32 v0, s14, v0
	v_cndmask_b32_e32 v0, v140, v0, vcc
	s_lshl2_add_u32 s1, s2, s1
	v_cmp_le_u32_e32 vcc, s0, v97
	ds_write_b32 v0, v96
	s_bcnt1_i32_b64 s2, vcc
	v_mbcnt_lo_u32_b32 v0, vcc_lo, 0
	v_mbcnt_hi_u32_b32 v0, vcc_hi, v0
	v_lshl_add_u32 v0, v0, 2, s1
	v_min_u32_e32 v0, s14, v0
	v_cndmask_b32_e32 v0, v140, v0, vcc
	s_lshl2_add_u32 s1, s2, s1
	v_cmp_le_u32_e32 vcc, s0, v98
	ds_write_b32 v0, v97
	s_bcnt1_i32_b64 s2, vcc
	v_mbcnt_lo_u32_b32 v0, vcc_lo, 0
	v_mbcnt_hi_u32_b32 v0, vcc_hi, v0
	v_lshl_add_u32 v0, v0, 2, s1
	v_min_u32_e32 v0, s14, v0
	v_cndmask_b32_e32 v0, v140, v0, vcc
	s_lshl2_add_u32 s1, s2, s1
	v_cmp_le_u32_e32 vcc, s0, v99
	ds_write_b32 v0, v98
	s_bcnt1_i32_b64 s2, vcc
	v_mbcnt_lo_u32_b32 v0, vcc_lo, 0
	v_mbcnt_hi_u32_b32 v0, vcc_hi, v0
	v_lshl_add_u32 v0, v0, 2, s1
	v_min_u32_e32 v0, s14, v0
	v_cndmask_b32_e32 v0, v140, v0, vcc
	s_lshl2_add_u32 s1, s2, s1
	v_cmp_le_u32_e32 vcc, s0, v100
	ds_write_b32 v0, v99
	s_bcnt1_i32_b64 s2, vcc
	v_mbcnt_lo_u32_b32 v0, vcc_lo, 0
	v_mbcnt_hi_u32_b32 v0, vcc_hi, v0
	v_lshl_add_u32 v0, v0, 2, s1
	v_min_u32_e32 v0, s14, v0
	v_cndmask_b32_e32 v0, v140, v0, vcc
	s_lshl2_add_u32 s1, s2, s1
	v_cmp_le_u32_e32 vcc, s0, v101
	ds_write_b32 v0, v100
	s_bcnt1_i32_b64 s2, vcc
	v_mbcnt_lo_u32_b32 v0, vcc_lo, 0
	v_mbcnt_hi_u32_b32 v0, vcc_hi, v0
	v_lshl_add_u32 v0, v0, 2, s1
	v_min_u32_e32 v0, s14, v0
	v_cndmask_b32_e32 v0, v140, v0, vcc
	s_lshl2_add_u32 s1, s2, s1
	v_cmp_le_u32_e32 vcc, s0, v102
	ds_write_b32 v0, v101
	s_bcnt1_i32_b64 s2, vcc
	v_mbcnt_lo_u32_b32 v0, vcc_lo, 0
	v_mbcnt_hi_u32_b32 v0, vcc_hi, v0
	v_lshl_add_u32 v0, v0, 2, s1
	v_min_u32_e32 v0, s14, v0
	v_cndmask_b32_e32 v0, v140, v0, vcc
	s_lshl2_add_u32 s1, s2, s1
	v_cmp_le_u32_e32 vcc, s0, v103
	ds_write_b32 v0, v102
	s_bcnt1_i32_b64 s2, vcc
	v_mbcnt_lo_u32_b32 v0, vcc_lo, 0
	v_mbcnt_hi_u32_b32 v0, vcc_hi, v0
	v_lshl_add_u32 v0, v0, 2, s1
	v_min_u32_e32 v0, s14, v0
	v_cndmask_b32_e32 v0, v140, v0, vcc
	s_lshl2_add_u32 s1, s2, s1
	v_cmp_le_u32_e32 vcc, s0, v104
	ds_write_b32 v0, v103
	s_bcnt1_i32_b64 s2, vcc
	v_mbcnt_lo_u32_b32 v0, vcc_lo, 0
	v_mbcnt_hi_u32_b32 v0, vcc_hi, v0
	v_lshl_add_u32 v0, v0, 2, s1
	v_min_u32_e32 v0, s14, v0
	v_cndmask_b32_e32 v0, v140, v0, vcc
	s_lshl2_add_u32 s1, s2, s1
	v_cmp_le_u32_e32 vcc, s0, v105
	ds_write_b32 v0, v104
	s_bcnt1_i32_b64 s2, vcc
	v_mbcnt_lo_u32_b32 v0, vcc_lo, 0
	v_mbcnt_hi_u32_b32 v0, vcc_hi, v0
	v_lshl_add_u32 v0, v0, 2, s1
	v_min_u32_e32 v0, s14, v0
	v_cndmask_b32_e32 v0, v140, v0, vcc
	s_lshl2_add_u32 s1, s2, s1
	v_cmp_le_u32_e32 vcc, s0, v106
	ds_write_b32 v0, v105
	s_bcnt1_i32_b64 s2, vcc
	v_mbcnt_lo_u32_b32 v0, vcc_lo, 0
	v_mbcnt_hi_u32_b32 v0, vcc_hi, v0
	v_lshl_add_u32 v0, v0, 2, s1
	v_min_u32_e32 v0, s14, v0
	v_cndmask_b32_e32 v0, v140, v0, vcc
	s_lshl2_add_u32 s1, s2, s1
	v_cmp_le_u32_e32 vcc, s0, v107
	ds_write_b32 v0, v106
	s_bcnt1_i32_b64 s2, vcc
	v_mbcnt_lo_u32_b32 v0, vcc_lo, 0
	v_mbcnt_hi_u32_b32 v0, vcc_hi, v0
	v_lshl_add_u32 v0, v0, 2, s1
	v_min_u32_e32 v0, s14, v0
	v_cndmask_b32_e32 v0, v140, v0, vcc
	s_lshl2_add_u32 s1, s2, s1
	v_cmp_le_u32_e32 vcc, s0, v108
	ds_write_b32 v0, v107
	s_bcnt1_i32_b64 s2, vcc
	v_mbcnt_lo_u32_b32 v0, vcc_lo, 0
	v_mbcnt_hi_u32_b32 v0, vcc_hi, v0
; #define LAS __attribute__((address_space(3)))
; #define LDS_WAIT() asm volatile("s_waitcnt lgkmcnt(0)" ::: "memory")
; __device__ __forceinline__ void topk_phase(Frame& F) {
;     ...
;             for (int j = 0; j < 129; ++j) { const unsigned kv = j < 128 ? key[j] : key128; const bool p = kv >= ts;
;                 const unsigned long long m = __ballot(p);
;                 const int pos = ctot + (int)__builtin_amdgcn_mbcnt_hi((unsigned)(m >> 32), __builtin_amdgcn_mbcnt_lo((unsigned)m, 0u));
;                 LAS unsigned* a = (p && pos < 24 * 64) ? cbuf + pos : dump; *a = kv; ctot += __popcll(m);
;                 if ((j & 7) == 7) __builtin_amdgcn_sched_barrier(0); }
;             LDS_WAIT(); asm volatile("" ::: "memory");
;             if (ctot >= 256 && ctot <= 24 * 64) {
	v_lshl_add_u32 v0, v0, 2, s1
	v_min_u32_e32 v0, s14, v0
	v_cndmask_b32_e32 v0, v140, v0, vcc
	s_lshl2_add_u32 s1, s2, s1
	v_cmp_le_u32_e32 vcc, s0, v109
	ds_write_b32 v0, v108
	s_bcnt1_i32_b64 s2, vcc
	v_mbcnt_lo_u32_b32 v0, vcc_lo, 0
	v_mbcnt_hi_u32_b32 v0, vcc_hi, v0
	v_lshl_add_u32 v0, v0, 2, s1
	v_min_u32_e32 v0, s14, v0
	v_cndmask_b32_e32 v0, v140, v0, vcc
	s_lshl2_add_u32 s1, s2, s1
	v_cmp_le_u32_e32 vcc, s0, v110
	ds_write_b32 v0, v109
	s_bcnt1_i32_b64 s2, vcc
	v_mbcnt_lo_u32_b32 v0, vcc_lo, 0
	v_mbcnt_hi_u32_b32 v0, vcc_hi, v0
	v_lshl_add_u32 v0, v0, 2, s1
	v_min_u32_e32 v0, s14, v0
	v_cndmask_b32_e32 v0, v140, v0, vcc
	s_lshl2_add_u32 s1, s2, s1
	v_cmp_le_u32_e32 vcc, s0, v111
	ds_write_b32 v0, v110
	s_bcnt1_i32_b64 s2, vcc
	v_mbcnt_lo_u32_b32 v0, vcc_lo, 0
	v_mbcnt_hi_u32_b32 v0, vcc_hi, v0
	v_lshl_add_u32 v0, v0, 2, s1
	v_min_u32_e32 v0, s14, v0
	v_cndmask_b32_e32 v0, v140, v0, vcc
	s_lshl2_add_u32 s1, s2, s1
	v_cmp_le_u32_e32 vcc, s0, v112
	ds_write_b32 v0, v111
	s_bcnt1_i32_b64 s2, vcc
	v_mbcnt_lo_u32_b32 v0, vcc_lo, 0
	v_mbcnt_hi_u32_b32 v0, vcc_hi, v0
	v_lshl_add_u32 v0, v0, 2, s1
	v_min_u32_e32 v0, s14, v0
	v_cndmask_b32_e32 v0, v140, v0, vcc
	s_lshl2_add_u32 s1, s2, s1
	v_cmp_le_u32_e32 vcc, s0, v113
	ds_write_b32 v0, v112
	s_bcnt1_i32_b64 s2, vcc
	v_mbcnt_lo_u32_b32 v0, vcc_lo, 0
	v_mbcnt_hi_u32_b32 v0, vcc_hi, v0
	v_lshl_add_u32 v0, v0, 2, s1
	v_min_u32_e32 v0, s14, v0
	v_cndmask_b32_e32 v0, v140, v0, vcc
	s_lshl2_add_u32 s1, s2, s1
	v_cmp_le_u32_e32 vcc, s0, v114
	ds_write_b32 v0, v113
	s_bcnt1_i32_b64 s2, vcc
	v_mbcnt_lo_u32_b32 v0, vcc_lo, 0
	v_mbcnt_hi_u32_b32 v0, vcc_hi, v0
	v_lshl_add_u32 v0, v0, 2, s1
	v_min_u32_e32 v0, s14, v0
	v_cndmask_b32_e32 v0, v140, v0, vcc
	s_lshl2_add_u32 s1, s2, s1
	v_cmp_le_u32_e32 vcc, s0, v115
	ds_write_b32 v0, v114
	s_bcnt1_i32_b64 s2, vcc
	v_mbcnt_lo_u32_b32 v0, vcc_lo, 0
	v_mbcnt_hi_u32_b32 v0, vcc_hi, v0
	v_lshl_add_u32 v0, v0, 2, s1
	v_min_u32_e32 v0, s14, v0
	v_cndmask_b32_e32 v0, v140, v0, vcc
	s_lshl2_add_u32 s1, s2, s1
	v_cmp_le_u32_e32 vcc, s0, v116
	ds_write_b32 v0, v115
	s_bcnt1_i32_b64 s2, vcc
	v_mbcnt_lo_u32_b32 v0, vcc_lo, 0
	v_mbcnt_hi_u32_b32 v0, vcc_hi, v0
	v_lshl_add_u32 v0, v0, 2, s1
	v_min_u32_e32 v0, s14, v0
	v_cndmask_b32_e32 v0, v140, v0, vcc
	s_lshl2_add_u32 s1, s2, s1
	v_cmp_le_u32_e32 vcc, s0, v117
	ds_write_b32 v0, v116
	s_bcnt1_i32_b64 s2, vcc
	v_mbcnt_lo_u32_b32 v0, vcc_lo, 0
	v_mbcnt_hi_u32_b32 v0, vcc_hi, v0
	v_lshl_add_u32 v0, v0, 2, s1
	v_min_u32_e32 v0, s14, v0
	v_cndmask_b32_e32 v0, v140, v0, vcc
	s_lshl2_add_u32 s1, s2, s1
	v_cmp_le_u32_e32 vcc, s0, v118
	ds_write_b32 v0, v117
	s_bcnt1_i32_b64 s2, vcc
	v_mbcnt_lo_u32_b32 v0, vcc_lo, 0
	v_mbcnt_hi_u32_b32 v0, vcc_hi, v0
	v_lshl_add_u32 v0, v0, 2, s1
	v_min_u32_e32 v0, s14, v0
	v_cndmask_b32_e32 v0, v140, v0, vcc
	s_lshl2_add_u32 s1, s2, s1
	v_cmp_le_u32_e32 vcc, s0, v119
	ds_write_b32 v0, v118
	s_bcnt1_i32_b64 s2, vcc
	v_mbcnt_lo_u32_b32 v0, vcc_lo, 0
	v_mbcnt_hi_u32_b32 v0, vcc_hi, v0
	v_lshl_add_u32 v0, v0, 2, s1
	v_min_u32_e32 v0, s14, v0
	v_cndmask_b32_e32 v0, v140, v0, vcc
	s_lshl2_add_u32 s1, s2, s1
	v_cmp_le_u32_e32 vcc, s0, v120
	ds_write_b32 v0, v119
	s_bcnt1_i32_b64 s2, vcc
	v_mbcnt_lo_u32_b32 v0, vcc_lo, 0
	v_mbcnt_hi_u32_b32 v0, vcc_hi, v0
	v_lshl_add_u32 v0, v0, 2, s1
	v_min_u32_e32 v0, s14, v0
	v_cndmask_b32_e32 v0, v140, v0, vcc
	s_lshl2_add_u32 s1, s2, s1
	v_cmp_le_u32_e32 vcc, s0, v121
	ds_write_b32 v0, v120
	s_bcnt1_i32_b64 s2, vcc
	v_mbcnt_lo_u32_b32 v0, vcc_lo, 0
	v_mbcnt_hi_u32_b32 v0, vcc_hi, v0
	v_lshl_add_u32 v0, v0, 2, s1
	v_min_u32_e32 v0, s14, v0
	v_cndmask_b32_e32 v0, v140, v0, vcc
	s_lshl2_add_u32 s1, s2, s1
	v_cmp_le_u32_e32 vcc, s0, v122
	ds_write_b32 v0, v121
	s_bcnt1_i32_b64 s2, vcc
	v_mbcnt_lo_u32_b32 v0, vcc_lo, 0
	v_mbcnt_hi_u32_b32 v0, vcc_hi, v0
	v_lshl_add_u32 v0, v0, 2, s1
	v_min_u32_e32 v0, s14, v0
	v_cndmask_b32_e32 v0, v140, v0, vcc
	s_lshl2_add_u32 s1, s2, s1
	v_cmp_le_u32_e32 vcc, s0, v123
	ds_write_b32 v0, v122
	s_bcnt1_i32_b64 s2, vcc
	v_mbcnt_lo_u32_b32 v0, vcc_lo, 0
	v_mbcnt_hi_u32_b32 v0, vcc_hi, v0
	v_lshl_add_u32 v0, v0, 2, s1
	v_min_u32_e32 v0, s14, v0
	v_cndmask_b32_e32 v0, v140, v0, vcc
	s_lshl2_add_u32 s1, s2, s1
	v_cmp_le_u32_e32 vcc, s0, v124
	ds_write_b32 v0, v123
	s_bcnt1_i32_b64 s2, vcc
	v_mbcnt_lo_u32_b32 v0, vcc_lo, 0
	v_mbcnt_hi_u32_b32 v0, vcc_hi, v0
	v_lshl_add_u32 v0, v0, 2, s1
	v_min_u32_e32 v0, s14, v0
	v_cndmask_b32_e32 v0, v140, v0, vcc
	s_lshl2_add_u32 s1, s2, s1
	v_cmp_le_u32_e32 vcc, s0, v125
	ds_write_b32 v0, v124
	s_bcnt1_i32_b64 s2, vcc
	v_mbcnt_lo_u32_b32 v0, vcc_lo, 0
	v_mbcnt_hi_u32_b32 v0, vcc_hi, v0
	v_lshl_add_u32 v0, v0, 2, s1
	v_min_u32_e32 v0, s14, v0
	v_cndmask_b32_e32 v0, v140, v0, vcc
	s_lshl2_add_u32 s1, s2, s1
	v_cmp_le_u32_e32 vcc, s0, v126
	ds_write_b32 v0, v125
	s_bcnt1_i32_b64 s2, vcc
	v_mbcnt_lo_u32_b32 v0, vcc_lo, 0
	v_mbcnt_hi_u32_b32 v0, vcc_hi, v0
	v_lshl_add_u32 v0, v0, 2, s1
	v_min_u32_e32 v0, s14, v0
	v_cndmask_b32_e32 v0, v140, v0, vcc
	s_lshl2_add_u32 s1, s2, s1
	v_cmp_le_u32_e32 vcc, s0, v127
	ds_write_b32 v0, v126
	s_bcnt1_i32_b64 s2, vcc
	v_mbcnt_lo_u32_b32 v0, vcc_lo, 0
	v_mbcnt_hi_u32_b32 v0, vcc_hi, v0
	v_lshl_add_u32 v0, v0, 2, s1
	v_min_u32_e32 v0, s14, v0
	v_cndmask_b32_e32 v0, v140, v0, vcc
	s_lshl2_add_u32 s1, s2, s1
	v_cmp_le_u32_e32 vcc, s0, v72
	ds_write_b32 v0, v127
	s_bcnt1_i32_b64 s2, vcc
	v_mbcnt_lo_u32_b32 v0, vcc_lo, 0
	v_mbcnt_hi_u32_b32 v0, vcc_hi, v0
	v_lshl_add_u32 v0, v0, 2, s1
	v_min_u32_e32 v0, s14, v0
	v_cndmask_b32_e32 v0, v140, v0, vcc
	s_lshl2_add_u32 s1, s2, s1
	v_cmp_le_u32_e32 vcc, s0, v73
	ds_write_b32 v0, v72
	s_bcnt1_i32_b64 s2, vcc
	v_mbcnt_lo_u32_b32 v0, vcc_lo, 0
	v_mbcnt_hi_u32_b32 v0, vcc_hi, v0
	v_lshl_add_u32 v0, v0, 2, s1
	v_min_u32_e32 v0, s14, v0
	v_cndmask_b32_e32 v0, v140, v0, vcc
	s_lshl2_add_u32 s1, s2, s1
	v_cmp_le_u32_e32 vcc, s0, v74
	ds_write_b32 v0, v73
	s_bcnt1_i32_b64 s2, vcc
	v_mbcnt_lo_u32_b32 v0, vcc_lo, 0
	v_mbcnt_hi_u32_b32 v0, vcc_hi, v0
	v_lshl_add_u32 v0, v0, 2, s1
	v_min_u32_e32 v0, s14, v0
	v_cndmask_b32_e32 v0, v140, v0, vcc
	s_lshl2_add_u32 s1, s2, s1
	v_cmp_le_u32_e32 vcc, s0, v75
	ds_write_b32 v0, v74
	s_bcnt1_i32_b64 s2, vcc
	v_mbcnt_lo_u32_b32 v0, vcc_lo, 0
	v_mbcnt_hi_u32_b32 v0, vcc_hi, v0
	v_lshl_add_u32 v0, v0, 2, s1
	v_min_u32_e32 v0, s14, v0
	v_cndmask_b32_e32 v0, v140, v0, vcc
	s_lshl2_add_u32 s1, s2, s1
	v_cmp_le_u32_e32 vcc, s0, v27
	ds_write_b32 v0, v75
	s_bcnt1_i32_b64 s2, vcc
	v_mbcnt_lo_u32_b32 v0, vcc_lo, 0
	v_mbcnt_hi_u32_b32 v0, vcc_hi, v0
	v_lshl_add_u32 v0, v0, 2, s1
	v_min_u32_e32 v0, s14, v0
	v_cndmask_b32_e32 v0, v140, v0, vcc
	s_lshl2_add_u32 s1, s2, s1
	ds_write_b32 v0, v27
	s_sub_i32 s0, s1, s93
	s_lshr_b32 s0, s0, 2
	s_add_i32 s1, s0, 0xffffff00
	s_waitcnt lgkmcnt(0)
	s_cmpk_gt_u32 s1, 0x500
	s_cselect_b64 s[2:3], -1, 0
	v_writelane_b32 v255, s2, 12
	s_and_b64 vcc, exec, s[2:3]
	s_nop 0
	v_writelane_b32 v255, s3, 13
	s_cbranch_vccnz .LBB0_999
; __device__ __forceinline__ void topk_phase(Frame& F) {
;     ...
;             if (ctot >= 256 && ctot <= 24 * 64) {
;                 unsigned cd[24]; const int nr = (ctot + 63) >> 6;
; #pragma unroll
;                 for (int r = 0; r < 24; ++r) { const unsigned v = cbuf[64 * r + lane]; cd[r] = (64 * r + lane < ctot) ? v : 0u; }
;     ...
;                     const unsigned cand = prefix | (1u << bit); int cnt = 0;
; #pragma unroll
;                     for (int r = 0; r < 24; ++r) if (r < nr) cnt += __popcll(__ballot(cd[r] >= cand));
	s_cmpk_gt_u32 s0, 0x100
	s_cselect_b64 s[68:69], -1, 0
	s_cmpk_gt_u32 s0, 0x140
	s_cselect_b64 s[70:71], -1, 0
	s_cmpk_gt_u32 s0, 0x180
	s_cselect_b64 s[72:73], -1, 0
	s_cmpk_gt_u32 s0, 0x1c0
	s_cselect_b64 s[74:75], -1, 0
	s_cmpk_gt_u32 s0, 0x200
	s_cselect_b64 s[76:77], -1, 0
	s_cmpk_gt_u32 s0, 0x240
	v_add_u32_e32 v8, 0x180, v137
	s_cselect_b64 s[78:79], -1, 0
	s_cmpk_gt_u32 s0, 0x280
	v_cmp_gt_i32_e64 s[26:27], s0, v8
	v_add_u32_e32 v8, 0x1c0, v137
	s_cselect_b64 s[80:81], -1, 0
	s_cmpk_gt_u32 s0, 0x2c0
	v_cmp_gt_i32_e64 s[28:29], s0, v8
	v_add_u32_e32 v8, 0x200, v137
	s_cselect_b64 s[82:83], -1, 0
	s_cmpk_gt_u32 s0, 0x300
	v_add_u32_e32 v0, 64, v137
	v_cmp_gt_i32_e64 s[30:31], s0, v8
	v_add_u32_e32 v8, 0x240, v137
	s_cselect_b64 s[84:85], -1, 0
	s_cmpk_gt_u32 s0, 0x340
	v_cmp_gt_i32_e64 s[16:17], s0, v0
	v_add_u32_e32 v0, 0x80, v137
	v_cmp_gt_i32_e64 s[34:35], s0, v8
	v_add_u32_e32 v8, 0x280, v137
	s_cselect_b64 s[86:87], -1, 0
	s_cmpk_gt_u32 s0, 0x380
	v_cmp_gt_i32_e64 s[18:19], s0, v0
	v_add_u32_e32 v0, 0xc0, v137
	v_cmp_gt_i32_e64 s[36:37], s0, v8
	v_add_u32_e32 v8, 0x2c0, v137
	s_cselect_b64 s[88:89], -1, 0
	s_cmpk_gt_u32 s0, 0x3c0
	v_cmp_gt_i32_e64 s[20:21], s0, v0
	v_add_u32_e32 v0, 0x100, v137
	v_cmp_gt_i32_e64 s[38:39], s0, v8
	v_add_u32_e32 v8, 0x300, v137
	s_cselect_b64 s[90:91], -1, 0
	s_cmpk_gt_u32 s0, 0x400
	v_cmp_gt_i32_e64 s[22:23], s0, v0
	v_add_u32_e32 v0, 0x140, v137
	v_cmp_gt_i32_e64 s[40:41], s0, v8
	v_add_u32_e32 v8, 0x340, v137
	v_add_u32_e32 v16, 0x380, v137
	s_cselect_b64 s[96:97], -1, 0
	s_cmpk_gt_u32 s0, 0x440
	v_cmp_gt_i32_e64 s[24:25], s0, v0
	ds_read2st64_b32 v[0:1], v139 offset1:1
	ds_read2st64_b32 v[2:3], v139 offset0:2 offset1:3
	ds_read2st64_b32 v[4:5], v139 offset0:4 offset1:5
	ds_read2st64_b32 v[6:7], v139 offset0:6 offset1:7
	v_cmp_gt_i32_e64 s[42:43], s0, v8
	ds_read2st64_b32 v[8:9], v139 offset0:8 offset1:9
	ds_read2st64_b32 v[10:11], v139 offset0:10 offset1:11
	ds_read2st64_b32 v[12:13], v139 offset0:12 offset1:13
	ds_read2st64_b32 v[14:15], v139 offset0:14 offset1:15
	v_cmp_gt_i32_e64 s[44:45], s0, v16
	ds_read2st64_b32 v[16:17], v139 offset0:16 offset1:17
	ds_read2st64_b32 v[18:19], v139 offset0:18 offset1:19
	ds_read2st64_b32 v[20:21], v139 offset0:20 offset1:21
	ds_read2st64_b32 v[22:23], v139 offset0:22 offset1:23
	s_cselect_b64 s[4:5], -1, 0
	s_cmpk_gt_u32 s0, 0x480
	s_cselect_b64 s[6:7], -1, 0
	s_cmpk_gt_u32 s0, 0x4c0
	s_cselect_b64 s[8:9], -1, 0
	s_cmpk_gt_u32 s0, 0x500
	s_cselect_b64 s[10:11], -1, 0
	s_cmpk_gt_u32 s0, 0x540
	s_cselect_b64 s[12:13], -1, 0
	s_cmpk_gt_u32 s0, 0x580
	s_cselect_b64 s[2:3], -1, 0
	s_cmpk_gt_u32 s0, 0x5c0
	v_cmp_gt_i32_e64 s[14:15], s0, v137
	v_cmp_gt_i32_e64 s[46:47], s0, v142
	v_cmp_gt_i32_e64 s[48:49], s0, v143
	v_cmp_gt_i32_e64 s[50:51], s0, v144
	v_cmp_gt_i32_e64 s[52:53], s0, v145
	v_cmp_gt_i32_e64 s[54:55], s0, v146
	v_cmp_gt_i32_e64 s[56:57], s0, v147
	v_cmp_gt_i32_e64 s[58:59], s0, v148
	v_cmp_gt_i32_e64 s[60:61], s0, v149
	v_cmp_gt_i32_e64 s[62:63], s0, v150
	s_mov_b64 s[64:65], 0
	s_cselect_b64 s[0:1], -1, 0
	v_mov_b32_e32 v211, 31
	v_mov_b32_e32 v210, 0
	s_branch .LBB0_958

; #define SBAR() __builtin_amdgcn_sched_barrier(0)
; #define TRRD(dst, off) asm volatile("ds_read_b64_tr_b16 %0, %1 offset:%2" : "=&v"(dst) : "v"(vb0), "i"(off) : "memory")
; #define TRRD(dst, off) asm volatile("ds_read_b64_tr_b16 %0, %1 offset:%2" : "=&v"(dst) : "v"(vb0), "i"(off) : "memory")
; template <int VB, int G>
; __device__ __forceinline__ void pv_group(f32x16* o, int vb0, bf16x8 pa0, bf16x8 pa1, bf16x8 pa2, bf16x8 pa3) {
;     ...
;     s16x4 l0, l1, l2, l3, h0, h1, h2, h3; constexpr int b_ = VB * SHM_V + v_rd_off(G, 0, 0);
;     TRRD(l0, b_); TRRD(h0, b_ + 2048); TRRD(l1, b_ + 4096); TRRD(h1, b_ + 6144); TRRD(l2, b_ + 8192); TRRD(h2, b_ + 10240); TRRD(l3, b_ + 12288); TRRD(h3, b_ + 14336);
;     asm volatile("s_waitcnt lgkmcnt(0)" ::: "memory"); SBAR();
;     o[G] = __builtin_amdgcn_mfma_f32_32x32x16_bf16(pa0, (bf16x8){l0[0], l0[1], l0[2], l0[3], h0[0], h0[1], h0[2], h0[3]}, o[G], 0, 0, 0);
;     o[G] = __builtin_amdgcn_mfma_f32_32x32x16_bf16(pa1, (bf16x8){l1[0], l1[1], l1[2], l1[3], h1[0], h1[1], h1[2], h1[3]}, o[G], 0, 0, 0);
;     o[G] = __builtin_amdgcn_mfma_f32_32x32x16_bf16(pa2, (bf16x8){l2[0], l2[1], l2[2], l2[3], h2[0], h2[1], h2[2], h2[3]}, o[G], 0, 0, 0);
;     o[G] = __builtin_amdgcn_mfma_f32_32x32x16_bf16(pa3, (bf16x8){l3[0], l3[1], l3[2], l3[3], h3[0], h3[1], h3[2], h3[3]}, o[G], 0, 0, 0);
;     SBAR();
.LBB0_1100:
	ds_read_b64_tr_b16 v[234:235], v228 offset:0x4000
	ds_read_b64_tr_b16 v[236:237], v228 offset:0x4800
	ds_read_b64_tr_b16 v[238:239], v228 offset:0x5000
	ds_read_b64_tr_b16 v[240:241], v228 offset:0x5800
	ds_read_b64_tr_b16 v[242:243], v228 offset:0x6000
	ds_read_b64_tr_b16 v[244:245], v228 offset:0x6800
	ds_read_b64_tr_b16 v[246:247], v228 offset:0x7000
	ds_read_b64_tr_b16 v[248:249], v228 offset:0x7800
	s_waitcnt lgkmcnt(6)
	v_mfma_f32_32x32x16_bf16 v[50:65], v[174:177], v[234:237], v[50:65]
	s_waitcnt lgkmcnt(4)
	v_mfma_f32_32x32x16_bf16 v[50:65], v[170:173], v[238:241], v[50:65]
	s_waitcnt lgkmcnt(2)
	v_mfma_f32_32x32x16_bf16 v[50:65], v[166:169], v[242:245], v[50:65]
	s_waitcnt lgkmcnt(0)
	v_mfma_f32_32x32x16_bf16 v[50:65], v[162:165], v[246:249], v[50:65]
	s_and_b64 vcc, exec, s[0:1]
	s_cbranch_vccnz .LBB0_1102
	v_add_u32_e32 v0, v229, v233
	ds_read2_b32 v[202:203], v0 offset1:9
	ds_read2_b32 v[206:207], v0 offset0:18 offset1:27
	ds_read2_b32 v[210:211], v0 offset0:36 offset1:45
	ds_read2_b32 v[212:213], v0 offset0:54 offset1:63
.LBB0_1102:
	ds_read_b64_tr_b16 v[234:235], v228 offset:0x4200
	ds_read_b64_tr_b16 v[236:237], v228 offset:0x4a00
	ds_read_b64_tr_b16 v[238:239], v228 offset:0x5200
	ds_read_b64_tr_b16 v[240:241], v228 offset:0x5a00
	ds_read_b64_tr_b16 v[242:243], v228 offset:0x6200
	ds_read_b64_tr_b16 v[244:245], v228 offset:0x6a00
	ds_read_b64_tr_b16 v[246:247], v228 offset:0x7200
	ds_read_b64_tr_b16 v[248:249], v228 offset:0x7a00
	s_waitcnt lgkmcnt(6)
	s_nop 0
	v_mfma_f32_32x32x16_bf16 v[34:49], v[174:177], v[234:237], v[34:49]
	s_waitcnt lgkmcnt(4)
	v_mfma_f32_32x32x16_bf16 v[34:49], v[170:173], v[238:241], v[34:49]
	s_waitcnt lgkmcnt(2)
	v_mfma_f32_32x32x16_bf16 v[34:49], v[166:169], v[242:245], v[34:49]
	s_waitcnt lgkmcnt(0)
	v_mfma_f32_32x32x16_bf16 v[34:49], v[162:165], v[246:249], v[34:49]
	s_and_b64 vcc, exec, s[0:1]
	s_cbranch_vccnz .LBB0_1104
	s_waitcnt lgkmcnt(3)
	v_perm_b32 v0, v203, v202, v181
	s_waitcnt lgkmcnt(2)
	v_perm_b32 v202, v207, v206, v181
	s_waitcnt lgkmcnt(1)
	v_perm_b32 v203, v211, v210, v181
	s_waitcnt lgkmcnt(0)
	v_perm_b32 v206, v213, v212, v181
	v_perm_b32 v203, v206, v203, s90
	v_lshl_add_u64 v[206:207], s[12:13], 0, v[184:185]
	v_perm_b32 v202, v202, v0, s90
	v_lshl_add_u64 v[206:207], v[206:207], 0, v[194:195]
	s_bitset1_b32 s98, 2
	global_store_dwordx2 v[206:207], v[202:203], off nt
	v_add_u32_e32 v0, v229, v233
	ds_read2_b32 v[202:203], v0 offset0:2 offset1:11
	ds_read2_b32 v[206:207], v0 offset0:20 offset1:29
	ds_read2_b32 v[210:211], v0 offset0:38 offset1:47
	ds_read2_b32 v[212:213], v0 offset0:56 offset1:65
.LBB0_1104:
	ds_read_b64_tr_b16 v[234:235], v228 offset:0x4400
	ds_read_b64_tr_b16 v[236:237], v228 offset:0x4c00
	ds_read_b64_tr_b16 v[238:239], v228 offset:0x5400
	ds_read_b64_tr_b16 v[240:241], v228 offset:0x5c00
	ds_read_b64_tr_b16 v[242:243], v228 offset:0x6400
	ds_read_b64_tr_b16 v[244:245], v228 offset:0x6c00
	ds_read_b64_tr_b16 v[246:247], v228 offset:0x7400
	ds_read_b64_tr_b16 v[248:249], v228 offset:0x7c00
	s_waitcnt lgkmcnt(6)
	s_nop 0
	v_mfma_f32_32x32x16_bf16 v[18:33], v[174:177], v[234:237], v[18:33]
	s_waitcnt lgkmcnt(4)
	v_mfma_f32_32x32x16_bf16 v[18:33], v[170:173], v[238:241], v[18:33]
	s_waitcnt lgkmcnt(2)
	v_mfma_f32_32x32x16_bf16 v[18:33], v[166:169], v[242:245], v[18:33]
	s_waitcnt lgkmcnt(0)
	v_mfma_f32_32x32x16_bf16 v[18:33], v[162:165], v[246:249], v[18:33]
	s_and_b64 vcc, exec, s[0:1]
	s_cbranch_vccnz .LBB0_1106
	s_waitcnt lgkmcnt(3)
	v_perm_b32 v0, v203, v202, v181
	s_waitcnt lgkmcnt(2)
	v_perm_b32 v202, v207, v206, v181
	s_waitcnt lgkmcnt(1)
	v_perm_b32 v203, v211, v210, v181
	s_waitcnt lgkmcnt(0)
	v_perm_b32 v206, v213, v212, v181
	v_perm_b32 v203, v206, v203, s90
	v_lshl_add_u64 v[206:207], s[12:13], 0, v[188:189]
	v_perm_b32 v202, v202, v0, s90
	v_lshl_add_u64 v[206:207], v[206:207], 0, v[194:195]
	global_store_dwordx2 v[206:207], v[202:203], off nt
	v_add_u32_e32 v0, v229, v233
	ds_read2_b32 v[202:203], v0 offset0:4 offset1:13
	ds_read2_b32 v[206:207], v0 offset0:22 offset1:31
	ds_read2_b32 v[210:211], v0 offset0:40 offset1:49
	ds_read2_b32 v[212:213], v0 offset0:58 offset1:67
.LBB0_1106:
	ds_read_b64_tr_b16 v[234:235], v228 offset:0x4600
	ds_read_b64_tr_b16 v[236:237], v228 offset:0x4e00
	ds_read_b64_tr_b16 v[238:239], v228 offset:0x5600
	ds_read_b64_tr_b16 v[240:241], v228 offset:0x5e00
	ds_read_b64_tr_b16 v[242:243], v228 offset:0x6600
	ds_read_b64_tr_b16 v[244:245], v228 offset:0x6e00
	ds_read_b64_tr_b16 v[246:247], v228 offset:0x7600
	ds_read_b64_tr_b16 v[248:249], v228 offset:0x7e00
	s_waitcnt lgkmcnt(6)
	s_nop 0
	v_mfma_f32_32x32x16_bf16 v[2:17], v[174:177], v[234:237], v[2:17]
	s_waitcnt lgkmcnt(4)
	v_mfma_f32_32x32x16_bf16 v[2:17], v[170:173], v[238:241], v[2:17]
	s_waitcnt lgkmcnt(2)
	v_mfma_f32_32x32x16_bf16 v[2:17], v[166:169], v[242:245], v[2:17]
	s_waitcnt lgkmcnt(0)
	v_mfma_f32_32x32x16_bf16 v[2:17], v[162:165], v[246:249], v[2:17]
	s_and_b64 vcc, exec, s[0:1]
	s_cbranch_vccnz .LBB0_1108
	s_waitcnt lgkmcnt(1)
	v_perm_b32 v163, v211, v210, v181
	s_waitcnt lgkmcnt(0)
	v_perm_b32 v164, v213, v212, v181
	v_perm_b32 v0, v203, v202, v181
	v_perm_b32 v162, v207, v206, v181
	v_perm_b32 v163, v164, v163, s90
	v_lshl_add_u64 v[164:165], s[12:13], 0, v[186:187]
	v_perm_b32 v162, v162, v0, s90
	v_lshl_add_u64 v[164:165], v[164:165], 0, v[194:195]
	global_store_dwordx2 v[164:165], v[162:163], off nt
	v_add_u32_e32 v0, v229, v233
	ds_read2_b32 v[202:203], v0 offset0:6 offset1:15
	ds_read2_b32 v[206:207], v0 offset0:24 offset1:33
	ds_read2_b32 v[210:211], v0 offset0:42 offset1:51
	ds_read2_b32 v[212:213], v0 offset0:60 offset1:69

; #define SBAR() __builtin_amdgcn_sched_barrier(0)
; #define TRRD(dst, off) asm volatile("ds_read_b64_tr_b16 %0, %1 offset:%2" : "=&v"(dst) : "v"(vb0), "i"(off) : "memory")
; #define TRRD(dst, off) asm volatile("ds_read_b64_tr_b16 %0, %1 offset:%2" : "=&v"(dst) : "v"(vb0), "i"(off) : "memory")
; template <int VB, int G>
; __device__ __forceinline__ void pv_group(f32x16* o, int vb0, bf16x8 pa0, bf16x8 pa1, bf16x8 pa2, bf16x8 pa3) {
;     ...
;     s16x4 l0, l1, l2, l3, h0, h1, h2, h3; constexpr int b_ = VB * SHM_V + v_rd_off(G, 0, 0);
;     TRRD(l0, b_); TRRD(h0, b_ + 2048); TRRD(l1, b_ + 4096); TRRD(h1, b_ + 6144); TRRD(l2, b_ + 8192); TRRD(h2, b_ + 10240); TRRD(l3, b_ + 12288); TRRD(h3, b_ + 14336);
;     asm volatile("s_waitcnt lgkmcnt(0)" ::: "memory"); SBAR();
;     o[G] = __builtin_amdgcn_mfma_f32_32x32x16_bf16(pa0, (bf16x8){l0[0], l0[1], l0[2], l0[3], h0[0], h0[1], h0[2], h0[3]}, o[G], 0, 0, 0);
;     o[G] = __builtin_amdgcn_mfma_f32_32x32x16_bf16(pa1, (bf16x8){l1[0], l1[1], l1[2], l1[3], h1[0], h1[1], h1[2], h1[3]}, o[G], 0, 0, 0);
;     o[G] = __builtin_amdgcn_mfma_f32_32x32x16_bf16(pa2, (bf16x8){l2[0], l2[1], l2[2], l2[3], h2[0], h2[1], h2[2], h2[3]}, o[G], 0, 0, 0);
;     o[G] = __builtin_amdgcn_mfma_f32_32x32x16_bf16(pa3, (bf16x8){l3[0], l3[1], l3[2], l3[3], h3[0], h3[1], h3[2], h3[3]}, o[G], 0, 0, 0);
;     SBAR();
.LBB0_1137:
	ds_read_b64_tr_b16 v[234:235], v228 offset:0
	ds_read_b64_tr_b16 v[236:237], v228 offset:0x800
	ds_read_b64_tr_b16 v[238:239], v228 offset:0x1000
	ds_read_b64_tr_b16 v[240:241], v228 offset:0x1800
	ds_read_b64_tr_b16 v[242:243], v228 offset:0x2000
	ds_read_b64_tr_b16 v[244:245], v228 offset:0x2800
	ds_read_b64_tr_b16 v[246:247], v228 offset:0x3000
	ds_read_b64_tr_b16 v[248:249], v228 offset:0x3800
	s_waitcnt lgkmcnt(6)
	v_mfma_f32_32x32x16_bf16 v[50:65], v[174:177], v[234:237], v[50:65]
	s_waitcnt lgkmcnt(4)
	v_mfma_f32_32x32x16_bf16 v[50:65], v[170:173], v[238:241], v[50:65]
	s_waitcnt lgkmcnt(2)
	v_mfma_f32_32x32x16_bf16 v[50:65], v[166:169], v[242:245], v[50:65]
	s_waitcnt lgkmcnt(0)
	v_mfma_f32_32x32x16_bf16 v[50:65], v[162:165], v[246:249], v[50:65]
	v_cndmask_b32_e64 v0, 0, 1, s[14:15]
	v_cmp_ne_u32_e64 s[0:1], 1, v0
	s_andn2_b64 vcc, exec, s[14:15]
	v_add_u32_e32 v0, v229, v233
	s_cbranch_vccnz .LBB0_1139
	ds_read2_b32 v[204:205], v0 offset1:9
	ds_read2_b32 v[208:209], v0 offset0:18 offset1:27
	ds_read2_b32 v[214:215], v0 offset0:36 offset1:45
	ds_read2_b32 v[216:217], v0 offset0:54 offset1:63
.LBB0_1139:
	ds_read_b64_tr_b16 v[234:235], v228 offset:0x200
	ds_read_b64_tr_b16 v[236:237], v228 offset:0xa00
	ds_read_b64_tr_b16 v[238:239], v228 offset:0x1200
	ds_read_b64_tr_b16 v[240:241], v228 offset:0x1a00
	ds_read_b64_tr_b16 v[242:243], v228 offset:0x2200
	ds_read_b64_tr_b16 v[244:245], v228 offset:0x2a00
	ds_read_b64_tr_b16 v[246:247], v228 offset:0x3200
	ds_read_b64_tr_b16 v[248:249], v228 offset:0x3a00
	s_waitcnt lgkmcnt(6)
	s_nop 0
	v_mfma_f32_32x32x16_bf16 v[34:49], v[174:177], v[234:237], v[34:49]
	s_waitcnt lgkmcnt(4)
	v_mfma_f32_32x32x16_bf16 v[34:49], v[170:173], v[238:241], v[34:49]
	s_waitcnt lgkmcnt(2)
	v_mfma_f32_32x32x16_bf16 v[34:49], v[166:169], v[242:245], v[34:49]
	s_waitcnt lgkmcnt(0)
	v_mfma_f32_32x32x16_bf16 v[34:49], v[162:165], v[246:249], v[34:49]
	s_and_b64 vcc, exec, s[0:1]
	s_cbranch_vccnz .LBB0_1141
	s_waitcnt lgkmcnt(3)
	v_perm_b32 v204, v205, v204, v181
	s_waitcnt lgkmcnt(2)
	v_perm_b32 v205, v209, v208, v181
	s_waitcnt lgkmcnt(1)
	v_perm_b32 v208, v215, v214, v181
	s_waitcnt lgkmcnt(0)
	v_perm_b32 v209, v217, v216, v181
	v_perm_b32 v204, v205, v204, s90
	v_perm_b32 v205, v209, v208, s90
	v_lshl_add_u64 v[208:209], s[8:9], 0, v[184:185]
	v_lshl_add_u64 v[208:209], v[208:209], 0, v[194:195]
	s_bitset1_b32 s98, 2
	global_store_dwordx2 v[208:209], v[204:205], off nt
	ds_read2_b32 v[204:205], v0 offset0:2 offset1:11
	ds_read2_b32 v[208:209], v0 offset0:20 offset1:29
	ds_read2_b32 v[214:215], v0 offset0:38 offset1:47
	ds_read2_b32 v[216:217], v0 offset0:56 offset1:65
.LBB0_1141:
	ds_read_b64_tr_b16 v[234:235], v228 offset:0x400
	ds_read_b64_tr_b16 v[236:237], v228 offset:0xc00
	ds_read_b64_tr_b16 v[238:239], v228 offset:0x1400
	ds_read_b64_tr_b16 v[240:241], v228 offset:0x1c00
	ds_read_b64_tr_b16 v[242:243], v228 offset:0x2400
	ds_read_b64_tr_b16 v[244:245], v228 offset:0x2c00
	ds_read_b64_tr_b16 v[246:247], v228 offset:0x3400
	ds_read_b64_tr_b16 v[248:249], v228 offset:0x3c00
	s_waitcnt lgkmcnt(6)
	s_nop 0
	v_mfma_f32_32x32x16_bf16 v[18:33], v[174:177], v[234:237], v[18:33]
	s_waitcnt lgkmcnt(4)
	v_mfma_f32_32x32x16_bf16 v[18:33], v[170:173], v[238:241], v[18:33]
	s_waitcnt lgkmcnt(2)
	v_mfma_f32_32x32x16_bf16 v[18:33], v[166:169], v[242:245], v[18:33]
	s_waitcnt lgkmcnt(0)
	v_mfma_f32_32x32x16_bf16 v[18:33], v[162:165], v[246:249], v[18:33]
	s_and_b64 vcc, exec, s[0:1]
	s_cbranch_vccnz .LBB0_1143
	s_waitcnt lgkmcnt(3)
	v_perm_b32 v204, v205, v204, v181
	s_waitcnt lgkmcnt(2)
	v_perm_b32 v205, v209, v208, v181
	s_waitcnt lgkmcnt(1)
	v_perm_b32 v208, v215, v214, v181
	s_waitcnt lgkmcnt(0)
	v_perm_b32 v209, v217, v216, v181
	v_perm_b32 v204, v205, v204, s90
	v_perm_b32 v205, v209, v208, s90
	v_lshl_add_u64 v[208:209], s[8:9], 0, v[188:189]
	v_lshl_add_u64 v[208:209], v[208:209], 0, v[194:195]
	global_store_dwordx2 v[208:209], v[204:205], off nt
	ds_read2_b32 v[204:205], v0 offset0:4 offset1:13
	ds_read2_b32 v[208:209], v0 offset0:22 offset1:31
	ds_read2_b32 v[214:215], v0 offset0:40 offset1:49
	ds_read2_b32 v[216:217], v0 offset0:58 offset1:67
.LBB0_1143:
	ds_read_b64_tr_b16 v[234:235], v228 offset:0x600
	ds_read_b64_tr_b16 v[236:237], v228 offset:0xe00
	ds_read_b64_tr_b16 v[238:239], v228 offset:0x1600
	ds_read_b64_tr_b16 v[240:241], v228 offset:0x1e00
	ds_read_b64_tr_b16 v[242:243], v228 offset:0x2600
	ds_read_b64_tr_b16 v[244:245], v228 offset:0x2e00
	ds_read_b64_tr_b16 v[246:247], v228 offset:0x3600
	ds_read_b64_tr_b16 v[248:249], v228 offset:0x3e00
	s_waitcnt lgkmcnt(6)
	s_nop 0
	v_mfma_f32_32x32x16_bf16 v[2:17], v[174:177], v[234:237], v[2:17]
	s_waitcnt lgkmcnt(4)
	v_mfma_f32_32x32x16_bf16 v[2:17], v[170:173], v[238:241], v[2:17]
	s_waitcnt lgkmcnt(2)
	v_mfma_f32_32x32x16_bf16 v[2:17], v[166:169], v[242:245], v[2:17]
	s_waitcnt lgkmcnt(0)
	v_mfma_f32_32x32x16_bf16 v[2:17], v[162:165], v[246:249], v[2:17]
	s_and_b64 vcc, exec, s[0:1]
	s_cbranch_vccnz .LBB0_1145
	s_waitcnt lgkmcnt(3)
	v_perm_b32 v162, v205, v204, v181
	s_waitcnt lgkmcnt(2)
	v_perm_b32 v163, v209, v208, v181
	s_waitcnt lgkmcnt(1)
	v_perm_b32 v164, v215, v214, v181
	s_waitcnt lgkmcnt(0)
	v_perm_b32 v165, v217, v216, v181
	v_perm_b32 v162, v163, v162, s90
	v_perm_b32 v163, v165, v164, s90
	v_lshl_add_u64 v[164:165], s[8:9], 0, v[186:187]
	v_lshl_add_u64 v[164:165], v[164:165], 0, v[194:195]
	global_store_dwordx2 v[164:165], v[162:163], off nt
	ds_read2_b32 v[204:205], v0 offset0:6 offset1:15
	ds_read2_b32 v[208:209], v0 offset0:24 offset1:33
	ds_read2_b32 v[214:215], v0 offset0:42 offset1:51
	ds_read2_b32 v[216:217], v0 offset0:60 offset1:69

; __device__ __forceinline__ void partialSM(f32x16& p0, f32x16& p1, float& m_reg, float& mn, float& alpha) {
;     ...
;     constexpr float C2 = 1.4426950408889634f * SCALE;
;     if (__builtin_expect(__all((pmax - m_reg) * SCALE <= THR), 1)) { mn = m_reg; alpha = 1.f; }
;     else { mn = fmaxf(m_reg, pmax); alpha = __builtin_amdgcn_exp2f((m_reg - mn) * C2); m_reg = mn; }
;     const float mnL = -mn * C2;
; #pragma unroll
;     for (int r = 0; r < 16; ++r) p0[r] = fmaf(p0[r], C2, mnL);
; #pragma unroll
;     for (int r = 0; r < 16; ++r) p1[r] = fmaf(p1[r], C2, mnL);
; __device__ __forceinline__ void finishSM(f32x16& p0, f32x16& p1, float alpha, float& l_reg, bf16x8& pa0, bf16x8& pa1, bf16x8& pa2, bf16x8& pa3) {
;     ...
;     float ps = 0;
; #pragma unroll
;     for (int r = 0; r < 16; ++r) ps += p0[r];
; #pragma unroll
;     for (int r = 0; r < 16; ++r) ps += p1[r];
;     { auto rr = __builtin_amdgcn_permlane32_swap(__float_as_uint(ps), __float_as_uint(ps), false, false);
;       ps = __uint_as_float(rr[0]) + __uint_as_float(rr[1]); }
;     l_reg = l_reg * alpha + ps;
.LBB0_1310:
	v_cndmask_b32_e64 v154, v147, v180, s[4:5]
	v_mul_f32_e32 v130, 0xbe0293ee, v154
	v_mov_b32_e32 v180, v130
	v_fmamk_f32 v82, v82, 0x3e0293ee, v130
	v_fmamk_f32 v83, v83, 0x3e0293ee, v130
	v_fmamk_f32 v84, v84, 0x3e0293ee, v130
	v_fmamk_f32 v85, v85, 0x3e0293ee, v130
	v_fmamk_f32 v86, v86, 0x3e0293ee, v130
	v_fmamk_f32 v87, v87, 0x3e0293ee, v130
	v_fmamk_f32 v88, v88, 0x3e0293ee, v130
	v_fmamk_f32 v89, v89, 0x3e0293ee, v130
	v_fmamk_f32 v90, v90, 0x3e0293ee, v130
	v_fmamk_f32 v91, v91, 0x3e0293ee, v130
	v_fmamk_f32 v92, v92, 0x3e0293ee, v130
	v_fmamk_f32 v93, v93, 0x3e0293ee, v130
	v_fmamk_f32 v94, v94, 0x3e0293ee, v130
	v_fmamk_f32 v95, v95, 0x3e0293ee, v130
	v_fmamk_f32 v96, v96, 0x3e0293ee, v130
	v_fmac_f32_e32 v180, 0x3e0293ee, v97
	v_exp_f32_e32 v147, v82
	v_exp_f32_e32 v148, v83
	v_exp_f32_e32 v149, v84
	v_exp_f32_e32 v185, v85
	v_exp_f32_e32 v186, v86
	v_exp_f32_e32 v188, v87
	v_exp_f32_e32 v184, v88
	v_exp_f32_e32 v187, v89
	v_exp_f32_e32 v150, v90
	v_exp_f32_e32 v151, v91
	v_exp_f32_e32 v153, v92
	v_exp_f32_e32 v155, v93
	v_exp_f32_e32 v152, v94
	v_exp_f32_e32 v156, v95
	v_exp_f32_e32 v157, v96
	v_exp_f32_e32 v183, v180
	v_fma_f32 v145, v67, s84, v130
	v_fma_f32 v144, v66, s84, v130
	v_add_f32_e32 v66, v175, v176
	s_waitcnt lgkmcnt(0)
	v_fmac_f32_e32 v66, v173, v170
	v_add_f32_e32 v170, v181, v182
	s_add_i32 s78, s78, 2
	s_addk_i32 s79, 0x80
	v_fma_f32 v143, v69, s84, v130
	v_fma_f32 v142, v68, s84, v130
	v_fma_f32 v141, v71, s84, v130
	v_fma_f32 v140, v70, s84, v130
	v_fma_f32 v139, v73, s84, v130
	v_fma_f32 v138, v72, s84, v130
	v_fma_f32 v137, v75, s84, v130
	v_fma_f32 v136, v74, s84, v130
	v_fma_f32 v135, v77, s84, v130
	v_fma_f32 v134, v76, s84, v130
	v_fma_f32 v133, v79, s84, v130
	v_fma_f32 v132, v78, s84, v130
	v_fma_f32 v131, v81, s84, v130
	v_fma_f32 v130, v80, s84, v130
	v_fmac_f32_e32 v170, v66, v177
	v_add_u32_e32 v174, 0xffffff80, v174
	s_cmp_lt_u32 s10, s77
	v_lshl_add_u64 v[158:159], v[158:159], 0, s[66:67]
	s_waitcnt lgkmcnt(0)
	s_barrier
	s_cbranch_scc0 .LBB0_1312
	v_mov_b32_e32 v173, v146
	s_branch .LBB0_1294

; __device__ __forceinline__ void partialSM(f32x16& p0, f32x16& p1, float& m_reg, float& mn, float& alpha) {
;     ...
;     constexpr float C2 = 1.4426950408889634f * SCALE;
;     if (__builtin_expect(__all((pmax - m_reg) * SCALE <= THR), 1)) { mn = m_reg; alpha = 1.f; }
;     else { mn = fmaxf(m_reg, pmax); alpha = __builtin_amdgcn_exp2f((m_reg - mn) * C2); m_reg = mn; }
;     const float mnL = -mn * C2;
; #pragma unroll
;     for (int r = 0; r < 16; ++r) p0[r] = fmaf(p0[r], C2, mnL);
; #pragma unroll
;     for (int r = 0; r < 16; ++r) p1[r] = fmaf(p1[r], C2, mnL);
; __device__ __forceinline__ void finishSM(f32x16& p0, f32x16& p1, float alpha, float& l_reg, bf16x8& pa0, bf16x8& pa1, bf16x8& pa2, bf16x8& pa3) {
;     ...
;     float ps = 0;
; #pragma unroll
;     for (int r = 0; r < 16; ++r) ps += p0[r];
; #pragma unroll
;     for (int r = 0; r < 16; ++r) ps += p1[r];
;     { auto rr = __builtin_amdgcn_permlane32_swap(__float_as_uint(ps), __float_as_uint(ps), false, false);
;       ps = __uint_as_float(rr[0]) + __uint_as_float(rr[1]); }
;     l_reg = l_reg * alpha + ps;
.LBB0_1460:
	v_cndmask_b32_e64 v152, v80, v193, s[2:3]
	v_mul_f32_e32 v80, 0xbe0293ee, v152
	v_mov_b32_e32 v136, v80
	v_fmamk_f32 v81, v146, 0x3e0293ee, v80
	v_fmamk_f32 v97, v147, 0x3e0293ee, v80
	v_fmamk_f32 v132, v148, 0x3e0293ee, v80
	v_fmamk_f32 v85, v85, 0x3e0293ee, v80
	v_fmamk_f32 v86, v86, 0x3e0293ee, v80
	v_fmamk_f32 v87, v87, 0x3e0293ee, v80
	v_fmamk_f32 v88, v88, 0x3e0293ee, v80
	v_fmamk_f32 v89, v89, 0x3e0293ee, v80
	v_fmamk_f32 v90, v90, 0x3e0293ee, v80
	v_fmamk_f32 v91, v91, 0x3e0293ee, v80
	v_fmamk_f32 v92, v92, 0x3e0293ee, v80
	v_fmamk_f32 v93, v93, 0x3e0293ee, v80
	v_fmamk_f32 v94, v94, 0x3e0293ee, v80
	v_fmamk_f32 v95, v95, 0x3e0293ee, v80
	v_fmamk_f32 v133, v149, 0x3e0293ee, v80
	v_fmac_f32_e32 v136, 0x3e0293ee, v96
	v_exp_f32_e32 v146, v81
	v_exp_f32_e32 v147, v97
	v_exp_f32_e32 v148, v132
	v_exp_f32_e32 v170, v85
	v_exp_f32_e32 v171, v86
	v_exp_f32_e32 v173, v87
	v_exp_f32_e32 v149, v88
	v_exp_f32_e32 v172, v89
	v_exp_f32_e32 v154, v90
	v_exp_f32_e32 v156, v91
	v_exp_f32_e32 v157, v92
	v_exp_f32_e32 v160, v93
	v_exp_f32_e32 v155, v94
	v_exp_f32_e32 v158, v95
	v_exp_f32_e32 v159, v133
	v_exp_f32_e32 v161, v136
	v_fma_f32 v145, v67, s84, v80
	v_fma_f32 v144, v66, s84, v80
	v_add_f32_e32 v66, v190, v191
	v_fmac_f32_e32 v66, v189, v188
	v_add_f32_e32 v188, v0, v194
	s_add_i32 s2, s31, 2
	s_add_i32 s3, s31, 1
	v_fma_f32 v143, v69, s84, v80
	v_fma_f32 v142, v68, s84, v80
	v_fma_f32 v139, v71, s84, v80
	v_fma_f32 v138, v70, s84, v80
	v_fma_f32 v135, v73, s84, v80
	v_fma_f32 v134, v72, s84, v80
	v_fma_f32 v131, v83, s84, v80
	v_fma_f32 v130, v82, s84, v80
	v_fma_f32 v141, v75, s84, v80
	v_fma_f32 v140, v74, s84, v80
	v_fma_f32 v137, v77, s84, v80
	v_fma_f32 v136, v76, s84, v80
	v_fma_f32 v133, v79, s84, v80
	v_fma_f32 v132, v78, s84, v80
	v_fmac_f32_e32 v188, v66, v192
	s_cmp_le_u32 s3, s34
	v_lshl_add_u64 v[168:169], v[168:169], 0, s[66:67]
	s_waitcnt lgkmcnt(0)
	s_barrier
	s_cbranch_scc0 .LBB0_1462
	s_mov_b32 s31, s2
	v_mov_b32_e32 v189, v84
	s_branch .LBB0_1448

; __device__ __forceinline__ void partialSM(f32x16& p0, f32x16& p1, float& m_reg, float& mn, float& alpha) {
;     ...
;     constexpr float C2 = 1.4426950408889634f * SCALE;
;     if (__builtin_expect(__all((pmax - m_reg) * SCALE <= THR), 1)) { mn = m_reg; alpha = 1.f; }
;     else { mn = fmaxf(m_reg, pmax); alpha = __builtin_amdgcn_exp2f((m_reg - mn) * C2); m_reg = mn; }
;     const float mnL = -mn * C2;
; #pragma unroll
;     for (int r = 0; r < 16; ++r) p0[r] = fmaf(p0[r], C2, mnL);
; #pragma unroll
;     for (int r = 0; r < 16; ++r) p1[r] = fmaf(p1[r], C2, mnL);
; __device__ __forceinline__ void finishSM(f32x16& p0, f32x16& p1, float alpha, float& l_reg, bf16x8& pa0, bf16x8& pa1, bf16x8& pa2, bf16x8& pa3) {
;     ...
;     float ps = 0;
; #pragma unroll
;     for (int r = 0; r < 16; ++r) ps += p0[r];
; #pragma unroll
;     for (int r = 0; r < 16; ++r) ps += p1[r];
;     { auto rr = __builtin_amdgcn_permlane32_swap(__float_as_uint(ps), __float_as_uint(ps), false, false);
;       ps = __uint_as_float(rr[0]) + __uint_as_float(rr[1]); }
;     l_reg = l_reg * alpha + ps;
.LBB0_1605:
	v_cndmask_b32_e64 v152, v81, v192, s[2:3]
	v_mul_f32_e32 v132, 0xbe0293ee, v152
	v_mov_b32_e32 v136, v132
	v_fmamk_f32 v81, v146, 0x3e0293ee, v132
	v_fmamk_f32 v97, v147, 0x3e0293ee, v132
	v_fmamk_f32 v84, v84, 0x3e0293ee, v132
	v_fmamk_f32 v85, v85, 0x3e0293ee, v132
	v_fmamk_f32 v86, v86, 0x3e0293ee, v132
	v_fmamk_f32 v87, v87, 0x3e0293ee, v132
	v_fmamk_f32 v88, v88, 0x3e0293ee, v132
	v_fmamk_f32 v89, v89, 0x3e0293ee, v132
	v_fmamk_f32 v90, v90, 0x3e0293ee, v132
	v_fmamk_f32 v91, v91, 0x3e0293ee, v132
	v_fmamk_f32 v92, v92, 0x3e0293ee, v132
	v_fmamk_f32 v93, v93, 0x3e0293ee, v132
	v_fmamk_f32 v94, v94, 0x3e0293ee, v132
	v_fmamk_f32 v95, v95, 0x3e0293ee, v132
	v_fmamk_f32 v133, v148, 0x3e0293ee, v132
	v_fmac_f32_e32 v136, 0x3e0293ee, v96
	v_exp_f32_e32 v146, v81
	v_exp_f32_e32 v147, v97
	v_exp_f32_e32 v148, v84
	v_exp_f32_e32 v170, v85
	v_exp_f32_e32 v171, v86
	v_exp_f32_e32 v173, v87
	v_exp_f32_e32 v149, v88
	v_exp_f32_e32 v172, v89
	v_exp_f32_e32 v154, v90
	v_exp_f32_e32 v156, v91
	v_exp_f32_e32 v157, v92
	v_exp_f32_e32 v160, v93
	v_exp_f32_e32 v155, v94
	v_exp_f32_e32 v158, v95
	v_exp_f32_e32 v159, v133
	v_exp_f32_e32 v161, v136
	v_fma_f32 v145, v67, s84, v132
	v_fma_f32 v144, v66, s84, v132
	v_add_f32_e32 v66, v189, v190
	v_fmac_f32_e32 v66, v188, v187
	v_add_f32_e32 v187, v0, v193
	s_add_i32 s2, s27, 2
	s_add_i32 s3, s27, 1
	v_fma_f32 v143, v69, s84, v132
	v_fma_f32 v142, v68, s84, v132
	v_fma_f32 v139, v71, s84, v132
	v_fma_f32 v138, v70, s84, v132
	v_fma_f32 v135, v73, s84, v132
	v_fma_f32 v134, v72, s84, v132
	v_fma_f32 v131, v83, s84, v132
	v_fma_f32 v130, v82, s84, v132
	v_fma_f32 v141, v75, s84, v132
	v_fma_f32 v140, v74, s84, v132
	v_fma_f32 v137, v77, s84, v132
	v_fma_f32 v136, v76, s84, v132
	v_fma_f32 v133, v79, s84, v132
	v_fma_f32 v132, v78, s84, v132
	v_fmac_f32_e32 v187, v66, v191
	s_cmp_le_u32 s3, s26
	v_lshl_add_u64 v[168:169], v[168:169], 0, s[66:67]
	s_waitcnt lgkmcnt(0)
	s_barrier
	s_cbranch_scc0 .LBB0_1607
	s_mov_b32 s27, s2
	v_mov_b32_e32 v188, v80
	s_branch .LBB0_1593

; #define LAS __attribute__((address_space(3)))
; #define GAS __attribute__((address_space(1)))
; __device__ __forceinline__ int fresh_lane() { int l = (int)__builtin_amdgcn_mbcnt_hi(~0u, __builtin_amdgcn_mbcnt_lo(~0u, 0u)); asm volatile("" : "+v"(l)); return l; }
; __device__ __forceinline__ void final_phase(Frame& F) {
;     const int lane_ = fresh_lane();
;     const int gw = F.vcu * NWAVES + F.wave, NGW = F.G * NWAVES;
;     const bf16_t* H1 = (const bf16_t*)(F.ws + WS_H1); const bf16_t* Y = (const bf16_t*)(F.ws + WS_Y); const float* GATE = (const float*)(F.ws + WS_GATE); const int* SEI = (const int*)(F.ws + WS_SEI);
;     const float* g_fin = F.in[19]; volatile LAS int* tb = (volatile LAS int*)(F.lds + MOE_TB_OFF);
;     for (int t = gw; t < NX; t += NGW) {
;         const GAS u32x2* hr = (const GAS u32x2*)(H1 + (size_t)t * D) + lane_;
;         f32x4 v[8];
; #pragma unroll
;         for (int j = 0; j < 8; ++j) { const u32x2 w = hr[64 * j]; v[j] = (f32x4){__uint_as_float(w.x << 16), __uint_as_float(w.x & 0xffff0000u), __uint_as_float(w.y << 16), __uint_as_float(w.y & 0xffff0000u)}; }
;         const f32x4 gt = *(const f32x4*)(GATE + (size_t)t * 4);
;     ...
;         GAS f32x4* orow = (GAS f32x4*)(F.out + (size_t)t * D) + lane_; const GAS f32x4* gr = (const GAS f32x4*)g_fin + lane_;
; #pragma unroll
;         for (int j = 0; j < 8; ++j) { const f32x4 g = gr[64 * j]; orow[64 * j] = v[j] * rs * g; }
.LBB0_2293:
	s_or_b64 exec, exec, s[0:1]
	v_readlane_b32 s0, v254, 2
	s_lshl_b32 s0, s0, 3
	s_add_i32 s2, s0, s90
	v_mov_b32_e32 v0, v2
	s_cmpk_gt_i32 s2, 0x3fff
	s_waitcnt lgkmcnt(0)
	s_barrier
	s_cbranch_scc1 .LBB0_2296
	v_and_b32_e32 v3, 64, v2
	v_add_u32_e32 v3, 64, v3
	v_xor_b32_e32 v4, 1, v2
	v_cmp_lt_i32_e32 vcc, v4, v3
	v_ashrrev_i32_e32 v1, 31, v0
	v_readlane_b32 s8, v254, 3
	v_cndmask_b32_e32 v4, v2, v4, vcc
	v_lshlrev_b32_e32 v48, 2, v4
	v_xor_b32_e32 v4, 2, v2
	v_cmp_lt_i32_e32 vcc, v4, v3
	v_readlane_b32 s9, v254, 4
	v_readlane_b32 s14, v254, 9
	v_cndmask_b32_e32 v4, v2, v4, vcc
	v_lshlrev_b32_e32 v49, 2, v4
	v_xor_b32_e32 v4, 4, v2
	v_cmp_lt_i32_e32 vcc, v4, v3
	v_readlane_b32 s15, v254, 10
	s_lshl_b32 s4, s93, 3
	v_cndmask_b32_e32 v4, v2, v4, vcc
	v_lshlrev_b32_e32 v50, 2, v4
	v_xor_b32_e32 v4, 8, v2
	v_cmp_lt_i32_e32 vcc, v4, v3
	s_mov_b64 s[8:9], 0x1400
	s_add_u32 s6, s70, 0x7cbc7000
	v_cndmask_b32_e32 v4, v2, v4, vcc
	v_lshlrev_b32_e32 v51, 2, v4
	v_xor_b32_e32 v4, 16, v2
	v_cmp_lt_i32_e32 vcc, v4, v3
	s_addc_u32 s7, s71, 0
	v_readlane_b32 s10, v254, 5
	v_cndmask_b32_e32 v4, v2, v4, vcc
	v_lshlrev_b32_e32 v52, 2, v4
	v_xor_b32_e32 v4, 32, v2
	v_cmp_lt_i32_e32 vcc, v4, v3
	v_readlane_b32 s11, v254, 6
	v_readlane_b32 s12, v254, 7
	v_cndmask_b32_e32 v2, v2, v4, vcc
	v_lshlrev_b32_e32 v53, 2, v2
	v_lshlrev_b64 v[2:3], 4, v[0:1]
	v_lshl_add_u64 v[8:9], s[14:15], 0, v[2:3]
	v_lshl_add_u64 v[12:13], v[8:9], 0, s[8:9]
	s_mov_b64 s[8:9], 0x1800
	v_readlane_b32 s13, v254, 8
	v_lshl_add_u64 v[14:15], v[8:9], 0, s[8:9]
	s_mov_b64 s[8:9], 0x1c00
	s_ashr_i32 s3, s2, 31
	s_ashr_i32 s5, s4, 31
	v_lshl_add_u64 v[16:17], v[8:9], 0, s[8:9]
	s_lshl_b64 s[8:9], s[2:3], 4
	s_lshl_b64 s[10:11], s[4:5], 4
	s_lshl_b64 s[12:13], s[2:3], 13
	s_add_u32 s12, s68, s12
	s_addc_u32 s13, s69, s13
	s_mov_b64 s[0:1], 0x1000
	v_lshl_add_u64 v[2:3], s[12:13], 0, v[2:3]
	v_lshl_add_u64 v[10:11], v[8:9], 0, s[0:1]
	v_lshl_add_u64 v[18:19], v[2:3], 0, s[0:1]
	s_lshl_b64 s[0:1], s[2:3], 12
	s_lshl_b64 s[12:13], s[4:5], 13
	v_lshl_add_u64 v[20:21], v[0:1], 3, s[0:1]
	s_lshl_b64 s[14:15], s[4:5], 12
	s_mov_b32 s17, 0
	v_mov_b32_e32 v54, 0x6a947000
	v_mov_b32_e32 v55, 0x6a987000
	s_add_i32 s3, 0, 0x20400
	v_lshlrev_b64 v[22:23], 3, v[0:1]
	v_mov_b32_e32 v56, 0x3727c5ac
	s_mov_b32 s5, 0xf800000
	v_mov_b32_e32 v57, 0x260
	global_load_dwordx4 v[160:163], v[8:9], off offset:1024
	global_load_dwordx4 v[164:167], v[8:9], off offset:2048
	global_load_dwordx4 v[168:171], v[8:9], off offset:3072
	global_load_dwordx4 v[172:175], v[10:11], off
	global_load_dwordx4 v[176:179], v[12:13], off
	global_load_dwordx4 v[180:183], v[14:15], off
	global_load_dwordx4 v[184:187], v[16:17], off
	s_waitcnt vmcnt(0)
.LBB0_2295:
	s_add_u32 s0, s70, s8
	s_addc_u32 s1, s71, s9
	global_load_dwordx4 v[38:41], v55, s[0:1]
	global_load_dwordx4 v[0:3], v54, s[0:1]
	v_lshl_add_u64 v[4:5], s[70:71], 0, v[20:21]
	v_add_co_u32_e32 v24, vcc, 0x5e947000, v4
	s_add_i32 s2, s2, s4
	s_nop 0
	v_addc_co_u32_e32 v25, vcc, 0, v5, vcc
	global_load_dwordx2 v[32:33], v[24:25], off offset:2560
	global_load_dwordx2 v[30:31], v[24:25], off offset:3072
	global_load_dwordx2 v[36:37], v[24:25], off offset:3584
	global_load_dwordx2 v[34:35], v[24:25], off
	global_load_dwordx2 v[4:5], v[24:25], off offset:2048
	global_load_dwordx2 v[28:29], v[24:25], off offset:512
	global_load_dwordx2 v[26:27], v[24:25], off offset:1024
	global_load_dwordx2 v[6:7], v[24:25], off offset:1536
	v_lshl_add_u64 v[20:21], v[20:21], 0, s[14:15]
	s_waitcnt vmcnt(9)
	v_readfirstlane_b32 s0, v38
	s_ashr_i32 s19, s0, 16
	s_lshl_b32 s19, s19, 2
	s_add_i32 s19, s3, s19
	s_waitcnt vmcnt(5)
	v_lshlrev_b32_e32 v158, 16, v36
	v_and_b32_e32 v43, 0xffff0000, v36
	v_lshlrev_b32_e32 v47, 16, v37
	v_and_b32_e32 v45, 0xffff0000, v37
	s_waitcnt vmcnt(4)
	v_lshlrev_b32_e32 v36, 16, v34
	v_and_b32_e32 v37, 0xffff0000, v34
	v_lshlrev_b32_e32 v58, 16, v35
	v_and_b32_e32 v59, 0xffff0000, v35
	s_waitcnt vmcnt(3)
	v_lshlrev_b32_e32 v34, 16, v4
	v_and_b32_e32 v35, 0xffff0000, v4
	v_mov_b32_e32 v4, s19
	ds_read_b32 v4, v4
	v_readfirstlane_b32 s1, v39
	v_lshlrev_b32_e32 v68, 16, v5
	v_and_b32_e32 v69, 0xffff0000, v5
	v_readfirstlane_b32 s16, v40
	s_waitcnt lgkmcnt(0)
	v_ashrrev_i32_e32 v5, 31, v4
	s_lshl_b32 s0, s0, 12
	s_ashr_i32 s20, s1, 16
	v_lshlrev_b64 v[4:5], 20, v[4:5]
	s_ashr_i32 s21, s16, 16
	s_lshl_b32 s22, s16, 12
	s_and_b32 s16, s0, 0xffff000
	s_lshl_b32 s0, s20, 2
	v_lshl_add_u64 v[4:5], s[6:7], 0, v[4:5]
	s_add_i32 s0, s3, s0
	v_lshl_add_u64 v[4:5], v[4:5], 0, s[16:17]
	s_waitcnt vmcnt(0)
	v_lshlrev_b32_e32 v64, 16, v6
	v_and_b32_e32 v66, 0xffff0000, v6
	v_mov_b32_e32 v6, s0
	v_lshl_add_u64 v[4:5], v[4:5], 0, v[22:23]
	global_load_dwordx2 v[70:71], v[4:5], off offset:3072
	global_load_dwordx2 v[72:73], v[4:5], off offset:3584
	global_load_dwordx2 v[74:75], v[4:5], off offset:2048
	global_load_dwordx2 v[76:77], v[4:5], off offset:2560
	global_load_dwordx2 v[78:79], v[4:5], off
	global_load_dwordx2 v[80:81], v[4:5], off offset:512
	global_load_dwordx2 v[82:83], v[4:5], off offset:1024
	global_load_dwordx2 v[84:85], v[4:5], off offset:1536
	ds_read_b32 v4, v6
	s_lshl_b32 s1, s1, 12
	s_lshl_b32 s20, s21, 2
	s_and_b32 s16, s1, 0xffff000
	s_add_i32 s20, s3, s20
	s_waitcnt lgkmcnt(0)
; #define GAS __attribute__((address_space(1)))
; __device__ __forceinline__ void final_phase(Frame& F) {
;     ...
;         for (int j = 0; j < 8; ++j) { const u32x2 w = hr[64 * j]; v[j] = (f32x4){__uint_as_float(w.x << 16), __uint_as_float(w.x & 0xffff0000u), __uint_as_float(w.y << 16), __uint_as_float(w.y & 0xffff0000u)}; }
;         const f32x4 gt = *(const f32x4*)(GATE + (size_t)t * 4);
;         typedef int i32x4 __attribute__((ext_vector_type(4)));
;         const i32x4 se = *(const i32x4*)(SEI + (size_t)t * 4);
; #pragma unroll
;         for (int k = 0; k < 4; ++k) { const int e = se[k] >> 16, i = se[k] & 0xffff; const size_t slot = (size_t)tb[e] * 256 + i; const float gk = gt[k];
;             const GAS u32x2* yr = (const GAS u32x2*)(Y + slot * D) + lane_;
; #pragma unroll
;             for (int j = 0; j < 8; ++j) { const u32x2 w = yr[64 * j];
;                 v[j][0] += gk * __uint_as_float(w.x << 16); v[j][1] += gk * __uint_as_float(w.x & 0xffff0000u); v[j][2] += gk * __uint_as_float(w.y << 16); v[j][3] += gk * __uint_as_float(w.y & 0xffff0000u); } }
	v_ashrrev_i32_e32 v5, 31, v4
	v_lshlrev_b64 v[4:5], 20, v[4:5]
	v_lshl_add_u64 v[4:5], s[6:7], 0, v[4:5]
	v_lshl_add_u64 v[4:5], v[4:5], 0, s[16:17]
	v_lshlrev_b32_e32 v65, 16, v7
	v_and_b32_e32 v67, 0xffff0000, v7
	v_mov_b32_e32 v7, s20
	v_lshl_add_u64 v[4:5], v[4:5], 0, v[22:23]
	global_load_dwordx2 v[86:87], v[4:5], off
	global_load_dwordx2 v[88:89], v[4:5], off offset:512
	global_load_dwordx2 v[90:91], v[4:5], off offset:1024
	global_load_dwordx2 v[92:93], v[4:5], off offset:1536
	global_load_dwordx2 v[94:95], v[4:5], off offset:2048
	global_load_dwordx2 v[96:97], v[4:5], off offset:2560
	global_load_dwordx2 v[98:99], v[4:5], off offset:3072
	global_load_dwordx2 v[100:101], v[4:5], off offset:3584
	ds_read_b32 v4, v7
	v_readfirstlane_b32 s18, v41
	s_ashr_i32 s23, s18, 16
	s_lshl_b32 s21, s23, 2
	s_and_b32 s16, s22, 0xffff000
	s_waitcnt lgkmcnt(0)
	v_ashrrev_i32_e32 v5, 31, v4
	v_lshlrev_b64 v[4:5], 20, v[4:5]
	v_lshl_add_u64 v[4:5], s[6:7], 0, v[4:5]
	s_add_i32 s21, s3, s21
	v_lshl_add_u64 v[4:5], v[4:5], 0, s[16:17]
	v_mov_b32_e32 v118, s21
	v_lshl_add_u64 v[4:5], v[4:5], 0, v[22:23]
	global_load_dwordx2 v[102:103], v[4:5], off
	global_load_dwordx2 v[104:105], v[4:5], off offset:512
	global_load_dwordx2 v[106:107], v[4:5], off offset:1024
	global_load_dwordx2 v[108:109], v[4:5], off offset:1536
	global_load_dwordx2 v[110:111], v[4:5], off offset:2048
	global_load_dwordx2 v[112:113], v[4:5], off offset:2560
	global_load_dwordx2 v[114:115], v[4:5], off offset:3072
	global_load_dwordx2 v[116:117], v[4:5], off offset:3584
	ds_read_b32 v118, v118
	s_lshl_b32 s18, s18, 12
	s_and_b32 s16, s18, 0xffff000
	global_load_dwordx4 v[4:7], v[8:9], off
	v_lshlrev_b32_e32 v46, 16, v30
	s_waitcnt lgkmcnt(0)
	v_ashrrev_i32_e32 v119, 31, v118
	v_lshlrev_b64 v[118:119], 20, v[118:119]
	v_lshl_add_u64 v[118:119], s[6:7], 0, v[118:119]
	v_lshl_add_u64 v[118:119], v[118:119], 0, s[16:17]
	v_lshl_add_u64 v[118:119], v[118:119], 0, v[22:23]
	global_load_dwordx2 v[120:121], v[118:119], off
	global_load_dwordx2 v[122:123], v[118:119], off offset:512
	global_load_dwordx2 v[124:125], v[118:119], off offset:1024
	global_load_dwordx2 v[126:127], v[118:119], off offset:1536
	global_load_dwordx2 v[128:129], v[118:119], off offset:2048
	global_load_dwordx2 v[130:131], v[118:119], off offset:2560
	global_load_dwordx2 v[132:133], v[118:119], off offset:3072
	s_nop 0
	global_load_dwordx2 v[118:119], v[118:119], off offset:3584
	v_lshlrev_b32_e32 v44, 16, v31
	v_lshlrev_b32_e32 v38, 16, v32
	v_lshlrev_b32_e32 v61, 16, v29
	v_lshlrev_b32_e32 v60, 16, v28
	v_and_b32_e32 v29, 0xffff0000, v29
	v_and_b32_e32 v28, 0xffff0000, v28
	v_lshlrev_b32_e32 v63, 16, v27
	v_lshlrev_b32_e32 v62, 16, v26
	v_and_b32_e32 v27, 0xffff0000, v27
	v_and_b32_e32 v26, 0xffff0000, v26
	v_and_b32_e32 v42, 0xffff0000, v33
	v_mov_b32_e32 v40, v2
	v_mov_b32_e32 v41, v0
	v_and_b32_e32 v32, 0xffff0000, v32
	v_lshlrev_b32_e32 v33, 16, v33
	v_and_b32_e32 v31, 0xffff0000, v31
	v_and_b32_e32 v30, 0xffff0000, v30
	v_mov_b32_e32 v24, v3
	v_mov_b32_e32 v25, v3
	v_mov_b32_e32 v39, v2
	s_add_u32 s8, s8, s10
	s_addc_u32 s9, s9, s11
	s_cmpk_lt_i32 s2, 0x4000
	s_waitcnt vmcnt(32)
	v_lshlrev_b32_e32 v135, 16, v70
	v_lshlrev_b32_e32 v137, 16, v71
	s_waitcnt vmcnt(30)
	v_lshlrev_b32_e32 v134, 16, v74
	v_and_b32_e32 v74, 0xffff0000, v74
	v_lshlrev_b32_e32 v152, 16, v75
	v_and_b32_e32 v153, 0xffff0000, v75
	v_fmac_f32_e32 v46, v0, v135
	v_lshlrev_b32_e32 v139, 16, v72
	s_waitcnt vmcnt(29)
	v_lshlrev_b32_e32 v136, 16, v76
	v_lshlrev_b32_e32 v155, 16, v73
	v_and_b32_e32 v73, 0xffff0000, v73
	v_and_b32_e32 v157, 0xffff0000, v72
	v_fmac_f32_e32 v44, v0, v137
	v_and_b32_e32 v76, 0xffff0000, v76
	v_lshlrev_b32_e32 v138, 16, v77
	v_and_b32_e32 v140, 0xffff0000, v77
	v_and_b32_e32 v70, 0xffff0000, v70
	v_and_b32_e32 v142, 0xffff0000, v71
	s_waitcnt vmcnt(20)
	v_lshlrev_b32_e32 v135, 16, v94
	v_and_b32_e32 v75, 0xffff0000, v94
	s_waitcnt vmcnt(19)
	v_lshlrev_b32_e32 v137, 16, v96
	s_waitcnt vmcnt(18)
	v_lshlrev_b32_e32 v72, 16, v99
	v_pk_mul_f32 v[134:135], v[0:1], v[134:135]
	v_pk_mul_f32 v[74:75], v[0:1], v[74:75]
	v_lshlrev_b32_e32 v144, 16, v78
	v_and_b32_e32 v145, 0xffff0000, v78
	v_lshlrev_b32_e32 v78, 16, v79
	v_and_b32_e32 v79, 0xffff0000, v79
	v_lshlrev_b32_e32 v147, 16, v81
	v_lshlrev_b32_e32 v146, 16, v80
	v_and_b32_e32 v81, 0xffff0000, v81
	v_and_b32_e32 v80, 0xffff0000, v80
	v_lshlrev_b32_e32 v149, 16, v83
	v_lshlrev_b32_e32 v148, 16, v82
	v_and_b32_e32 v83, 0xffff0000, v83
	v_and_b32_e32 v82, 0xffff0000, v82
	v_lshlrev_b32_e32 v151, 16, v85
	v_lshlrev_b32_e32 v150, 16, v84
	v_and_b32_e32 v85, 0xffff0000, v85
	v_and_b32_e32 v84, 0xffff0000, v84
	v_mul_f32_e32 v159, v0, v139
	v_and_b32_e32 v77, 0xffff0000, v96
	v_lshlrev_b32_e32 v139, 16, v97
	v_and_b32_e32 v141, 0xffff0000, v97
	v_and_b32_e32 v71, 0xffff0000, v98
	v_and_b32_e32 v143, 0xffff0000, v99
	v_pk_mul_f32 v[136:137], v[0:1], v[136:137]
	v_pk_fma_f32 v[44:45], v[0:1], v[72:73], v[44:45] op_sel:[1,0,0] op_sel_hi:[0,1,1]
	v_mov_b32_e32 v72, v134
	v_mov_b32_e32 v73, v74
	v_pk_fma_f32 v[36:37], v[0:1], v[144:145], v[36:37] op_sel_hi:[0,1,1]
	v_pk_fma_f32 v[58:59], v[0:1], v[78:79], v[58:59] op_sel_hi:[0,1,1]
	v_pk_fma_f32 v[60:61], v[0:1], v[146:147], v[60:61] op_sel_hi:[0,1,1]
	v_pk_fma_f32 v[28:29], v[0:1], v[80:81], v[28:29] op_sel_hi:[0,1,1]
	v_pk_fma_f32 v[62:63], v[0:1], v[148:149], v[62:63] op_sel_hi:[0,1,1]
	v_pk_fma_f32 v[26:27], v[0:1], v[82:83], v[26:27] op_sel_hi:[0,1,1]
	v_pk_fma_f32 v[64:65], v[0:1], v[150:151], v[64:65] op_sel_hi:[0,1,1]
	v_pk_fma_f32 v[66:67], v[0:1], v[84:85], v[66:67] op_sel_hi:[0,1,1]
	v_pk_fma_f32 v[68:69], v[0:1], v[152:153], v[68:69] op_sel_hi:[0,1,1]
	s_waitcnt vmcnt(17)
; #define GAS __attribute__((address_space(1)))
; __device__ __forceinline__ void final_phase(Frame& F) {
;     ...
;         for (int k = 0; k < 4; ++k) { const int e = se[k] >> 16, i = se[k] & 0xffff; const size_t slot = (size_t)tb[e] * 256 + i; const float gk = gt[k];
;             const GAS u32x2* yr = (const GAS u32x2*)(Y + slot * D) + lane_;
; #pragma unroll
;             for (int j = 0; j < 8; ++j) { const u32x2 w = yr[64 * j];
;                 v[j][0] += gk * __uint_as_float(w.x << 16); v[j][1] += gk * __uint_as_float(w.x & 0xffff0000u); v[j][2] += gk * __uint_as_float(w.y << 16); v[j][3] += gk * __uint_as_float(w.y & 0xffff0000u); } }
	v_lshlrev_b32_e32 v96, 16, v100
	v_lshlrev_b32_e32 v78, 16, v86
	v_and_b32_e32 v79, 0xffff0000, v86
	v_lshlrev_b32_e32 v80, 16, v87
	v_and_b32_e32 v81, 0xffff0000, v87
	v_lshlrev_b32_e32 v83, 16, v89
	v_lshlrev_b32_e32 v82, 16, v88
	v_and_b32_e32 v85, 0xffff0000, v89
	v_and_b32_e32 v84, 0xffff0000, v88
	v_lshlrev_b32_e32 v87, 16, v91
	v_lshlrev_b32_e32 v86, 16, v90
	v_and_b32_e32 v89, 0xffff0000, v91
	v_and_b32_e32 v88, 0xffff0000, v90
	v_lshlrev_b32_e32 v91, 16, v93
	v_lshlrev_b32_e32 v90, 16, v92
	v_and_b32_e32 v93, 0xffff0000, v93
	v_and_b32_e32 v92, 0xffff0000, v92
	v_lshlrev_b32_e32 v94, 16, v95
	v_and_b32_e32 v95, 0xffff0000, v95
	v_lshlrev_b32_e32 v154, 16, v98
	v_pk_mul_f32 v[76:77], v[0:1], v[76:77]
	v_pk_mul_f32 v[138:139], v[0:1], v[138:139]
	v_pk_mul_f32 v[140:141], v[0:1], v[140:141]
	v_pk_mul_f32 v[70:71], v[0:1], v[70:71]
	v_pk_mul_f32 v[142:143], v[0:1], v[142:143]
	v_add_f32_e32 v38, v136, v38
	v_mov_b32_e32 v74, v135
	v_pk_add_f32 v[34:35], v[72:73], v[34:35]
	v_lshlrev_b32_e32 v97, 16, v101
	v_mul_f32_e32 v144, v1, v96
	v_pk_fma_f32 v[36:37], v[0:1], v[78:79], v[36:37] op_sel:[1,0,0]
	v_pk_fma_f32 v[58:59], v[0:1], v[80:81], v[58:59] op_sel:[1,0,0]
	v_pk_fma_f32 v[60:61], v[0:1], v[82:83], v[60:61] op_sel:[1,0,0]
	v_pk_fma_f32 v[28:29], v[0:1], v[84:85], v[28:29] op_sel:[1,0,0]
	v_pk_fma_f32 v[62:63], v[0:1], v[86:87], v[62:63] op_sel:[1,0,0]
	v_pk_fma_f32 v[26:27], v[0:1], v[88:89], v[26:27] op_sel:[1,0,0]
	v_pk_fma_f32 v[64:65], v[0:1], v[90:91], v[64:65] op_sel:[1,0,0]
	v_pk_fma_f32 v[66:67], v[0:1], v[92:93], v[66:67] op_sel:[1,0,0]
	v_pk_fma_f32 v[68:69], v[0:1], v[94:95], v[68:69] op_sel:[1,0,0]
	v_pk_fma_f32 v[46:47], v[0:1], v[154:155], v[46:47] op_sel:[1,0,0] op_sel_hi:[0,1,1]
	v_mov_b32_e32 v0, v2
	v_add_f32_e32 v80, v140, v42
	v_mov_b32_e32 v78, v76
	v_mov_b32_e32 v79, v138
	v_mov_b32_e32 v138, v77
	v_mov_b32_e32 v76, v70
	v_mov_b32_e32 v77, v142
	v_add_f32_e32 v42, v38, v137
	v_pk_add_f32 v[34:35], v[34:35], v[74:75]
	s_waitcnt vmcnt(16)
	v_lshlrev_b32_e32 v72, 16, v102
	v_and_b32_e32 v73, 0xffff0000, v102
	v_lshlrev_b32_e32 v74, 16, v103
	v_and_b32_e32 v75, 0xffff0000, v103
	s_waitcnt vmcnt(15)
	v_and_b32_e32 v93, 0xffff0000, v105
	v_and_b32_e32 v92, 0xffff0000, v104
	s_waitcnt vmcnt(14)
	v_and_b32_e32 v103, 0xffff0000, v107
	v_and_b32_e32 v102, 0xffff0000, v106
	s_waitcnt vmcnt(11)
	v_lshlrev_b32_e32 v156, 16, v112
	s_waitcnt vmcnt(10)
	v_lshlrev_b32_e32 v96, 16, v114
	v_and_b32_e32 v99, 0xffff0000, v101
	v_add_f32_e32 v38, v80, v141
	v_pk_add_f32 v[32:33], v[78:79], v[32:33]
	v_pk_add_f32 v[30:31], v[76:77], v[30:31]
	s_waitcnt vmcnt(9)
	v_and_b32_e32 v70, 0xffff0000, v116
	v_lshlrev_b32_e32 v76, 16, v110
	v_and_b32_e32 v78, 0xffff0000, v110
	v_and_b32_e32 v80, 0xffff0000, v112
	v_lshlrev_b32_e32 v82, 16, v113
	v_and_b32_e32 v84, 0xffff0000, v113
	v_and_b32_e32 v86, 0xffff0000, v114
	v_and_b32_e32 v88, 0xffff0000, v115
	v_lshlrev_b32_e32 v91, 16, v105
	v_lshlrev_b32_e32 v90, 16, v104
	v_lshlrev_b32_e32 v95, 16, v107
	v_lshlrev_b32_e32 v94, 16, v106
	v_lshlrev_b32_e32 v105, 16, v109
	v_lshlrev_b32_e32 v104, 16, v108
	v_and_b32_e32 v107, 0xffff0000, v109
	v_and_b32_e32 v106, 0xffff0000, v108
	v_lshlrev_b32_e32 v108, 16, v111
	v_and_b32_e32 v109, 0xffff0000, v111
	v_lshlrev_b32_e32 v98, 16, v115
	v_pk_fma_f32 v[36:37], v[2:3], v[72:73], v[36:37] op_sel_hi:[0,1,1]
	v_pk_fma_f32 v[58:59], v[2:3], v[74:75], v[58:59] op_sel_hi:[0,1,1]
	v_pk_fma_f32 v[28:29], v[2:3], v[92:93], v[28:29] op_sel_hi:[0,1,1]
	v_pk_fma_f32 v[26:27], v[2:3], v[102:103], v[26:27] op_sel_hi:[0,1,1]
	v_pk_fma_f32 v[40:41], v[40:41], v[156:157], v[42:43]
	v_pk_fma_f32 v[42:43], v[0:1], v[96:97], v[46:47]
	s_waitcnt vmcnt(7)
	v_lshlrev_b32_e32 v46, 16, v120
	v_and_b32_e32 v47, 0xffff0000, v120
	v_lshlrev_b32_e32 v72, 16, v121
	v_and_b32_e32 v73, 0xffff0000, v121
	s_waitcnt vmcnt(3)
	v_lshlrev_b32_e32 v77, 16, v128
	v_and_b32_e32 v79, 0xffff0000, v128
	s_waitcnt vmcnt(2)
	v_and_b32_e32 v81, 0xffff0000, v130
	v_lshlrev_b32_e32 v83, 16, v131
	v_and_b32_e32 v85, 0xffff0000, v131
	s_waitcnt vmcnt(1)
	v_and_b32_e32 v87, 0xffff0000, v132
	v_and_b32_e32 v89, 0xffff0000, v133
	v_and_b32_e32 v93, 0xffff0000, v123
	v_and_b32_e32 v92, 0xffff0000, v122
	v_and_b32_e32 v97, 0xffff0000, v125
	v_and_b32_e32 v96, 0xffff0000, v124
	v_mov_b32_e32 v142, v71
	v_mul_f32_e32 v115, v2, v70
	v_pk_fma_f32 v[60:61], v[2:3], v[90:91], v[60:61] op_sel_hi:[0,1,1]
	v_pk_fma_f32 v[62:63], v[2:3], v[94:95], v[62:63] op_sel_hi:[0,1,1]
	v_pk_fma_f32 v[64:65], v[2:3], v[104:105], v[64:65] op_sel_hi:[0,1,1]
	v_pk_fma_f32 v[66:67], v[2:3], v[106:107], v[66:67] op_sel_hi:[0,1,1]
	v_pk_fma_f32 v[68:69], v[2:3], v[108:109], v[68:69] op_sel_hi:[0,1,1]
	v_pk_fma_f32 v[44:45], v[0:1], v[98:99], v[44:45]
	s_waitcnt vmcnt(0)
; __device__ __forceinline__ void final_phase(Frame& F) {
;     ...
;             for (int j = 0; j < 8; ++j) { const u32x2 w = yr[64 * j];
;                 v[j][0] += gk * __uint_as_float(w.x << 16); v[j][1] += gk * __uint_as_float(w.x & 0xffff0000u); v[j][2] += gk * __uint_as_float(w.y << 16); v[j][3] += gk * __uint_as_float(w.y & 0xffff0000u); } }
;         float s = 0.f;
; #pragma unroll
;         for (int j = 0; j < 8; ++j) s += (v[j][0] * v[j][0] + v[j][1] * v[j][1]) + (v[j][2] * v[j][2] + v[j][3] * v[j][3]);
;         float rs = 1.0f / sqrtf(wave_sum(s) * (1.0f / D) + EPS);
	v_lshlrev_b32_e32 v70, 16, v118
	v_lshlrev_b32_e32 v91, 16, v123
	v_lshlrev_b32_e32 v90, 16, v122
	v_lshlrev_b32_e32 v95, 16, v125
	v_lshlrev_b32_e32 v94, 16, v124
	v_lshlrev_b32_e32 v99, 16, v127
	v_lshlrev_b32_e32 v98, 16, v126
	v_and_b32_e32 v103, 0xffff0000, v127
	v_and_b32_e32 v102, 0xffff0000, v126
	v_lshlrev_b32_e32 v104, 16, v129
	v_and_b32_e32 v105, 0xffff0000, v129
	v_pk_fma_f32 v[36:37], v[24:25], v[46:47], v[36:37] op_sel_hi:[0,1,1]
	v_pk_fma_f32 v[46:47], v[24:25], v[72:73], v[58:59] op_sel_hi:[0,1,1]
	v_pk_mul_f32 v[58:59], v[2:3], v[76:77]
	v_pk_mul_f32 v[72:73], v[2:3], v[78:79]
	v_pk_mul_f32 v[76:77], v[2:3], v[80:81]
	v_pk_mul_f32 v[78:79], v[2:3], v[82:83]
	v_pk_mul_f32 v[80:81], v[2:3], v[84:85]
	v_pk_mul_f32 v[82:83], v[2:3], v[86:87]
	v_pk_mul_f32 v[84:85], v[2:3], v[88:89]
	v_pk_fma_f32 v[28:29], v[24:25], v[92:93], v[28:29] op_sel_hi:[0,1,1]
	v_pk_fma_f32 v[26:27], v[24:25], v[96:97], v[26:27] op_sel_hi:[0,1,1]
	v_pk_add_f32 v[32:33], v[32:33], v[138:139]
	v_pk_add_f32 v[30:31], v[30:31], v[142:143]
	v_lshlrev_b32_e32 v71, 16, v116
	v_mul_f32_e32 v107, v3, v70
	v_pk_fma_f32 v[60:61], v[24:25], v[90:91], v[60:61] op_sel_hi:[0,1,1]
	v_pk_fma_f32 v[62:63], v[24:25], v[94:95], v[62:63] op_sel_hi:[0,1,1]
	v_pk_fma_f32 v[64:65], v[24:25], v[98:99], v[64:65] op_sel_hi:[0,1,1]
	v_pk_fma_f32 v[66:67], v[24:25], v[102:103], v[66:67] op_sel_hi:[0,1,1]
	v_pk_fma_f32 v[68:69], v[24:25], v[104:105], v[68:69] op_sel_hi:[0,1,1]
	v_mov_b32_e32 v90, v58
	v_mov_b32_e32 v91, v72
	v_mov_b32_e32 v72, v59
	v_mov_b32_e32 v58, v76
	v_mov_b32_e32 v59, v78
	v_mov_b32_e32 v78, v77
	v_add_f32_e32 v24, v38, v80
	v_mov_b32_e32 v76, v82
	v_mov_b32_e32 v77, v84
	v_mov_b32_e32 v84, v83
	v_pk_mul_f32 v[82:83], v[28:29], v[28:29]
	v_pk_mul_f32 v[92:93], v[26:27], v[26:27]
	v_mul_f32_e32 v38, v37, v37
	v_mul_f32_e32 v70, v47, v47
	v_and_b32_e32 v101, 0xffff0000, v100
	v_mov_b32_e32 v0, v3
	v_lshlrev_b32_e32 v100, 16, v130
	v_pk_add_f32 v[34:35], v[34:35], v[90:91]
	v_pk_add_f32 v[32:33], v[32:33], v[58:59]
	v_pk_add_f32 v[30:31], v[30:31], v[76:77]
	v_pk_fma_f32 v[58:59], v[60:61], v[60:61], v[82:83]
	v_pk_fma_f32 v[76:77], v[62:63], v[62:63], v[92:93]
	v_pk_fma_f32 v[90:91], v[36:37], v[36:37], v[38:39] op_sel_hi:[1,1,0]
	v_pk_fma_f32 v[92:93], v[46:47], v[46:47], v[70:71] op_sel_hi:[1,1,0]
	v_pk_fma_f32 v[40:41], v[0:1], v[100:101], v[40:41]
	v_pk_add_f32 v[34:35], v[34:35], v[72:73]
	v_mov_b32_e32 v91, v159
	v_mov_b32_e32 v93, v158
	v_pk_add_f32 v[58:59], v[58:59], v[58:59] op_sel:[0,1] op_sel_hi:[1,0]
	v_and_b32_e32 v75, 0xffff0000, v118
	v_pk_mul_f32 v[94:95], v[66:67], v[66:67]
	v_mov_b32_e32 v114, v40
	v_pk_add_f32 v[32:33], v[32:33], v[78:79]
	v_pk_add_f32 v[90:91], v[90:91], v[92:93]
	v_mov_b32_e32 v59, v144
	v_mov_b32_e32 v70, v35
	v_lshlrev_b32_e32 v111, 16, v117
	v_and_b32_e32 v113, 0xffff0000, v117
	v_lshlrev_b32_e32 v74, 16, v119
	v_lshlrev_b32_e32 v110, 16, v132
	v_lshlrev_b32_e32 v112, 16, v133
	v_mov_b32_e32 v1, v75
	v_mul_f32_e32 v0, v69, v69
	v_pk_mul_f32 v[96:97], v[40:41], v[40:41]
	v_add_f32_e32 v24, v24, v81
	v_pk_fma_f32 v[80:81], v[64:65], v[64:65], v[94:95]
	v_pk_add_f32 v[94:95], v[40:41], v[114:115]
	v_pk_add_f32 v[30:31], v[30:31], v[84:85]
	v_pk_add_f32 v[72:73], v[76:77], v[76:77] op_sel:[0,1] op_sel_hi:[1,0]
	v_pk_mul_f32 v[84:85], v[34:35], v[34:35]
	v_pk_mul_f32 v[98:99], v[32:33], v[32:33]
	v_pk_add_f32 v[58:59], v[90:91], v[58:59]
	v_pk_mul_f32 v[90:91], v[2:3], v[70:71] op_sel_hi:[0,1]
	v_and_b32_e32 v106, 0xffff0000, v119
	v_mul_f32_e32 v87, v3, v74
	v_pk_fma_f32 v[42:43], v[2:3], v[110:111], v[42:43] op_sel:[1,0,0] op_sel_hi:[0,1,1]
	v_pk_fma_f32 v[44:45], v[2:3], v[112:113], v[44:45] op_sel:[1,0,0] op_sel_hi:[0,1,1]
	v_pk_fma_f32 v[82:83], v[68:69], v[68:69], v[0:1] op_sel_hi:[1,1,0]
	v_pk_add_f32 v[76:77], v[80:81], v[80:81] op_sel:[0,1] op_sel_hi:[1,0]
	v_mov_b32_e32 v97, v95
	v_mov_b32_e32 v0, v24
	v_mov_b32_e32 v38, v35
	v_mov_b32_e32 v74, v32
	v_mov_b32_e32 v2, v32
	v_mov_b32_e32 v94, v99
	v_mov_b32_e32 v73, v91
	v_mov_b32_e32 v85, v59
	v_mul_f32_e32 v89, v3, v106
	v_mov_b32_e32 v86, v42
	v_mov_b32_e32 v88, v44
	v_mov_b32_e32 v83, v107
	v_mov_b32_e32 v77, v107
	v_pk_fma_f32 v[74:75], v[2:3], v[74:75], v[96:97]
	v_pk_fma_f32 v[0:1], v[24:25], v[0:1], v[94:95]
	v_pk_add_f32 v[2:3], v[58:59], v[72:73]
	v_pk_fma_f32 v[38:39], v[38:39], v[70:71], v[84:85]
	v_pk_add_f32 v[86:87], v[42:43], v[86:87]
	v_pk_add_f32 v[88:89], v[44:45], v[88:89]
	v_pk_mul_f32 v[100:101], v[30:31], v[30:31]
	v_pk_add_f32 v[58:59], v[74:75], v[0:1]
	v_pk_mul_f32 v[0:1], v[74:75], v[0:1]
	v_pk_add_f32 v[72:73], v[2:3], v[76:77]
	v_pk_add_f32 v[2:3], v[38:39], v[82:83]
	v_pk_mul_f32 v[78:79], v[86:87], v[86:87]
	v_pk_mul_f32 v[80:81], v[88:89], v[88:89]
	v_pk_fma_f32 v[92:93], v[42:43], v[42:43], v[100:101]
	v_pk_fma_f32 v[98:99], v[44:45], v[44:45], v[100:101] op_sel:[0,0,1] op_sel_hi:[1,1,0]
	v_mov_b32_e32 v59, v1
	v_pk_add_f32 v[0:1], v[72:73], v[2:3]
	v_pk_mul_f32 v[2:3], v[72:73], v[2:3]
	v_mov_b32_e32 v93, v79
	v_mov_b32_e32 v99, v81
	v_mov_b32_e32 v1, v3
	v_pk_add_f32 v[70:71], v[92:93], v[98:99]
	v_pk_add_f32 v[0:1], v[0:1], v[58:59]
	v_mov_b32_e32 v41, v32
	v_pk_add_f32 v[0:1], v[0:1], v[70:71]
	v_mov_b32_e32 v45, v31
	v_add_f32_e32 v0, v0, v1
	ds_bpermute_b32 v1, v48, v0
	v_mov_b32_e32 v43, v30
	v_mov_b32_e32 v88, v87
	v_mov_b32_e32 v74, v73
	s_waitcnt lgkmcnt(0)
; #define GAS __attribute__((address_space(1)))
; __device__ __forceinline__ void final_phase(Frame& F) {
;     ...
;         float rs = 1.0f / sqrtf(wave_sum(s) * (1.0f / D) + EPS);
;         GAS f32x4* orow = (GAS f32x4*)(F.out + (size_t)t * D) + lane_; const GAS f32x4* gr = (const GAS f32x4*)g_fin + lane_;
; #pragma unroll
;         for (int j = 0; j < 8; ++j) { const f32x4 g = gr[64 * j]; orow[64 * j] = v[j] * rs * g; }
	v_add_f32_e32 v0, v0, v1
	ds_bpermute_b32 v1, v49, v0
	s_waitcnt lgkmcnt(0)
	v_add_f32_e32 v0, v0, v1
	ds_bpermute_b32 v1, v50, v0
	s_waitcnt lgkmcnt(0)
	v_add_f32_e32 v0, v0, v1
	ds_bpermute_b32 v1, v51, v0
	s_waitcnt lgkmcnt(0)
	v_add_f32_e32 v0, v0, v1
	ds_bpermute_b32 v1, v52, v0
	s_waitcnt lgkmcnt(0)
	v_add_f32_e32 v0, v0, v1
	ds_bpermute_b32 v1, v53, v0
	s_waitcnt lgkmcnt(0)
	v_add_f32_e32 v0, v0, v1
	v_fmamk_f32 v0, v0, 0x3a000000, v56
	v_mul_f32_e32 v1, 0x4f800000, v0
	v_cmp_gt_f32_e32 vcc, s5, v0
	s_nop 1
	v_cndmask_b32_e32 v0, v0, v1, vcc
	v_sqrt_f32_e32 v1, v0
	s_nop 0
	v_add_u32_e32 v2, -1, v1
	v_add_u32_e32 v3, 1, v1
	v_fma_f32 v25, -v2, v1, v0
	v_fma_f32 v38, -v3, v1, v0
	v_cmp_ge_f32_e64 s[0:1], 0, v25
	s_nop 1
	v_cndmask_b32_e64 v1, v1, v2, s[0:1]
	v_cmp_lt_f32_e64 s[0:1], 0, v38
	s_nop 1
	v_cndmask_b32_e64 v1, v1, v3, s[0:1]
	v_mul_f32_e32 v2, 0x37800000, v1
	v_cndmask_b32_e32 v1, v1, v2, vcc
	v_cmp_class_f32_e32 vcc, v0, v57
	s_nop 1
	v_cndmask_b32_e32 v0, v1, v0, vcc
	v_div_scale_f32 v1, s[0:1], v0, v0, 1.0
	v_rcp_f32_e32 v3, v1
	v_div_scale_f32 v2, vcc, 1.0, v0, 1.0
	v_fma_f32 v25, -v1, v3, 1.0
	v_fmac_f32_e32 v3, v25, v3
	v_mul_f32_e32 v25, v2, v3
	v_fma_f32 v38, -v1, v25, v2
	v_fmac_f32_e32 v25, v38, v3
	v_fma_f32 v1, -v1, v25, v2
	v_div_fmas_f32 v1, v1, v3, v25
	v_div_fixup_f32 v38, v1, v0, 1.0
	v_pk_mul_f32 v[0:1], v[36:37], v[38:39] op_sel_hi:[1,0]
	v_pk_mul_f32 v[2:3], v[46:47], v[38:39] op_sel_hi:[1,0]
	v_pk_mul_f32 v[0:1], v[4:5], v[0:1]
	v_pk_mul_f32 v[2:3], v[6:7], v[2:3]
	global_store_dwordx4 v[18:19], v[0:3], off offset:-4096
	s_nop 0
	v_mov_b32_e32 v4, v61
	v_mov_b32_e32 v5, v29
	v_mov_b32_e32 v61, v28
	v_pk_mul_f32 v[4:5], v[4:5], v[38:39] op_sel_hi:[1,0]
	v_pk_mul_f32 v[6:7], v[60:61], v[38:39] op_sel_hi:[1,0]
	s_nop 0
	v_pk_mul_f32 v[2:3], v[162:163], v[4:5]
	v_pk_mul_f32 v[0:1], v[160:161], v[6:7]
	global_store_dwordx4 v[18:19], v[0:3], off offset:-3072
	s_nop 0
	v_mov_b32_e32 v4, v63
	v_mov_b32_e32 v5, v27
	v_mov_b32_e32 v63, v26
	v_pk_mul_f32 v[4:5], v[4:5], v[38:39] op_sel_hi:[1,0]
	v_pk_mul_f32 v[6:7], v[62:63], v[38:39] op_sel_hi:[1,0]
	s_nop 0
	v_pk_mul_f32 v[2:3], v[166:167], v[4:5]
	v_pk_mul_f32 v[0:1], v[164:165], v[6:7]
	global_store_dwordx4 v[18:19], v[0:3], off offset:-2048
	s_nop 0
	v_mov_b32_e32 v4, v65
	v_mov_b32_e32 v5, v67
	v_mov_b32_e32 v65, v66
	v_pk_mul_f32 v[4:5], v[4:5], v[38:39] op_sel_hi:[1,0]
	v_pk_mul_f32 v[6:7], v[64:65], v[38:39] op_sel_hi:[1,0]
	s_nop 0
	v_pk_mul_f32 v[2:3], v[170:171], v[4:5]
	v_pk_mul_f32 v[0:1], v[168:169], v[6:7]
	global_store_dwordx4 v[18:19], v[0:3], off offset:-1024
	s_nop 0
	v_pk_mul_f32 v[4:5], v[68:69], v[38:39] op_sel_hi:[1,0]
	v_pk_mul_f32 v[6:7], v[34:35], v[38:39] op_sel_hi:[1,0]
	s_nop 0
	v_pk_mul_f32 v[2:3], v[174:175], v[4:5]
	v_pk_mul_f32 v[0:1], v[172:173], v[6:7]
	global_store_dwordx4 v[18:19], v[0:3], off
	s_nop 0
	v_mov_b32_e32 v5, v24
	v_mov_b32_e32 v4, v33
	v_pk_mul_f32 v[4:5], v[4:5], v[38:39] op_sel_hi:[1,0]
	v_pk_mul_f32 v[6:7], v[40:41], v[38:39] op_sel_hi:[1,0]
	s_nop 0
	v_pk_mul_f32 v[2:3], v[178:179], v[4:5]
	v_pk_mul_f32 v[0:1], v[176:177], v[6:7]
	global_store_dwordx4 v[18:19], v[0:3], off offset:1024
	s_nop 0
	v_pk_mul_f32 v[4:5], v[44:45], v[38:39] op_sel_hi:[1,0]
	v_pk_mul_f32 v[6:7], v[42:43], v[38:39] op_sel_hi:[1,0]
	s_nop 0
	v_pk_mul_f32 v[2:3], v[182:183], v[4:5]
	v_pk_mul_f32 v[0:1], v[180:181], v[6:7]
	global_store_dwordx4 v[18:19], v[0:3], off offset:2048
	s_nop 0
	v_pk_mul_f32 v[4:5], v[88:89], v[38:39] op_sel_hi:[1,0]
	v_pk_mul_f32 v[6:7], v[74:75], v[38:39] op_sel_hi:[1,0]
	s_nop 0
	v_pk_mul_f32 v[2:3], v[4:5], v[186:187]
	v_pk_mul_f32 v[0:1], v[6:7], v[184:185]
	global_store_dwordx4 v[18:19], v[0:3], off offset:3072
	v_lshl_add_u64 v[18:19], v[18:19], 0, s[12:13]
	s_cbranch_scc1 .LBB0_2295
